# in-proj sigmoid epilogue: per-column bias quads loaded once per tile (groups 2..15 reuse parked registers, no vmcnt(0) drain per group)
# baseline (speedup 1.0000x reference)
; __device__ __forceinline__ float sigmoidf_(float x) { return __builtin_amdgcn_rcpf(1.f + __expf(-x)); }
; __device__ __forceinline__ u32x4 pack8(f32x4 v0, f32x4 v1) { u32x4 w; w.x = cvt_pk_bf16(v0[0], v0[1]); w.y = cvt_pk_bf16(v0[2], v0[3]); w.z = cvt_pk_bf16(v1[0], v1[1]); w.w = cvt_pk_bf16(v1[2], v1[3]); return w; }
;     __device__ __forceinline__ void operator()(const f32x4 (&acc)[2][2][4][2], const pg8::Unit& u, int wr, int wc, int fr, int fq) const {
;     ...
;             const int row = u.pm * 256 + trow, col = u.pn * 256 + tcol;
;             if (col < C_KA) { v0 = v0 * QS_A; v1 = v1 * QS_A; }
;             else if (col >= C_GA && col < INC) { const f32x4 b0 = *(const f32x4*)(bg + col - C_GA), b1 = *(const f32x4*)(bg + col - C_GA + 4);
; #pragma unroll
;                 for (int i = 0; i < 4; ++i) { v0[i] = sigmoidf_(v0[i] + b0[i]); v1[i] = sigmoidf_(v1[i] + b1[i]); } }
;             *(u32x4*)(O + (size_t)row * INCP + col) = pg8::pack8(v0, v1);
.LBB0_166:
	s_lshl_b32 s4, s6, 8
	s_or_b32 s23, s51, s4
	v_or_b32_e32 v4, s23, v222
	v_cmp_lt_i32_e64 s[4:5], s58, v4
	s_and_saveexec_b64 s[6:7], s[4:5]
	s_xor_b64 s[6:7], exec, s[6:7]
	s_cbranch_execz .LBB0_169
	s_add_i32 s26, s23, 0xfffff760
	s_cmpk_gt_u32 s26, 0x7ff
	v_mov_b32_e32 v135, v129
	v_mov_b32_e32 v134, v128
	v_mov_b32_e32 v137, v127
	v_mov_b32_e32 v136, v126
	v_mov_b32_e32 v139, v133
	v_mov_b32_e32 v138, v132
	v_mov_b32_e32 v141, v131
	v_mov_b32_e32 v140, v130
	s_cbranch_scc1 .LBB0_169
	v_readlane_b32 s60, v253, 5
	v_mov_b32_e32 v5, v3
	v_readlane_b32 s64, v253, 9
	v_readlane_b32 s65, v253, 10
	v_readlane_b32 s61, v253, 6
	v_readlane_b32 s62, v253, 7
	v_lshl_add_u64 v[134:135], v[4:5], 2, s[64:65]
	v_lshl_add_u64 v[138:139], v[134:135], 0, s[16:17]
	v_add_co_u32_e32 v134, vcc, 0xffffe000, v134
	v_readlane_b32 s63, v253, 8
	s_nop 0
	v_addc_co_u32_e32 v135, vcc, -1, v135, vcc
	global_load_dwordx4 v[134:137], v[134:135], off offset:-640
	s_nop 0
	global_load_dwordx4 v[138:141], v[138:139], off offset:16
	v_readlane_b32 s66, v253, 11
	v_readlane_b32 s67, v253, 12
	v_readlane_b32 s68, v253, 13
	v_readlane_b32 s69, v253, 14
	v_readlane_b32 s70, v253, 15
	v_readlane_b32 s71, v253, 16
	v_readlane_b32 s72, v253, 17
	v_readlane_b32 s73, v253, 18
	v_readlane_b32 s74, v253, 19
	v_readlane_b32 s75, v253, 20
	s_waitcnt vmcnt(0)
	v_mov_b64_e32 v[150:151], v[134:135]
	v_mov_b64_e32 v[152:153], v[136:137]
	v_mov_b64_e32 v[154:155], v[138:139]
	v_mov_b64_e32 v[156:157], v[140:141]
	v_add_f32_e32 v2, v130, v134
	v_add_f32_e32 v5, v126, v138
	v_add_f32_e32 v134, v131, v135
	v_add_f32_e32 v135, v127, v139
	v_add_f32_e32 v136, v132, v136
	v_add_f32_e32 v138, v128, v140
	v_add_f32_e32 v137, v133, v137
	v_add_f32_e32 v139, v129, v141
	v_mul_f32_e32 v2, 0xbfb8aa3b, v2
	v_mul_f32_e32 v5, 0xbfb8aa3b, v5
	v_mul_f32_e32 v134, 0xbfb8aa3b, v134
	v_mul_f32_e32 v135, 0xbfb8aa3b, v135
	v_mul_f32_e32 v136, 0xbfb8aa3b, v136
	v_mul_f32_e32 v138, 0xbfb8aa3b, v138
	v_mul_f32_e32 v137, 0xbfb8aa3b, v137
	v_mul_f32_e32 v139, 0xbfb8aa3b, v139
	v_exp_f32_e32 v2, v2
	v_exp_f32_e32 v5, v5
	v_exp_f32_e32 v134, v134
	v_exp_f32_e32 v135, v135
	v_exp_f32_e32 v136, v136
	v_exp_f32_e32 v138, v138
	v_exp_f32_e32 v137, v137
	v_exp_f32_e32 v139, v139
	v_add_f32_e32 v2, 1.0, v2
	v_add_f32_e32 v5, 1.0, v5
	v_add_f32_e32 v134, 1.0, v134
	v_add_f32_e32 v135, 1.0, v135
	v_add_f32_e32 v142, 1.0, v136
	v_add_f32_e32 v143, 1.0, v138
	v_add_f32_e32 v144, 1.0, v137
	v_add_f32_e32 v145, 1.0, v139
	v_rcp_f32_e32 v140, v2
	v_rcp_f32_e32 v136, v5
	v_rcp_f32_e32 v141, v134
	v_rcp_f32_e32 v137, v135
	v_rcp_f32_e32 v138, v142
	v_rcp_f32_e32 v134, v143
	v_rcp_f32_e32 v139, v144
	v_rcp_f32_e32 v135, v145
.LBB0_169:
	s_andn2_saveexec_b64 s[6:7], s[6:7]
	v_pk_mul_f32 v[138:139], v[132:133], s[18:19] op_sel_hi:[1,0]
	v_pk_mul_f32 v[140:141], v[130:131], s[18:19] op_sel_hi:[1,0]
	v_pk_mul_f32 v[134:135], v[128:129], s[18:19] op_sel_hi:[1,0]
	v_pk_mul_f32 v[136:137], v[126:127], s[18:19] op_sel_hi:[1,0]
	s_or_b64 exec, exec, s[6:7]
	v_readlane_b32 s6, v253, 54
	s_lshl_b32 s28, s33, 8
	v_readlane_b32 s7, v253, 55
	v_add_u32_e32 v2, s28, v221
	v_ashrrev_i32_e32 v5, 31, v4
	v_mov_b64_e32 v[126:127], s[6:7]
	v_mad_i64_i32 v[126:127], s[6:7], v2, s59, v[126:127]
	v_or_b32_e32 v2, 0x80, v4
	v_cvt_pk_bf16_f32 v128, v140, v141
	v_cvt_pk_bf16_f32 v129, v138, v139
	v_cvt_pk_bf16_f32 v130, v136, v137
	v_cvt_pk_bf16_f32 v131, v134, v135
	v_lshl_add_u64 v[126:127], v[4:5], 1, v[126:127]
	v_cmp_lt_i32_e64 s[6:7], s58, v2
	global_store_dwordx4 v[126:127], v[128:131], off
	s_and_saveexec_b64 s[26:27], s[6:7]
	s_xor_b64 s[26:27], exec, s[26:27]
	s_cbranch_execz .LBB0_174
	s_add_i32 s29, s23, 0xfffff7e0
	s_cmpk_gt_u32 s29, 0x7ff
	v_mov_b32_e32 v129, v121
	v_mov_b32_e32 v128, v120
	v_mov_b32_e32 v131, v119
	v_mov_b32_e32 v130, v118
	v_mov_b32_e32 v133, v125
	v_mov_b32_e32 v132, v124
	v_mov_b32_e32 v135, v123
	v_mov_b32_e32 v134, v122
	s_cbranch_scc1 .LBB0_174
	v_readlane_b32 s60, v253, 5
	v_mov_b32_e32 v2, v4
	v_readlane_b32 s64, v253, 9
	v_readlane_b32 s65, v253, 10
	v_readlane_b32 s61, v253, 6
	v_readlane_b32 s62, v253, 7
	v_lshl_add_u64 v[128:129], v[2:3], 2, s[64:65]
	v_lshl_add_u64 v[132:133], v[128:129], 0, s[20:21]
	v_add_co_u32_e32 v128, vcc, 0xffffe000, v128
	v_readlane_b32 s63, v253, 8
	s_nop 0
	v_addc_co_u32_e32 v129, vcc, -1, v129, vcc
	global_load_dwordx4 v[128:131], v[128:129], off offset:-128
	s_nop 0
	global_load_dwordx4 v[132:135], v[132:133], off offset:16
	v_readlane_b32 s66, v253, 11
	v_readlane_b32 s67, v253, 12
	v_readlane_b32 s68, v253, 13
	v_readlane_b32 s69, v253, 14
	v_readlane_b32 s70, v253, 15
	v_readlane_b32 s71, v253, 16
	v_readlane_b32 s72, v253, 17
	v_readlane_b32 s73, v253, 18
	v_readlane_b32 s74, v253, 19
	v_readlane_b32 s75, v253, 20
	s_waitcnt vmcnt(0)
	v_mov_b64_e32 v[158:159], v[128:129]
	v_mov_b64_e32 v[160:161], v[130:131]
	v_mov_b64_e32 v[162:163], v[132:133]
	v_mov_b64_e32 v[164:165], v[134:135]
	v_add_f32_e32 v2, v122, v128
	v_add_f32_e32 v128, v118, v132
	v_add_f32_e32 v129, v123, v129
	v_add_f32_e32 v132, v119, v133
	v_add_f32_e32 v130, v124, v130
	v_add_f32_e32 v133, v120, v134
	v_add_f32_e32 v131, v125, v131
	v_add_f32_e32 v134, v121, v135
	v_mul_f32_e32 v2, 0xbfb8aa3b, v2
	v_mul_f32_e32 v128, 0xbfb8aa3b, v128
	v_mul_f32_e32 v129, 0xbfb8aa3b, v129
	v_mul_f32_e32 v132, 0xbfb8aa3b, v132
	v_mul_f32_e32 v130, 0xbfb8aa3b, v130
	v_mul_f32_e32 v133, 0xbfb8aa3b, v133
	v_mul_f32_e32 v131, 0xbfb8aa3b, v131
	v_mul_f32_e32 v134, 0xbfb8aa3b, v134
	v_exp_f32_e32 v2, v2
	v_exp_f32_e32 v128, v128
	v_exp_f32_e32 v129, v129
	v_exp_f32_e32 v132, v132
	v_exp_f32_e32 v130, v130
	v_exp_f32_e32 v133, v133
	v_exp_f32_e32 v131, v131
	v_exp_f32_e32 v134, v134
	v_add_f32_e32 v2, 1.0, v2
	v_add_f32_e32 v128, 1.0, v128
	v_add_f32_e32 v129, 1.0, v129
	v_add_f32_e32 v132, 1.0, v132
	v_add_f32_e32 v136, 1.0, v130
	v_add_f32_e32 v133, 1.0, v133
	v_add_f32_e32 v137, 1.0, v131
	v_add_f32_e32 v138, 1.0, v134
	v_rcp_f32_e32 v134, v2
	v_rcp_f32_e32 v130, v128
	v_rcp_f32_e32 v135, v129
	v_rcp_f32_e32 v131, v132
	v_rcp_f32_e32 v132, v136
	v_rcp_f32_e32 v128, v133
	v_rcp_f32_e32 v133, v137
	v_rcp_f32_e32 v129, v138
; __device__ __forceinline__ float sigmoidf_(float x) { return __builtin_amdgcn_rcpf(1.f + __expf(-x)); }
; __device__ __forceinline__ u32x4 pack8(f32x4 v0, f32x4 v1) { u32x4 w; w.x = cvt_pk_bf16(v0[0], v0[1]); w.y = cvt_pk_bf16(v0[2], v0[3]); w.z = cvt_pk_bf16(v1[0], v1[1]); w.w = cvt_pk_bf16(v1[2], v1[3]); return w; }
;     __device__ __forceinline__ void operator()(const f32x4 (&acc)[2][2][4][2], const pg8::Unit& u, int wr, int wc, int fr, int fq) const {
;     ...
;             const int row = u.pm * 256 + trow, col = u.pn * 256 + tcol;
;             if (col < C_KA) { v0 = v0 * QS_A; v1 = v1 * QS_A; }
;             else if (col >= C_GA && col < INC) { const f32x4 b0 = *(const f32x4*)(bg + col - C_GA), b1 = *(const f32x4*)(bg + col - C_GA + 4);
; #pragma unroll
;                 for (int i = 0; i < 4; ++i) { v0[i] = sigmoidf_(v0[i] + b0[i]); v1[i] = sigmoidf_(v1[i] + b1[i]); } }
;             *(u32x4*)(O + (size_t)row * INCP + col) = pg8::pack8(v0, v1);
.LBB0_174:
	s_andn2_saveexec_b64 s[26:27], s[26:27]
	v_pk_mul_f32 v[132:133], v[124:125], s[18:19] op_sel_hi:[1,0]
	v_pk_mul_f32 v[134:135], v[122:123], s[18:19] op_sel_hi:[1,0]
	v_pk_mul_f32 v[128:129], v[120:121], s[18:19] op_sel_hi:[1,0]
	v_pk_mul_f32 v[130:131], v[118:119], s[18:19] op_sel_hi:[1,0]
	s_or_b64 exec, exec, s[26:27]
	v_cvt_pk_bf16_f32 v118, v134, v135
	v_cvt_pk_bf16_f32 v119, v132, v133
	v_cvt_pk_bf16_f32 v120, v130, v131
	v_cvt_pk_bf16_f32 v121, v128, v129
	global_store_dwordx4 v[126:127], v[118:121], off offset:256
	s_and_saveexec_b64 s[26:27], s[4:5]
	s_xor_b64 s[26:27], exec, s[26:27]
	s_cbranch_execz .LBB0_179
	s_add_i32 s29, s23, 0xfffff760
	s_cmpk_gt_u32 s29, 0x7ff
	v_mov_b32_e32 v119, v113
	v_mov_b32_e32 v118, v112
	v_mov_b32_e32 v121, v111
	v_mov_b32_e32 v120, v110
	v_mov_b32_e32 v123, v117
	v_mov_b32_e32 v122, v116
	v_mov_b32_e32 v125, v115
	v_mov_b32_e32 v124, v114
	s_cbranch_scc1 .LBB0_179
	v_readlane_b32 s60, v253, 5
	v_mov_b32_e32 v2, v4
	v_readlane_b32 s64, v253, 9
	v_readlane_b32 s65, v253, 10
	v_readlane_b32 s61, v253, 6
	v_readlane_b32 s62, v253, 7
	v_lshl_add_u64 v[118:119], v[2:3], 2, s[64:65]
	v_lshl_add_u64 v[122:123], v[118:119], 0, s[16:17]
	v_add_co_u32_e32 v118, vcc, 0xffffe000, v118
	v_readlane_b32 s63, v253, 8
	s_nop 0
	v_addc_co_u32_e32 v119, vcc, -1, v119, vcc
	v_mov_b64_e32 v[118:119], v[150:151]
	v_mov_b64_e32 v[120:121], v[152:153]
	s_nop 0
	v_mov_b64_e32 v[122:123], v[154:155]
	v_mov_b64_e32 v[124:125], v[156:157]
	v_readlane_b32 s66, v253, 11
	v_readlane_b32 s67, v253, 12
	v_readlane_b32 s68, v253, 13
	v_readlane_b32 s69, v253, 14
	v_readlane_b32 s70, v253, 15
	v_readlane_b32 s71, v253, 16
	v_readlane_b32 s72, v253, 17
	v_readlane_b32 s73, v253, 18
	v_readlane_b32 s74, v253, 19
	v_readlane_b32 s75, v253, 20
	v_add_f32_e32 v2, v114, v118
	v_add_f32_e32 v118, v110, v122
	v_add_f32_e32 v119, v115, v119
	v_add_f32_e32 v122, v111, v123
	v_add_f32_e32 v120, v116, v120
	v_add_f32_e32 v123, v112, v124
	v_add_f32_e32 v121, v117, v121
	v_add_f32_e32 v124, v113, v125
	v_mul_f32_e32 v2, 0xbfb8aa3b, v2
	v_mul_f32_e32 v118, 0xbfb8aa3b, v118
	v_mul_f32_e32 v119, 0xbfb8aa3b, v119
	v_mul_f32_e32 v122, 0xbfb8aa3b, v122
	v_mul_f32_e32 v120, 0xbfb8aa3b, v120
	v_mul_f32_e32 v123, 0xbfb8aa3b, v123
	v_mul_f32_e32 v121, 0xbfb8aa3b, v121
	v_mul_f32_e32 v124, 0xbfb8aa3b, v124
	v_exp_f32_e32 v2, v2
	v_exp_f32_e32 v118, v118
	v_exp_f32_e32 v119, v119
	v_exp_f32_e32 v122, v122
	v_exp_f32_e32 v120, v120
	v_exp_f32_e32 v123, v123
	v_exp_f32_e32 v121, v121
	v_exp_f32_e32 v124, v124
	v_add_f32_e32 v2, 1.0, v2
	v_add_f32_e32 v118, 1.0, v118
	v_add_f32_e32 v119, 1.0, v119
	v_add_f32_e32 v122, 1.0, v122
	v_add_f32_e32 v126, 1.0, v120
	v_add_f32_e32 v123, 1.0, v123
	v_add_f32_e32 v127, 1.0, v121
	v_add_f32_e32 v128, 1.0, v124
	v_rcp_f32_e32 v124, v2
	v_rcp_f32_e32 v120, v118
	v_rcp_f32_e32 v125, v119
	v_rcp_f32_e32 v121, v122
	v_rcp_f32_e32 v122, v126
	v_rcp_f32_e32 v118, v123
	v_rcp_f32_e32 v123, v127
	v_rcp_f32_e32 v119, v128
.LBB0_179:
	s_andn2_saveexec_b64 s[26:27], s[26:27]
	v_pk_mul_f32 v[122:123], v[116:117], s[18:19] op_sel_hi:[1,0]
	v_pk_mul_f32 v[124:125], v[114:115], s[18:19] op_sel_hi:[1,0]
	v_pk_mul_f32 v[118:119], v[112:113], s[18:19] op_sel_hi:[1,0]
	v_pk_mul_f32 v[120:121], v[110:111], s[18:19] op_sel_hi:[1,0]
	s_or_b64 exec, exec, s[26:27]
	v_readlane_b32 s26, v253, 54
	v_readlane_b32 s27, v253, 55
	v_add_u32_e32 v2, s28, v224
	v_cvt_pk_bf16_f32 v112, v124, v125
	v_mov_b64_e32 v[110:111], s[26:27]
	v_mad_i64_i32 v[110:111], s[26:27], v2, s59, v[110:111]
	v_cvt_pk_bf16_f32 v113, v122, v123
	v_cvt_pk_bf16_f32 v114, v120, v121
	v_cvt_pk_bf16_f32 v115, v118, v119
	v_lshl_add_u64 v[110:111], v[4:5], 1, v[110:111]
	global_store_dwordx4 v[110:111], v[112:115], off
	s_and_saveexec_b64 s[26:27], s[6:7]
	s_xor_b64 s[26:27], exec, s[26:27]
	s_cbranch_execz .LBB0_184
	s_add_i32 s29, s23, 0xfffff7e0
	s_cmpk_gt_u32 s29, 0x7ff
	v_mov_b32_e32 v113, v105
	v_mov_b32_e32 v112, v104
	v_mov_b32_e32 v115, v103
	v_mov_b32_e32 v114, v102
	v_mov_b32_e32 v117, v109
	v_mov_b32_e32 v116, v108
	v_mov_b32_e32 v119, v107
	v_mov_b32_e32 v118, v106
	s_cbranch_scc1 .LBB0_184
	v_readlane_b32 s60, v253, 5
	v_mov_b32_e32 v2, v4
	v_readlane_b32 s64, v253, 9
	v_readlane_b32 s65, v253, 10
	v_readlane_b32 s61, v253, 6
	v_readlane_b32 s62, v253, 7
	v_lshl_add_u64 v[112:113], v[2:3], 2, s[64:65]
	v_lshl_add_u64 v[116:117], v[112:113], 0, s[20:21]
	v_add_co_u32_e32 v112, vcc, 0xffffe000, v112
	v_readlane_b32 s63, v253, 8
	s_nop 0
	v_addc_co_u32_e32 v113, vcc, -1, v113, vcc
	v_mov_b64_e32 v[112:113], v[158:159]
	v_mov_b64_e32 v[114:115], v[160:161]
	s_nop 0
	v_mov_b64_e32 v[116:117], v[162:163]
	v_mov_b64_e32 v[118:119], v[164:165]
	v_readlane_b32 s66, v253, 11
	v_readlane_b32 s67, v253, 12
	v_readlane_b32 s68, v253, 13
	v_readlane_b32 s69, v253, 14
	v_readlane_b32 s70, v253, 15
	v_readlane_b32 s71, v253, 16
	v_readlane_b32 s72, v253, 17
	v_readlane_b32 s73, v253, 18
	v_readlane_b32 s74, v253, 19
	v_readlane_b32 s75, v253, 20
	v_add_f32_e32 v2, v106, v112
	v_add_f32_e32 v112, v102, v116
	v_add_f32_e32 v113, v107, v113
	v_add_f32_e32 v116, v103, v117
	v_add_f32_e32 v114, v108, v114
	v_add_f32_e32 v117, v104, v118
	v_add_f32_e32 v115, v109, v115
	v_add_f32_e32 v118, v105, v119
	v_mul_f32_e32 v2, 0xbfb8aa3b, v2
	v_mul_f32_e32 v112, 0xbfb8aa3b, v112
	v_mul_f32_e32 v113, 0xbfb8aa3b, v113
	v_mul_f32_e32 v116, 0xbfb8aa3b, v116
	v_mul_f32_e32 v114, 0xbfb8aa3b, v114
	v_mul_f32_e32 v117, 0xbfb8aa3b, v117
	v_mul_f32_e32 v115, 0xbfb8aa3b, v115
	v_mul_f32_e32 v118, 0xbfb8aa3b, v118
	v_exp_f32_e32 v2, v2
	v_exp_f32_e32 v112, v112
	v_exp_f32_e32 v113, v113
	v_exp_f32_e32 v116, v116
	v_exp_f32_e32 v114, v114
	v_exp_f32_e32 v117, v117
	v_exp_f32_e32 v115, v115
	v_exp_f32_e32 v118, v118
	v_add_f32_e32 v2, 1.0, v2
	v_add_f32_e32 v112, 1.0, v112
	v_add_f32_e32 v113, 1.0, v113
	v_add_f32_e32 v116, 1.0, v116
	v_add_f32_e32 v120, 1.0, v114
	v_add_f32_e32 v117, 1.0, v117
	v_add_f32_e32 v121, 1.0, v115
	v_add_f32_e32 v122, 1.0, v118
	v_rcp_f32_e32 v118, v2
	v_rcp_f32_e32 v114, v112
	v_rcp_f32_e32 v119, v113
	v_rcp_f32_e32 v115, v116
	v_rcp_f32_e32 v116, v120
	v_rcp_f32_e32 v112, v117
	v_rcp_f32_e32 v117, v121
	v_rcp_f32_e32 v113, v122
; __device__ __forceinline__ float sigmoidf_(float x) { return __builtin_amdgcn_rcpf(1.f + __expf(-x)); }
; __device__ __forceinline__ u32x4 pack8(f32x4 v0, f32x4 v1) { u32x4 w; w.x = cvt_pk_bf16(v0[0], v0[1]); w.y = cvt_pk_bf16(v0[2], v0[3]); w.z = cvt_pk_bf16(v1[0], v1[1]); w.w = cvt_pk_bf16(v1[2], v1[3]); return w; }
;     __device__ __forceinline__ void operator()(const f32x4 (&acc)[2][2][4][2], const pg8::Unit& u, int wr, int wc, int fr, int fq) const {
;     ...
;             const int row = u.pm * 256 + trow, col = u.pn * 256 + tcol;
;             if (col < C_KA) { v0 = v0 * QS_A; v1 = v1 * QS_A; }
;             else if (col >= C_GA && col < INC) { const f32x4 b0 = *(const f32x4*)(bg + col - C_GA), b1 = *(const f32x4*)(bg + col - C_GA + 4);
; #pragma unroll
;                 for (int i = 0; i < 4; ++i) { v0[i] = sigmoidf_(v0[i] + b0[i]); v1[i] = sigmoidf_(v1[i] + b1[i]); } }
;             *(u32x4*)(O + (size_t)row * INCP + col) = pg8::pack8(v0, v1);
.LBB0_184:
	s_andn2_saveexec_b64 s[26:27], s[26:27]
	v_pk_mul_f32 v[116:117], v[108:109], s[18:19] op_sel_hi:[1,0]
	v_pk_mul_f32 v[118:119], v[106:107], s[18:19] op_sel_hi:[1,0]
	v_pk_mul_f32 v[112:113], v[104:105], s[18:19] op_sel_hi:[1,0]
	v_pk_mul_f32 v[114:115], v[102:103], s[18:19] op_sel_hi:[1,0]
	s_or_b64 exec, exec, s[26:27]
	v_cvt_pk_bf16_f32 v102, v118, v119
	v_cvt_pk_bf16_f32 v103, v116, v117
	v_cvt_pk_bf16_f32 v104, v114, v115
	v_cvt_pk_bf16_f32 v105, v112, v113
	global_store_dwordx4 v[110:111], v[102:105], off offset:256
	s_and_saveexec_b64 s[26:27], s[4:5]
	s_xor_b64 s[26:27], exec, s[26:27]
	s_cbranch_execz .LBB0_189
	s_add_i32 s29, s23, 0xfffff760
	s_cmpk_gt_u32 s29, 0x7ff
	v_mov_b32_e32 v103, v97
	v_mov_b32_e32 v102, v96
	v_mov_b32_e32 v105, v95
	v_mov_b32_e32 v104, v94
	v_mov_b32_e32 v107, v101
	v_mov_b32_e32 v106, v100
	v_mov_b32_e32 v109, v99
	v_mov_b32_e32 v108, v98
	s_cbranch_scc1 .LBB0_189
	v_readlane_b32 s60, v253, 5
	v_mov_b32_e32 v2, v4
	v_readlane_b32 s64, v253, 9
	v_readlane_b32 s65, v253, 10
	v_readlane_b32 s61, v253, 6
	v_readlane_b32 s62, v253, 7
	v_lshl_add_u64 v[102:103], v[2:3], 2, s[64:65]
	v_lshl_add_u64 v[106:107], v[102:103], 0, s[16:17]
	v_add_co_u32_e32 v102, vcc, 0xffffe000, v102
	v_readlane_b32 s63, v253, 8
	s_nop 0
	v_addc_co_u32_e32 v103, vcc, -1, v103, vcc
	v_mov_b64_e32 v[102:103], v[150:151]
	v_mov_b64_e32 v[104:105], v[152:153]
	s_nop 0
	v_mov_b64_e32 v[106:107], v[154:155]
	v_mov_b64_e32 v[108:109], v[156:157]
	v_readlane_b32 s66, v253, 11
	v_readlane_b32 s67, v253, 12
	v_readlane_b32 s68, v253, 13
	v_readlane_b32 s69, v253, 14
	v_readlane_b32 s70, v253, 15
	v_readlane_b32 s71, v253, 16
	v_readlane_b32 s72, v253, 17
	v_readlane_b32 s73, v253, 18
	v_readlane_b32 s74, v253, 19
	v_readlane_b32 s75, v253, 20
	v_add_f32_e32 v2, v98, v102
	v_add_f32_e32 v102, v94, v106
	v_add_f32_e32 v103, v99, v103
	v_add_f32_e32 v106, v95, v107
	v_add_f32_e32 v104, v100, v104
	v_add_f32_e32 v107, v96, v108
	v_add_f32_e32 v105, v101, v105
	v_add_f32_e32 v108, v97, v109
	v_mul_f32_e32 v2, 0xbfb8aa3b, v2
	v_mul_f32_e32 v102, 0xbfb8aa3b, v102
	v_mul_f32_e32 v103, 0xbfb8aa3b, v103
	v_mul_f32_e32 v106, 0xbfb8aa3b, v106
	v_mul_f32_e32 v104, 0xbfb8aa3b, v104
	v_mul_f32_e32 v107, 0xbfb8aa3b, v107
	v_mul_f32_e32 v105, 0xbfb8aa3b, v105
	v_mul_f32_e32 v108, 0xbfb8aa3b, v108
	v_exp_f32_e32 v2, v2
	v_exp_f32_e32 v102, v102
	v_exp_f32_e32 v103, v103
	v_exp_f32_e32 v106, v106
	v_exp_f32_e32 v104, v104
	v_exp_f32_e32 v107, v107
	v_exp_f32_e32 v105, v105
	v_exp_f32_e32 v108, v108
	v_add_f32_e32 v2, 1.0, v2
	v_add_f32_e32 v102, 1.0, v102
	v_add_f32_e32 v103, 1.0, v103
	v_add_f32_e32 v106, 1.0, v106
	v_add_f32_e32 v110, 1.0, v104
	v_add_f32_e32 v107, 1.0, v107
	v_add_f32_e32 v111, 1.0, v105
	v_add_f32_e32 v112, 1.0, v108
	v_rcp_f32_e32 v108, v2
	v_rcp_f32_e32 v104, v102
	v_rcp_f32_e32 v109, v103
	v_rcp_f32_e32 v105, v106
	v_rcp_f32_e32 v106, v110
	v_rcp_f32_e32 v102, v107
	v_rcp_f32_e32 v107, v111
	v_rcp_f32_e32 v103, v112
.LBB0_189:
	s_andn2_saveexec_b64 s[26:27], s[26:27]
	v_pk_mul_f32 v[106:107], v[100:101], s[18:19] op_sel_hi:[1,0]
	v_pk_mul_f32 v[108:109], v[98:99], s[18:19] op_sel_hi:[1,0]
	v_pk_mul_f32 v[102:103], v[96:97], s[18:19] op_sel_hi:[1,0]
	v_pk_mul_f32 v[104:105], v[94:95], s[18:19] op_sel_hi:[1,0]
	s_or_b64 exec, exec, s[26:27]
	v_readlane_b32 s26, v253, 54
	v_readlane_b32 s27, v253, 55
	v_add_u32_e32 v2, s28, v225
	v_cvt_pk_bf16_f32 v96, v108, v109
	v_mov_b64_e32 v[94:95], s[26:27]
	v_mad_i64_i32 v[94:95], s[26:27], v2, s59, v[94:95]
	v_cvt_pk_bf16_f32 v97, v106, v107
	v_cvt_pk_bf16_f32 v98, v104, v105
	v_cvt_pk_bf16_f32 v99, v102, v103
	v_lshl_add_u64 v[94:95], v[4:5], 1, v[94:95]
	global_store_dwordx4 v[94:95], v[96:99], off
	s_and_saveexec_b64 s[26:27], s[6:7]
	s_xor_b64 s[26:27], exec, s[26:27]
	s_cbranch_execz .LBB0_194
	s_add_i32 s29, s23, 0xfffff7e0
	s_cmpk_gt_u32 s29, 0x7ff
	v_mov_b32_e32 v97, v89
	v_mov_b32_e32 v96, v88
	v_mov_b32_e32 v99, v87
	v_mov_b32_e32 v98, v86
	v_mov_b32_e32 v101, v93
	v_mov_b32_e32 v100, v92
	v_mov_b32_e32 v103, v91
	v_mov_b32_e32 v102, v90
	s_cbranch_scc1 .LBB0_194
	v_readlane_b32 s60, v253, 5
	v_mov_b32_e32 v2, v4
	v_readlane_b32 s64, v253, 9
	v_readlane_b32 s65, v253, 10
	v_readlane_b32 s61, v253, 6
	v_readlane_b32 s62, v253, 7
	v_lshl_add_u64 v[96:97], v[2:3], 2, s[64:65]
	v_lshl_add_u64 v[100:101], v[96:97], 0, s[20:21]
	v_add_co_u32_e32 v96, vcc, 0xffffe000, v96
	v_readlane_b32 s63, v253, 8
	s_nop 0
	v_addc_co_u32_e32 v97, vcc, -1, v97, vcc
	v_mov_b64_e32 v[96:97], v[158:159]
	v_mov_b64_e32 v[98:99], v[160:161]
	s_nop 0
	v_mov_b64_e32 v[100:101], v[162:163]
	v_mov_b64_e32 v[102:103], v[164:165]
	v_readlane_b32 s66, v253, 11
	v_readlane_b32 s67, v253, 12
	v_readlane_b32 s68, v253, 13
	v_readlane_b32 s69, v253, 14
	v_readlane_b32 s70, v253, 15
	v_readlane_b32 s71, v253, 16
	v_readlane_b32 s72, v253, 17
	v_readlane_b32 s73, v253, 18
	v_readlane_b32 s74, v253, 19
	v_readlane_b32 s75, v253, 20
	v_add_f32_e32 v2, v90, v96
	v_add_f32_e32 v96, v86, v100
	v_add_f32_e32 v97, v91, v97
	v_add_f32_e32 v100, v87, v101
	v_add_f32_e32 v98, v92, v98
	v_add_f32_e32 v101, v88, v102
	v_add_f32_e32 v99, v93, v99
	v_add_f32_e32 v102, v89, v103
	v_mul_f32_e32 v2, 0xbfb8aa3b, v2
	v_mul_f32_e32 v96, 0xbfb8aa3b, v96
	v_mul_f32_e32 v97, 0xbfb8aa3b, v97
	v_mul_f32_e32 v100, 0xbfb8aa3b, v100
	v_mul_f32_e32 v98, 0xbfb8aa3b, v98
	v_mul_f32_e32 v101, 0xbfb8aa3b, v101
	v_mul_f32_e32 v99, 0xbfb8aa3b, v99
	v_mul_f32_e32 v102, 0xbfb8aa3b, v102
	v_exp_f32_e32 v2, v2
	v_exp_f32_e32 v96, v96
	v_exp_f32_e32 v97, v97
	v_exp_f32_e32 v100, v100
	v_exp_f32_e32 v98, v98
	v_exp_f32_e32 v101, v101
	v_exp_f32_e32 v99, v99
	v_exp_f32_e32 v102, v102
	v_add_f32_e32 v2, 1.0, v2
	v_add_f32_e32 v96, 1.0, v96
	v_add_f32_e32 v97, 1.0, v97
	v_add_f32_e32 v100, 1.0, v100
	v_add_f32_e32 v104, 1.0, v98
	v_add_f32_e32 v101, 1.0, v101
	v_add_f32_e32 v105, 1.0, v99
	v_add_f32_e32 v106, 1.0, v102
	v_rcp_f32_e32 v102, v2
	v_rcp_f32_e32 v98, v96
	v_rcp_f32_e32 v103, v97
	v_rcp_f32_e32 v99, v100
	v_rcp_f32_e32 v100, v104
	v_rcp_f32_e32 v96, v101
	v_rcp_f32_e32 v101, v105
	v_rcp_f32_e32 v97, v106
; __device__ __forceinline__ float sigmoidf_(float x) { return __builtin_amdgcn_rcpf(1.f + __expf(-x)); }
; __device__ __forceinline__ u32x4 pack8(f32x4 v0, f32x4 v1) { u32x4 w; w.x = cvt_pk_bf16(v0[0], v0[1]); w.y = cvt_pk_bf16(v0[2], v0[3]); w.z = cvt_pk_bf16(v1[0], v1[1]); w.w = cvt_pk_bf16(v1[2], v1[3]); return w; }
;     __device__ __forceinline__ void operator()(const f32x4 (&acc)[2][2][4][2], const pg8::Unit& u, int wr, int wc, int fr, int fq) const {
;     ...
;             const int row = u.pm * 256 + trow, col = u.pn * 256 + tcol;
;             if (col < C_KA) { v0 = v0 * QS_A; v1 = v1 * QS_A; }
;             else if (col >= C_GA && col < INC) { const f32x4 b0 = *(const f32x4*)(bg + col - C_GA), b1 = *(const f32x4*)(bg + col - C_GA + 4);
; #pragma unroll
;                 for (int i = 0; i < 4; ++i) { v0[i] = sigmoidf_(v0[i] + b0[i]); v1[i] = sigmoidf_(v1[i] + b1[i]); } }
;             *(u32x4*)(O + (size_t)row * INCP + col) = pg8::pack8(v0, v1);
.LBB0_194:
	s_andn2_saveexec_b64 s[26:27], s[26:27]
	v_pk_mul_f32 v[100:101], v[92:93], s[18:19] op_sel_hi:[1,0]
	v_pk_mul_f32 v[102:103], v[90:91], s[18:19] op_sel_hi:[1,0]
	v_pk_mul_f32 v[96:97], v[88:89], s[18:19] op_sel_hi:[1,0]
	v_pk_mul_f32 v[98:99], v[86:87], s[18:19] op_sel_hi:[1,0]
	s_or_b64 exec, exec, s[26:27]
	v_cvt_pk_bf16_f32 v86, v102, v103
	v_cvt_pk_bf16_f32 v87, v100, v101
	v_cvt_pk_bf16_f32 v88, v98, v99
	v_cvt_pk_bf16_f32 v89, v96, v97
	global_store_dwordx4 v[94:95], v[86:89], off offset:256
	s_and_saveexec_b64 s[26:27], s[4:5]
	s_xor_b64 s[26:27], exec, s[26:27]
	s_cbranch_execz .LBB0_199
	s_add_i32 s29, s23, 0xfffff760
	s_cmpk_gt_u32 s29, 0x7ff
	v_mov_b32_e32 v87, v81
	v_mov_b32_e32 v86, v80
	v_mov_b32_e32 v89, v79
	v_mov_b32_e32 v88, v78
	v_mov_b32_e32 v91, v85
	v_mov_b32_e32 v90, v84
	v_mov_b32_e32 v93, v83
	v_mov_b32_e32 v92, v82
	s_cbranch_scc1 .LBB0_199
	v_readlane_b32 s60, v253, 5
	v_mov_b32_e32 v2, v4
	v_readlane_b32 s64, v253, 9
	v_readlane_b32 s65, v253, 10
	v_readlane_b32 s61, v253, 6
	v_readlane_b32 s62, v253, 7
	v_lshl_add_u64 v[86:87], v[2:3], 2, s[64:65]
	v_lshl_add_u64 v[90:91], v[86:87], 0, s[16:17]
	v_add_co_u32_e32 v86, vcc, 0xffffe000, v86
	v_readlane_b32 s63, v253, 8
	s_nop 0
	v_addc_co_u32_e32 v87, vcc, -1, v87, vcc
	v_mov_b64_e32 v[86:87], v[150:151]
	v_mov_b64_e32 v[88:89], v[152:153]
	s_nop 0
	v_mov_b64_e32 v[90:91], v[154:155]
	v_mov_b64_e32 v[92:93], v[156:157]
	v_readlane_b32 s66, v253, 11
	v_readlane_b32 s67, v253, 12
	v_readlane_b32 s68, v253, 13
	v_readlane_b32 s69, v253, 14
	v_readlane_b32 s70, v253, 15
	v_readlane_b32 s71, v253, 16
	v_readlane_b32 s72, v253, 17
	v_readlane_b32 s73, v253, 18
	v_readlane_b32 s74, v253, 19
	v_readlane_b32 s75, v253, 20
	v_add_f32_e32 v2, v82, v86
	v_add_f32_e32 v86, v78, v90
	v_add_f32_e32 v87, v83, v87
	v_add_f32_e32 v90, v79, v91
	v_add_f32_e32 v88, v84, v88
	v_add_f32_e32 v91, v80, v92
	v_add_f32_e32 v89, v85, v89
	v_add_f32_e32 v92, v81, v93
	v_mul_f32_e32 v2, 0xbfb8aa3b, v2
	v_mul_f32_e32 v86, 0xbfb8aa3b, v86
	v_mul_f32_e32 v87, 0xbfb8aa3b, v87
	v_mul_f32_e32 v90, 0xbfb8aa3b, v90
	v_mul_f32_e32 v88, 0xbfb8aa3b, v88
	v_mul_f32_e32 v91, 0xbfb8aa3b, v91
	v_mul_f32_e32 v89, 0xbfb8aa3b, v89
	v_mul_f32_e32 v92, 0xbfb8aa3b, v92
	v_exp_f32_e32 v2, v2
	v_exp_f32_e32 v86, v86
	v_exp_f32_e32 v87, v87
	v_exp_f32_e32 v90, v90
	v_exp_f32_e32 v88, v88
	v_exp_f32_e32 v91, v91
	v_exp_f32_e32 v89, v89
	v_exp_f32_e32 v92, v92
	v_add_f32_e32 v2, 1.0, v2
	v_add_f32_e32 v86, 1.0, v86
	v_add_f32_e32 v87, 1.0, v87
	v_add_f32_e32 v90, 1.0, v90
	v_add_f32_e32 v94, 1.0, v88
	v_add_f32_e32 v91, 1.0, v91
	v_add_f32_e32 v95, 1.0, v89
	v_add_f32_e32 v96, 1.0, v92
	v_rcp_f32_e32 v92, v2
	v_rcp_f32_e32 v88, v86
	v_rcp_f32_e32 v93, v87
	v_rcp_f32_e32 v89, v90
	v_rcp_f32_e32 v90, v94
	v_rcp_f32_e32 v86, v91
	v_rcp_f32_e32 v91, v95
	v_rcp_f32_e32 v87, v96
.LBB0_199:
	s_andn2_saveexec_b64 s[26:27], s[26:27]
	v_pk_mul_f32 v[90:91], v[84:85], s[18:19] op_sel_hi:[1,0]
	v_pk_mul_f32 v[92:93], v[82:83], s[18:19] op_sel_hi:[1,0]
	v_pk_mul_f32 v[86:87], v[80:81], s[18:19] op_sel_hi:[1,0]
	v_pk_mul_f32 v[88:89], v[78:79], s[18:19] op_sel_hi:[1,0]
	s_or_b64 exec, exec, s[26:27]
	v_readlane_b32 s26, v253, 54
	v_readlane_b32 s27, v253, 55
	v_add_u32_e32 v2, s28, v226
	v_cvt_pk_bf16_f32 v80, v92, v93
	v_mov_b64_e32 v[78:79], s[26:27]
	v_mad_i64_i32 v[78:79], s[26:27], v2, s59, v[78:79]
	v_cvt_pk_bf16_f32 v81, v90, v91
	v_cvt_pk_bf16_f32 v82, v88, v89
	v_cvt_pk_bf16_f32 v83, v86, v87
	v_lshl_add_u64 v[78:79], v[4:5], 1, v[78:79]
	global_store_dwordx4 v[78:79], v[80:83], off
	s_and_saveexec_b64 s[26:27], s[6:7]
	s_xor_b64 s[26:27], exec, s[26:27]
	s_cbranch_execz .LBB0_204
	s_add_i32 s29, s23, 0xfffff7e0
	s_cmpk_gt_u32 s29, 0x7ff
	v_mov_b32_e32 v81, v73
	v_mov_b32_e32 v80, v72
	v_mov_b32_e32 v83, v71
	v_mov_b32_e32 v82, v70
	v_mov_b32_e32 v85, v77
	v_mov_b32_e32 v84, v76
	v_mov_b32_e32 v87, v75
	v_mov_b32_e32 v86, v74
	s_cbranch_scc1 .LBB0_204
	v_readlane_b32 s60, v253, 5
	v_mov_b32_e32 v2, v4
	v_readlane_b32 s64, v253, 9
	v_readlane_b32 s65, v253, 10
	v_readlane_b32 s61, v253, 6
	v_readlane_b32 s62, v253, 7
	v_lshl_add_u64 v[80:81], v[2:3], 2, s[64:65]
	v_lshl_add_u64 v[84:85], v[80:81], 0, s[20:21]
	v_add_co_u32_e32 v80, vcc, 0xffffe000, v80
	v_readlane_b32 s63, v253, 8
	s_nop 0
	v_addc_co_u32_e32 v81, vcc, -1, v81, vcc
	v_mov_b64_e32 v[80:81], v[158:159]
	v_mov_b64_e32 v[82:83], v[160:161]
	s_nop 0
	v_mov_b64_e32 v[84:85], v[162:163]
	v_mov_b64_e32 v[86:87], v[164:165]
	v_readlane_b32 s66, v253, 11
	v_readlane_b32 s67, v253, 12
	v_readlane_b32 s68, v253, 13
	v_readlane_b32 s69, v253, 14
	v_readlane_b32 s70, v253, 15
	v_readlane_b32 s71, v253, 16
	v_readlane_b32 s72, v253, 17
	v_readlane_b32 s73, v253, 18
	v_readlane_b32 s74, v253, 19
	v_readlane_b32 s75, v253, 20
	v_add_f32_e32 v2, v74, v80
	v_add_f32_e32 v80, v70, v84
	v_add_f32_e32 v81, v75, v81
	v_add_f32_e32 v84, v71, v85
	v_add_f32_e32 v82, v76, v82
	v_add_f32_e32 v85, v72, v86
	v_add_f32_e32 v83, v77, v83
	v_add_f32_e32 v86, v73, v87
	v_mul_f32_e32 v2, 0xbfb8aa3b, v2
	v_mul_f32_e32 v80, 0xbfb8aa3b, v80
	v_mul_f32_e32 v81, 0xbfb8aa3b, v81
	v_mul_f32_e32 v84, 0xbfb8aa3b, v84
	v_mul_f32_e32 v82, 0xbfb8aa3b, v82
	v_mul_f32_e32 v85, 0xbfb8aa3b, v85
	v_mul_f32_e32 v83, 0xbfb8aa3b, v83
	v_mul_f32_e32 v86, 0xbfb8aa3b, v86
	v_exp_f32_e32 v2, v2
	v_exp_f32_e32 v80, v80
	v_exp_f32_e32 v81, v81
	v_exp_f32_e32 v84, v84
	v_exp_f32_e32 v82, v82
	v_exp_f32_e32 v85, v85
	v_exp_f32_e32 v83, v83
	v_exp_f32_e32 v86, v86
	v_add_f32_e32 v2, 1.0, v2
	v_add_f32_e32 v80, 1.0, v80
	v_add_f32_e32 v81, 1.0, v81
	v_add_f32_e32 v84, 1.0, v84
	v_add_f32_e32 v88, 1.0, v82
	v_add_f32_e32 v85, 1.0, v85
	v_add_f32_e32 v89, 1.0, v83
	v_add_f32_e32 v90, 1.0, v86
	v_rcp_f32_e32 v86, v2
	v_rcp_f32_e32 v82, v80
	v_rcp_f32_e32 v87, v81
	v_rcp_f32_e32 v83, v84
	v_rcp_f32_e32 v84, v88
	v_rcp_f32_e32 v80, v85
	v_rcp_f32_e32 v85, v89
	v_rcp_f32_e32 v81, v90
; __device__ __forceinline__ float sigmoidf_(float x) { return __builtin_amdgcn_rcpf(1.f + __expf(-x)); }
; __device__ __forceinline__ u32x4 pack8(f32x4 v0, f32x4 v1) { u32x4 w; w.x = cvt_pk_bf16(v0[0], v0[1]); w.y = cvt_pk_bf16(v0[2], v0[3]); w.z = cvt_pk_bf16(v1[0], v1[1]); w.w = cvt_pk_bf16(v1[2], v1[3]); return w; }
;     __device__ __forceinline__ void operator()(const f32x4 (&acc)[2][2][4][2], const pg8::Unit& u, int wr, int wc, int fr, int fq) const {
;     ...
;             const int row = u.pm * 256 + trow, col = u.pn * 256 + tcol;
;             if (col < C_KA) { v0 = v0 * QS_A; v1 = v1 * QS_A; }
;             else if (col >= C_GA && col < INC) { const f32x4 b0 = *(const f32x4*)(bg + col - C_GA), b1 = *(const f32x4*)(bg + col - C_GA + 4);
; #pragma unroll
;                 for (int i = 0; i < 4; ++i) { v0[i] = sigmoidf_(v0[i] + b0[i]); v1[i] = sigmoidf_(v1[i] + b1[i]); } }
;             *(u32x4*)(O + (size_t)row * INCP + col) = pg8::pack8(v0, v1);
.LBB0_204:
	s_andn2_saveexec_b64 s[26:27], s[26:27]
	v_pk_mul_f32 v[84:85], v[76:77], s[18:19] op_sel_hi:[1,0]
	v_pk_mul_f32 v[86:87], v[74:75], s[18:19] op_sel_hi:[1,0]
	v_pk_mul_f32 v[80:81], v[72:73], s[18:19] op_sel_hi:[1,0]
	v_pk_mul_f32 v[82:83], v[70:71], s[18:19] op_sel_hi:[1,0]
	s_or_b64 exec, exec, s[26:27]
	v_cvt_pk_bf16_f32 v70, v86, v87
	v_cvt_pk_bf16_f32 v71, v84, v85
	v_cvt_pk_bf16_f32 v72, v82, v83
	v_cvt_pk_bf16_f32 v73, v80, v81
	global_store_dwordx4 v[78:79], v[70:73], off offset:256
	s_and_saveexec_b64 s[26:27], s[4:5]
	s_xor_b64 s[26:27], exec, s[26:27]
	s_cbranch_execz .LBB0_209
	s_add_i32 s29, s23, 0xfffff760
	v_mov_b64_e32 v[76:77], v[64:65]
	v_mov_b64_e32 v[72:73], v[68:69]
	s_cmpk_gt_u32 s29, 0x7ff
	v_mov_b64_e32 v[74:75], v[62:63]
	v_mov_b64_e32 v[70:71], v[66:67]
	s_cbranch_scc1 .LBB0_209
	v_readlane_b32 s60, v253, 5
	v_mov_b32_e32 v2, v4
	v_readlane_b32 s64, v253, 9
	v_readlane_b32 s65, v253, 10
	v_readlane_b32 s61, v253, 6
	v_readlane_b32 s62, v253, 7
	v_lshl_add_u64 v[70:71], v[2:3], 2, s[64:65]
	v_lshl_add_u64 v[74:75], v[70:71], 0, s[16:17]
	v_add_co_u32_e32 v70, vcc, 0xffffe000, v70
	v_readlane_b32 s63, v253, 8
	s_nop 0
	v_addc_co_u32_e32 v71, vcc, -1, v71, vcc
	v_mov_b64_e32 v[70:71], v[150:151]
	v_mov_b64_e32 v[72:73], v[152:153]
	s_nop 0
	v_mov_b64_e32 v[74:75], v[154:155]
	v_mov_b64_e32 v[76:77], v[156:157]
	v_readlane_b32 s66, v253, 11
	v_readlane_b32 s67, v253, 12
	v_readlane_b32 s68, v253, 13
	v_readlane_b32 s69, v253, 14
	v_readlane_b32 s70, v253, 15
	v_readlane_b32 s71, v253, 16
	v_readlane_b32 s72, v253, 17
	v_readlane_b32 s73, v253, 18
	v_readlane_b32 s74, v253, 19
	v_readlane_b32 s75, v253, 20
	v_add_f32_e32 v2, v66, v70
	v_add_f32_e32 v70, v62, v74
	v_add_f32_e32 v71, v67, v71
	v_add_f32_e32 v74, v63, v75
	v_add_f32_e32 v72, v68, v72
	v_add_f32_e32 v75, v64, v76
	v_add_f32_e32 v73, v69, v73
	v_add_f32_e32 v76, v65, v77
	v_mul_f32_e32 v2, 0xbfb8aa3b, v2
	v_mul_f32_e32 v70, 0xbfb8aa3b, v70
	v_mul_f32_e32 v71, 0xbfb8aa3b, v71
	v_mul_f32_e32 v74, 0xbfb8aa3b, v74
	v_mul_f32_e32 v72, 0xbfb8aa3b, v72
	v_mul_f32_e32 v75, 0xbfb8aa3b, v75
	v_mul_f32_e32 v73, 0xbfb8aa3b, v73
	v_mul_f32_e32 v76, 0xbfb8aa3b, v76
	v_exp_f32_e32 v2, v2
	v_exp_f32_e32 v70, v70
	v_exp_f32_e32 v71, v71
	v_exp_f32_e32 v74, v74
	v_exp_f32_e32 v72, v72
	v_exp_f32_e32 v75, v75
	v_exp_f32_e32 v73, v73
	v_exp_f32_e32 v76, v76
	v_add_f32_e32 v2, 1.0, v2
	v_add_f32_e32 v77, 1.0, v70
	v_add_f32_e32 v71, 1.0, v71
	v_add_f32_e32 v78, 1.0, v74
	v_add_f32_e32 v72, 1.0, v72
	v_add_f32_e32 v79, 1.0, v75
	v_add_f32_e32 v73, 1.0, v73
	v_add_f32_e32 v80, 1.0, v76
	v_rcp_f32_e32 v70, v2
	v_rcp_f32_e32 v74, v77
	v_rcp_f32_e32 v71, v71
	v_rcp_f32_e32 v75, v78
	v_rcp_f32_e32 v72, v72
	v_rcp_f32_e32 v76, v79
	v_rcp_f32_e32 v73, v73
	v_rcp_f32_e32 v77, v80
.LBB0_209:
	s_andn2_saveexec_b64 s[26:27], s[26:27]
	v_pk_mul_f32 v[72:73], v[68:69], s[18:19] op_sel_hi:[1,0]
	v_pk_mul_f32 v[70:71], v[66:67], s[18:19] op_sel_hi:[1,0]
	v_pk_mul_f32 v[76:77], v[64:65], s[18:19] op_sel_hi:[1,0]
	v_pk_mul_f32 v[74:75], v[62:63], s[18:19] op_sel_hi:[1,0]
	s_or_b64 exec, exec, s[26:27]
	v_readlane_b32 s26, v253, 54
	v_readlane_b32 s27, v253, 55
	v_add_u32_e32 v2, s28, v227
	v_cvt_pk_bf16_f32 v62, v70, v71
	v_mov_b64_e32 v[66:67], s[26:27]
	v_mad_i64_i32 v[66:67], s[26:27], v2, s59, v[66:67]
	v_cvt_pk_bf16_f32 v63, v72, v73
	v_cvt_pk_bf16_f32 v64, v74, v75
	v_cvt_pk_bf16_f32 v65, v76, v77
	v_lshl_add_u64 v[70:71], v[4:5], 1, v[66:67]
	global_store_dwordx4 v[70:71], v[62:65], off
	s_and_saveexec_b64 s[26:27], s[6:7]
	s_xor_b64 s[26:27], exec, s[26:27]
	s_cbranch_execz .LBB0_214
	s_add_i32 s29, s23, 0xfffff7e0
	v_mov_b64_e32 v[68:69], v[56:57]
	v_mov_b64_e32 v[64:65], v[60:61]
	s_cmpk_gt_u32 s29, 0x7ff
	v_mov_b64_e32 v[66:67], v[54:55]
	v_mov_b64_e32 v[62:63], v[58:59]
	s_cbranch_scc1 .LBB0_214
	v_readlane_b32 s60, v253, 5
	v_mov_b32_e32 v2, v4
	v_readlane_b32 s64, v253, 9
	v_readlane_b32 s65, v253, 10
	v_readlane_b32 s61, v253, 6
	v_readlane_b32 s62, v253, 7
	v_lshl_add_u64 v[62:63], v[2:3], 2, s[64:65]
	v_lshl_add_u64 v[66:67], v[62:63], 0, s[20:21]
	v_add_co_u32_e32 v62, vcc, 0xffffe000, v62
	v_readlane_b32 s63, v253, 8
	s_nop 0
	v_addc_co_u32_e32 v63, vcc, -1, v63, vcc
	v_mov_b64_e32 v[62:63], v[158:159]
	v_mov_b64_e32 v[64:65], v[160:161]
	s_nop 0
	v_mov_b64_e32 v[66:67], v[162:163]
	v_mov_b64_e32 v[68:69], v[164:165]
	v_readlane_b32 s66, v253, 11
	v_readlane_b32 s67, v253, 12
	v_readlane_b32 s68, v253, 13
	v_readlane_b32 s69, v253, 14
	v_readlane_b32 s70, v253, 15
	v_readlane_b32 s71, v253, 16
	v_readlane_b32 s72, v253, 17
	v_readlane_b32 s73, v253, 18
	v_readlane_b32 s74, v253, 19
	v_readlane_b32 s75, v253, 20
	v_add_f32_e32 v2, v58, v62
	v_add_f32_e32 v62, v54, v66
	v_add_f32_e32 v63, v59, v63
	v_add_f32_e32 v66, v55, v67
	v_add_f32_e32 v64, v60, v64
	v_add_f32_e32 v67, v56, v68
	v_add_f32_e32 v65, v61, v65
	v_add_f32_e32 v68, v57, v69
	v_mul_f32_e32 v2, 0xbfb8aa3b, v2
	v_mul_f32_e32 v62, 0xbfb8aa3b, v62
	v_mul_f32_e32 v63, 0xbfb8aa3b, v63
	v_mul_f32_e32 v66, 0xbfb8aa3b, v66
	v_mul_f32_e32 v64, 0xbfb8aa3b, v64
	v_mul_f32_e32 v67, 0xbfb8aa3b, v67
	v_mul_f32_e32 v65, 0xbfb8aa3b, v65
	v_mul_f32_e32 v68, 0xbfb8aa3b, v68
	v_exp_f32_e32 v2, v2
	v_exp_f32_e32 v62, v62
	v_exp_f32_e32 v63, v63
	v_exp_f32_e32 v66, v66
	v_exp_f32_e32 v64, v64
	v_exp_f32_e32 v67, v67
	v_exp_f32_e32 v65, v65
	v_exp_f32_e32 v68, v68
	v_add_f32_e32 v2, 1.0, v2
	v_add_f32_e32 v69, 1.0, v62
	v_add_f32_e32 v63, 1.0, v63
	v_add_f32_e32 v72, 1.0, v66
	v_add_f32_e32 v64, 1.0, v64
	v_add_f32_e32 v73, 1.0, v67
	v_add_f32_e32 v65, 1.0, v65
	v_add_f32_e32 v74, 1.0, v68
	v_rcp_f32_e32 v62, v2
	v_rcp_f32_e32 v66, v69
	v_rcp_f32_e32 v63, v63
	v_rcp_f32_e32 v67, v72
	v_rcp_f32_e32 v64, v64
	v_rcp_f32_e32 v68, v73
	v_rcp_f32_e32 v65, v65
	v_rcp_f32_e32 v69, v74
; __device__ __forceinline__ float sigmoidf_(float x) { return __builtin_amdgcn_rcpf(1.f + __expf(-x)); }
; __device__ __forceinline__ u32x4 pack8(f32x4 v0, f32x4 v1) { u32x4 w; w.x = cvt_pk_bf16(v0[0], v0[1]); w.y = cvt_pk_bf16(v0[2], v0[3]); w.z = cvt_pk_bf16(v1[0], v1[1]); w.w = cvt_pk_bf16(v1[2], v1[3]); return w; }
;     __device__ __forceinline__ void operator()(const f32x4 (&acc)[2][2][4][2], const pg8::Unit& u, int wr, int wc, int fr, int fq) const {
;     ...
;             const int row = u.pm * 256 + trow, col = u.pn * 256 + tcol;
;             if (col < C_KA) { v0 = v0 * QS_A; v1 = v1 * QS_A; }
;             else if (col >= C_GA && col < INC) { const f32x4 b0 = *(const f32x4*)(bg + col - C_GA), b1 = *(const f32x4*)(bg + col - C_GA + 4);
; #pragma unroll
;                 for (int i = 0; i < 4; ++i) { v0[i] = sigmoidf_(v0[i] + b0[i]); v1[i] = sigmoidf_(v1[i] + b1[i]); } }
;             *(u32x4*)(O + (size_t)row * INCP + col) = pg8::pack8(v0, v1);
.LBB0_214:
	s_andn2_saveexec_b64 s[26:27], s[26:27]
	v_pk_mul_f32 v[64:65], v[60:61], s[18:19] op_sel_hi:[1,0]
	v_pk_mul_f32 v[62:63], v[58:59], s[18:19] op_sel_hi:[1,0]
	v_pk_mul_f32 v[68:69], v[56:57], s[18:19] op_sel_hi:[1,0]
	v_pk_mul_f32 v[66:67], v[54:55], s[18:19] op_sel_hi:[1,0]
	s_or_b64 exec, exec, s[26:27]
	v_cvt_pk_bf16_f32 v54, v62, v63
	v_cvt_pk_bf16_f32 v55, v64, v65
	v_cvt_pk_bf16_f32 v56, v66, v67
	v_cvt_pk_bf16_f32 v57, v68, v69
	global_store_dwordx4 v[70:71], v[54:57], off offset:256
	s_and_saveexec_b64 s[26:27], s[4:5]
	s_xor_b64 s[26:27], exec, s[26:27]
	s_cbranch_execz .LBB0_219
	s_add_i32 s29, s23, 0xfffff760
	v_mov_b64_e32 v[60:61], v[48:49]
	v_mov_b64_e32 v[56:57], v[52:53]
	s_cmpk_gt_u32 s29, 0x7ff
	v_mov_b64_e32 v[58:59], v[46:47]
	v_mov_b64_e32 v[54:55], v[50:51]
	s_cbranch_scc1 .LBB0_219
	v_readlane_b32 s60, v253, 5
	v_mov_b32_e32 v2, v4
	v_readlane_b32 s64, v253, 9
	v_readlane_b32 s65, v253, 10
	v_readlane_b32 s61, v253, 6
	v_readlane_b32 s62, v253, 7
	v_lshl_add_u64 v[54:55], v[2:3], 2, s[64:65]
	v_lshl_add_u64 v[58:59], v[54:55], 0, s[16:17]
	v_add_co_u32_e32 v54, vcc, 0xffffe000, v54
	v_readlane_b32 s63, v253, 8
	s_nop 0
	v_addc_co_u32_e32 v55, vcc, -1, v55, vcc
	v_mov_b64_e32 v[54:55], v[150:151]
	v_mov_b64_e32 v[56:57], v[152:153]
	s_nop 0
	v_mov_b64_e32 v[58:59], v[154:155]
	v_mov_b64_e32 v[60:61], v[156:157]
	v_readlane_b32 s66, v253, 11
	v_readlane_b32 s67, v253, 12
	v_readlane_b32 s68, v253, 13
	v_readlane_b32 s69, v253, 14
	v_readlane_b32 s70, v253, 15
	v_readlane_b32 s71, v253, 16
	v_readlane_b32 s72, v253, 17
	v_readlane_b32 s73, v253, 18
	v_readlane_b32 s74, v253, 19
	v_readlane_b32 s75, v253, 20
	v_add_f32_e32 v2, v50, v54
	v_add_f32_e32 v54, v46, v58
	v_add_f32_e32 v55, v51, v55
	v_add_f32_e32 v58, v47, v59
	v_add_f32_e32 v56, v52, v56
	v_add_f32_e32 v59, v48, v60
	v_add_f32_e32 v57, v53, v57
	v_add_f32_e32 v60, v49, v61
	v_mul_f32_e32 v2, 0xbfb8aa3b, v2
	v_mul_f32_e32 v54, 0xbfb8aa3b, v54
	v_mul_f32_e32 v55, 0xbfb8aa3b, v55
	v_mul_f32_e32 v58, 0xbfb8aa3b, v58
	v_mul_f32_e32 v56, 0xbfb8aa3b, v56
	v_mul_f32_e32 v59, 0xbfb8aa3b, v59
	v_mul_f32_e32 v57, 0xbfb8aa3b, v57
	v_mul_f32_e32 v60, 0xbfb8aa3b, v60
	v_exp_f32_e32 v2, v2
	v_exp_f32_e32 v54, v54
	v_exp_f32_e32 v55, v55
	v_exp_f32_e32 v58, v58
	v_exp_f32_e32 v56, v56
	v_exp_f32_e32 v59, v59
	v_exp_f32_e32 v57, v57
	v_exp_f32_e32 v60, v60
	v_add_f32_e32 v2, 1.0, v2
	v_add_f32_e32 v61, 1.0, v54
	v_add_f32_e32 v55, 1.0, v55
	v_add_f32_e32 v62, 1.0, v58
	v_add_f32_e32 v56, 1.0, v56
	v_add_f32_e32 v63, 1.0, v59
	v_add_f32_e32 v57, 1.0, v57
	v_add_f32_e32 v64, 1.0, v60
	v_rcp_f32_e32 v54, v2
	v_rcp_f32_e32 v58, v61
	v_rcp_f32_e32 v55, v55
	v_rcp_f32_e32 v59, v62
	v_rcp_f32_e32 v56, v56
	v_rcp_f32_e32 v60, v63
	v_rcp_f32_e32 v57, v57
	v_rcp_f32_e32 v61, v64
.LBB0_219:
	s_andn2_saveexec_b64 s[26:27], s[26:27]
	v_pk_mul_f32 v[56:57], v[52:53], s[18:19] op_sel_hi:[1,0]
	v_pk_mul_f32 v[54:55], v[50:51], s[18:19] op_sel_hi:[1,0]
	v_pk_mul_f32 v[60:61], v[48:49], s[18:19] op_sel_hi:[1,0]
	v_pk_mul_f32 v[58:59], v[46:47], s[18:19] op_sel_hi:[1,0]
	s_or_b64 exec, exec, s[26:27]
	v_readlane_b32 s26, v253, 54
	v_readlane_b32 s27, v253, 55
	v_add_u32_e32 v2, s28, v228
	v_cvt_pk_bf16_f32 v46, v54, v55
	v_mov_b64_e32 v[50:51], s[26:27]
	v_mad_i64_i32 v[50:51], s[26:27], v2, s59, v[50:51]
	v_cvt_pk_bf16_f32 v47, v56, v57
	v_cvt_pk_bf16_f32 v48, v58, v59
	v_cvt_pk_bf16_f32 v49, v60, v61
	v_lshl_add_u64 v[54:55], v[4:5], 1, v[50:51]
	global_store_dwordx4 v[54:55], v[46:49], off
	s_and_saveexec_b64 s[26:27], s[6:7]
	s_xor_b64 s[26:27], exec, s[26:27]
	s_cbranch_execz .LBB0_224
	s_add_i32 s29, s23, 0xfffff7e0
	v_mov_b64_e32 v[52:53], v[40:41]
	v_mov_b64_e32 v[48:49], v[44:45]
	s_cmpk_gt_u32 s29, 0x7ff
	v_mov_b64_e32 v[50:51], v[38:39]
	v_mov_b64_e32 v[46:47], v[42:43]
	s_cbranch_scc1 .LBB0_224
	v_readlane_b32 s60, v253, 5
	v_mov_b32_e32 v2, v4
	v_readlane_b32 s64, v253, 9
	v_readlane_b32 s65, v253, 10
	v_readlane_b32 s61, v253, 6
	v_readlane_b32 s62, v253, 7
	v_lshl_add_u64 v[46:47], v[2:3], 2, s[64:65]
	v_lshl_add_u64 v[50:51], v[46:47], 0, s[20:21]
	v_add_co_u32_e32 v46, vcc, 0xffffe000, v46
	v_readlane_b32 s63, v253, 8
	s_nop 0
	v_addc_co_u32_e32 v47, vcc, -1, v47, vcc
	v_mov_b64_e32 v[46:47], v[158:159]
	v_mov_b64_e32 v[48:49], v[160:161]
	s_nop 0
	v_mov_b64_e32 v[50:51], v[162:163]
	v_mov_b64_e32 v[52:53], v[164:165]
	v_readlane_b32 s66, v253, 11
	v_readlane_b32 s67, v253, 12
	v_readlane_b32 s68, v253, 13
	v_readlane_b32 s69, v253, 14
	v_readlane_b32 s70, v253, 15
	v_readlane_b32 s71, v253, 16
	v_readlane_b32 s72, v253, 17
	v_readlane_b32 s73, v253, 18
	v_readlane_b32 s74, v253, 19
	v_readlane_b32 s75, v253, 20
	v_add_f32_e32 v2, v42, v46
	v_add_f32_e32 v46, v38, v50
	v_add_f32_e32 v47, v43, v47
	v_add_f32_e32 v50, v39, v51
	v_add_f32_e32 v48, v44, v48
	v_add_f32_e32 v51, v40, v52
	v_add_f32_e32 v49, v45, v49
	v_add_f32_e32 v52, v41, v53
	v_mul_f32_e32 v2, 0xbfb8aa3b, v2
	v_mul_f32_e32 v46, 0xbfb8aa3b, v46
	v_mul_f32_e32 v47, 0xbfb8aa3b, v47
	v_mul_f32_e32 v50, 0xbfb8aa3b, v50
	v_mul_f32_e32 v48, 0xbfb8aa3b, v48
	v_mul_f32_e32 v51, 0xbfb8aa3b, v51
	v_mul_f32_e32 v49, 0xbfb8aa3b, v49
	v_mul_f32_e32 v52, 0xbfb8aa3b, v52
	v_exp_f32_e32 v2, v2
	v_exp_f32_e32 v46, v46
	v_exp_f32_e32 v47, v47
	v_exp_f32_e32 v50, v50
	v_exp_f32_e32 v48, v48
	v_exp_f32_e32 v51, v51
	v_exp_f32_e32 v49, v49
	v_exp_f32_e32 v52, v52
	v_add_f32_e32 v2, 1.0, v2
	v_add_f32_e32 v53, 1.0, v46
	v_add_f32_e32 v47, 1.0, v47
	v_add_f32_e32 v56, 1.0, v50
	v_add_f32_e32 v48, 1.0, v48
	v_add_f32_e32 v57, 1.0, v51
	v_add_f32_e32 v49, 1.0, v49
	v_add_f32_e32 v58, 1.0, v52
	v_rcp_f32_e32 v46, v2
	v_rcp_f32_e32 v50, v53
	v_rcp_f32_e32 v47, v47
	v_rcp_f32_e32 v51, v56
	v_rcp_f32_e32 v48, v48
	v_rcp_f32_e32 v52, v57
	v_rcp_f32_e32 v49, v49
	v_rcp_f32_e32 v53, v58
; __device__ __forceinline__ float sigmoidf_(float x) { return __builtin_amdgcn_rcpf(1.f + __expf(-x)); }
; __device__ __forceinline__ u32x4 pack8(f32x4 v0, f32x4 v1) { u32x4 w; w.x = cvt_pk_bf16(v0[0], v0[1]); w.y = cvt_pk_bf16(v0[2], v0[3]); w.z = cvt_pk_bf16(v1[0], v1[1]); w.w = cvt_pk_bf16(v1[2], v1[3]); return w; }
;     __device__ __forceinline__ void operator()(const f32x4 (&acc)[2][2][4][2], const pg8::Unit& u, int wr, int wc, int fr, int fq) const {
;     ...
;             const int row = u.pm * 256 + trow, col = u.pn * 256 + tcol;
;             if (col < C_KA) { v0 = v0 * QS_A; v1 = v1 * QS_A; }
;             else if (col >= C_GA && col < INC) { const f32x4 b0 = *(const f32x4*)(bg + col - C_GA), b1 = *(const f32x4*)(bg + col - C_GA + 4);
; #pragma unroll
;                 for (int i = 0; i < 4; ++i) { v0[i] = sigmoidf_(v0[i] + b0[i]); v1[i] = sigmoidf_(v1[i] + b1[i]); } }
;             *(u32x4*)(O + (size_t)row * INCP + col) = pg8::pack8(v0, v1);
.LBB0_224:
	s_andn2_saveexec_b64 s[26:27], s[26:27]
	v_pk_mul_f32 v[48:49], v[44:45], s[18:19] op_sel_hi:[1,0]
	v_pk_mul_f32 v[46:47], v[42:43], s[18:19] op_sel_hi:[1,0]
	v_pk_mul_f32 v[52:53], v[40:41], s[18:19] op_sel_hi:[1,0]
	v_pk_mul_f32 v[50:51], v[38:39], s[18:19] op_sel_hi:[1,0]
	s_or_b64 exec, exec, s[26:27]
	v_cvt_pk_bf16_f32 v38, v46, v47
	v_cvt_pk_bf16_f32 v39, v48, v49
	v_cvt_pk_bf16_f32 v40, v50, v51
	v_cvt_pk_bf16_f32 v41, v52, v53
	global_store_dwordx4 v[54:55], v[38:41], off offset:256
	s_and_saveexec_b64 s[26:27], s[4:5]
	s_xor_b64 s[26:27], exec, s[26:27]
	s_cbranch_execz .LBB0_229
	s_add_i32 s29, s23, 0xfffff760
	v_mov_b64_e32 v[44:45], v[32:33]
	v_mov_b64_e32 v[40:41], v[36:37]
	s_cmpk_gt_u32 s29, 0x7ff
	v_mov_b64_e32 v[42:43], v[30:31]
	v_mov_b64_e32 v[38:39], v[34:35]
	s_cbranch_scc1 .LBB0_229
	v_readlane_b32 s60, v253, 5
	v_mov_b32_e32 v2, v4
	v_readlane_b32 s64, v253, 9
	v_readlane_b32 s65, v253, 10
	v_readlane_b32 s61, v253, 6
	v_readlane_b32 s62, v253, 7
	v_lshl_add_u64 v[38:39], v[2:3], 2, s[64:65]
	v_lshl_add_u64 v[42:43], v[38:39], 0, s[16:17]
	v_add_co_u32_e32 v38, vcc, 0xffffe000, v38
	v_readlane_b32 s63, v253, 8
	s_nop 0
	v_addc_co_u32_e32 v39, vcc, -1, v39, vcc
	v_mov_b64_e32 v[38:39], v[150:151]
	v_mov_b64_e32 v[40:41], v[152:153]
	s_nop 0
	v_mov_b64_e32 v[42:43], v[154:155]
	v_mov_b64_e32 v[44:45], v[156:157]
	v_readlane_b32 s66, v253, 11
	v_readlane_b32 s67, v253, 12
	v_readlane_b32 s68, v253, 13
	v_readlane_b32 s69, v253, 14
	v_readlane_b32 s70, v253, 15
	v_readlane_b32 s71, v253, 16
	v_readlane_b32 s72, v253, 17
	v_readlane_b32 s73, v253, 18
	v_readlane_b32 s74, v253, 19
	v_readlane_b32 s75, v253, 20
	v_add_f32_e32 v2, v34, v38
	v_add_f32_e32 v38, v30, v42
	v_add_f32_e32 v39, v35, v39
	v_add_f32_e32 v42, v31, v43
	v_add_f32_e32 v40, v36, v40
	v_add_f32_e32 v43, v32, v44
	v_add_f32_e32 v41, v37, v41
	v_add_f32_e32 v44, v33, v45
	v_mul_f32_e32 v2, 0xbfb8aa3b, v2
	v_mul_f32_e32 v38, 0xbfb8aa3b, v38
	v_mul_f32_e32 v39, 0xbfb8aa3b, v39
	v_mul_f32_e32 v42, 0xbfb8aa3b, v42
	v_mul_f32_e32 v40, 0xbfb8aa3b, v40
	v_mul_f32_e32 v43, 0xbfb8aa3b, v43
	v_mul_f32_e32 v41, 0xbfb8aa3b, v41
	v_mul_f32_e32 v44, 0xbfb8aa3b, v44
	v_exp_f32_e32 v2, v2
	v_exp_f32_e32 v38, v38
	v_exp_f32_e32 v39, v39
	v_exp_f32_e32 v42, v42
	v_exp_f32_e32 v40, v40
	v_exp_f32_e32 v43, v43
	v_exp_f32_e32 v41, v41
	v_exp_f32_e32 v44, v44
	v_add_f32_e32 v2, 1.0, v2
	v_add_f32_e32 v45, 1.0, v38
	v_add_f32_e32 v39, 1.0, v39
	v_add_f32_e32 v46, 1.0, v42
	v_add_f32_e32 v40, 1.0, v40
	v_add_f32_e32 v47, 1.0, v43
	v_add_f32_e32 v41, 1.0, v41
	v_add_f32_e32 v48, 1.0, v44
	v_rcp_f32_e32 v38, v2
	v_rcp_f32_e32 v42, v45
	v_rcp_f32_e32 v39, v39
	v_rcp_f32_e32 v43, v46
	v_rcp_f32_e32 v40, v40
	v_rcp_f32_e32 v44, v47
	v_rcp_f32_e32 v41, v41
	v_rcp_f32_e32 v45, v48
.LBB0_229:
	s_andn2_saveexec_b64 s[26:27], s[26:27]
	v_pk_mul_f32 v[40:41], v[36:37], s[18:19] op_sel_hi:[1,0]
	v_pk_mul_f32 v[38:39], v[34:35], s[18:19] op_sel_hi:[1,0]
	v_pk_mul_f32 v[44:45], v[32:33], s[18:19] op_sel_hi:[1,0]
	v_pk_mul_f32 v[42:43], v[30:31], s[18:19] op_sel_hi:[1,0]
	s_or_b64 exec, exec, s[26:27]
	v_readlane_b32 s26, v253, 54
	v_readlane_b32 s27, v253, 55
	v_add_u32_e32 v2, s28, v229
	v_cvt_pk_bf16_f32 v30, v38, v39
	v_mov_b64_e32 v[34:35], s[26:27]
	v_mad_i64_i32 v[34:35], s[26:27], v2, s59, v[34:35]
	v_cvt_pk_bf16_f32 v31, v40, v41
	v_cvt_pk_bf16_f32 v32, v42, v43
	v_cvt_pk_bf16_f32 v33, v44, v45
	v_lshl_add_u64 v[38:39], v[4:5], 1, v[34:35]
	global_store_dwordx4 v[38:39], v[30:33], off
	s_and_saveexec_b64 s[26:27], s[6:7]
	s_xor_b64 s[26:27], exec, s[26:27]
	s_cbranch_execz .LBB0_234
	s_add_i32 s29, s23, 0xfffff7e0
	v_mov_b64_e32 v[36:37], v[24:25]
	v_mov_b64_e32 v[32:33], v[28:29]
	s_cmpk_gt_u32 s29, 0x7ff
	v_mov_b64_e32 v[34:35], v[22:23]
	v_mov_b64_e32 v[30:31], v[26:27]
	s_cbranch_scc1 .LBB0_234
	v_readlane_b32 s60, v253, 5
	v_mov_b32_e32 v2, v4
	v_readlane_b32 s64, v253, 9
	v_readlane_b32 s65, v253, 10
	v_readlane_b32 s61, v253, 6
	v_readlane_b32 s62, v253, 7
	v_lshl_add_u64 v[30:31], v[2:3], 2, s[64:65]
	v_lshl_add_u64 v[34:35], v[30:31], 0, s[20:21]
	v_add_co_u32_e32 v30, vcc, 0xffffe000, v30
	v_readlane_b32 s63, v253, 8
	s_nop 0
	v_addc_co_u32_e32 v31, vcc, -1, v31, vcc
	v_mov_b64_e32 v[30:31], v[158:159]
	v_mov_b64_e32 v[32:33], v[160:161]
	s_nop 0
	v_mov_b64_e32 v[34:35], v[162:163]
	v_mov_b64_e32 v[36:37], v[164:165]
	v_readlane_b32 s66, v253, 11
	v_readlane_b32 s67, v253, 12
	v_readlane_b32 s68, v253, 13
	v_readlane_b32 s69, v253, 14
	v_readlane_b32 s70, v253, 15
	v_readlane_b32 s71, v253, 16
	v_readlane_b32 s72, v253, 17
	v_readlane_b32 s73, v253, 18
	v_readlane_b32 s74, v253, 19
	v_readlane_b32 s75, v253, 20
	v_add_f32_e32 v2, v26, v30
	v_add_f32_e32 v30, v22, v34
	v_add_f32_e32 v31, v27, v31
	v_add_f32_e32 v34, v23, v35
	v_add_f32_e32 v32, v28, v32
	v_add_f32_e32 v35, v24, v36
	v_add_f32_e32 v33, v29, v33
	v_add_f32_e32 v36, v25, v37
	v_mul_f32_e32 v2, 0xbfb8aa3b, v2
	v_mul_f32_e32 v30, 0xbfb8aa3b, v30
	v_mul_f32_e32 v31, 0xbfb8aa3b, v31
	v_mul_f32_e32 v34, 0xbfb8aa3b, v34
	v_mul_f32_e32 v32, 0xbfb8aa3b, v32
	v_mul_f32_e32 v35, 0xbfb8aa3b, v35
	v_mul_f32_e32 v33, 0xbfb8aa3b, v33
	v_mul_f32_e32 v36, 0xbfb8aa3b, v36
	v_exp_f32_e32 v2, v2
	v_exp_f32_e32 v30, v30
	v_exp_f32_e32 v31, v31
	v_exp_f32_e32 v34, v34
	v_exp_f32_e32 v32, v32
	v_exp_f32_e32 v35, v35
	v_exp_f32_e32 v33, v33
	v_exp_f32_e32 v36, v36
	v_add_f32_e32 v2, 1.0, v2
	v_add_f32_e32 v37, 1.0, v30
	v_add_f32_e32 v31, 1.0, v31
	v_add_f32_e32 v40, 1.0, v34
	v_add_f32_e32 v32, 1.0, v32
	v_add_f32_e32 v41, 1.0, v35
	v_add_f32_e32 v33, 1.0, v33
	v_add_f32_e32 v42, 1.0, v36
	v_rcp_f32_e32 v30, v2
	v_rcp_f32_e32 v34, v37
	v_rcp_f32_e32 v31, v31
	v_rcp_f32_e32 v35, v40
	v_rcp_f32_e32 v32, v32
	v_rcp_f32_e32 v36, v41
	v_rcp_f32_e32 v33, v33
	v_rcp_f32_e32 v37, v42
; __device__ __forceinline__ float sigmoidf_(float x) { return __builtin_amdgcn_rcpf(1.f + __expf(-x)); }
; __device__ __forceinline__ u32x4 pack8(f32x4 v0, f32x4 v1) { u32x4 w; w.x = cvt_pk_bf16(v0[0], v0[1]); w.y = cvt_pk_bf16(v0[2], v0[3]); w.z = cvt_pk_bf16(v1[0], v1[1]); w.w = cvt_pk_bf16(v1[2], v1[3]); return w; }
;     __device__ __forceinline__ void operator()(const f32x4 (&acc)[2][2][4][2], const pg8::Unit& u, int wr, int wc, int fr, int fq) const {
;     ...
;             const int row = u.pm * 256 + trow, col = u.pn * 256 + tcol;
;             if (col < C_KA) { v0 = v0 * QS_A; v1 = v1 * QS_A; }
;             else if (col >= C_GA && col < INC) { const f32x4 b0 = *(const f32x4*)(bg + col - C_GA), b1 = *(const f32x4*)(bg + col - C_GA + 4);
; #pragma unroll
;                 for (int i = 0; i < 4; ++i) { v0[i] = sigmoidf_(v0[i] + b0[i]); v1[i] = sigmoidf_(v1[i] + b1[i]); } }
;             *(u32x4*)(O + (size_t)row * INCP + col) = pg8::pack8(v0, v1);
.LBB0_234:
	s_andn2_saveexec_b64 s[26:27], s[26:27]
	v_pk_mul_f32 v[32:33], v[28:29], s[18:19] op_sel_hi:[1,0]
	v_pk_mul_f32 v[30:31], v[26:27], s[18:19] op_sel_hi:[1,0]
	v_pk_mul_f32 v[36:37], v[24:25], s[18:19] op_sel_hi:[1,0]
	v_pk_mul_f32 v[34:35], v[22:23], s[18:19] op_sel_hi:[1,0]
	s_or_b64 exec, exec, s[26:27]
	v_cvt_pk_bf16_f32 v22, v30, v31
	v_cvt_pk_bf16_f32 v23, v32, v33
	v_cvt_pk_bf16_f32 v24, v34, v35
	v_cvt_pk_bf16_f32 v25, v36, v37
	global_store_dwordx4 v[38:39], v[22:25], off offset:256
	s_and_saveexec_b64 s[26:27], s[4:5]
	s_xor_b64 s[4:5], exec, s[26:27]
	s_cbranch_execz .LBB0_239
	s_add_i32 s26, s23, 0xfffff760
	v_mov_b64_e32 v[28:29], v[16:17]
	v_mov_b64_e32 v[24:25], v[20:21]
	s_cmpk_gt_u32 s26, 0x7ff
	v_mov_b64_e32 v[26:27], v[14:15]
	v_mov_b64_e32 v[22:23], v[18:19]
	s_cbranch_scc1 .LBB0_239
	v_readlane_b32 s60, v253, 5
	v_mov_b32_e32 v2, v4
	v_readlane_b32 s64, v253, 9
	v_readlane_b32 s65, v253, 10
	v_readlane_b32 s61, v253, 6
	v_readlane_b32 s62, v253, 7
	v_lshl_add_u64 v[22:23], v[2:3], 2, s[64:65]
	v_lshl_add_u64 v[26:27], v[22:23], 0, s[16:17]
	v_add_co_u32_e32 v22, vcc, 0xffffe000, v22
	v_readlane_b32 s63, v253, 8
	s_nop 0
	v_addc_co_u32_e32 v23, vcc, -1, v23, vcc
	v_mov_b64_e32 v[22:23], v[150:151]
	v_mov_b64_e32 v[24:25], v[152:153]
	s_nop 0
	v_mov_b64_e32 v[26:27], v[154:155]
	v_mov_b64_e32 v[28:29], v[156:157]
	v_readlane_b32 s66, v253, 11
	v_readlane_b32 s67, v253, 12
	v_readlane_b32 s68, v253, 13
	v_readlane_b32 s69, v253, 14
	v_readlane_b32 s70, v253, 15
	v_readlane_b32 s71, v253, 16
	v_readlane_b32 s72, v253, 17
	v_readlane_b32 s73, v253, 18
	v_readlane_b32 s74, v253, 19
	v_readlane_b32 s75, v253, 20
	v_add_f32_e32 v2, v18, v22
	v_add_f32_e32 v22, v14, v26
	v_add_f32_e32 v23, v19, v23
	v_add_f32_e32 v26, v15, v27
	v_add_f32_e32 v24, v20, v24
	v_add_f32_e32 v27, v16, v28
	v_add_f32_e32 v25, v21, v25
	v_add_f32_e32 v28, v17, v29
	v_mul_f32_e32 v2, 0xbfb8aa3b, v2
	v_mul_f32_e32 v22, 0xbfb8aa3b, v22
	v_mul_f32_e32 v23, 0xbfb8aa3b, v23
	v_mul_f32_e32 v26, 0xbfb8aa3b, v26
	v_mul_f32_e32 v24, 0xbfb8aa3b, v24
	v_mul_f32_e32 v27, 0xbfb8aa3b, v27
	v_mul_f32_e32 v25, 0xbfb8aa3b, v25
	v_mul_f32_e32 v28, 0xbfb8aa3b, v28
	v_exp_f32_e32 v2, v2
	v_exp_f32_e32 v22, v22
	v_exp_f32_e32 v23, v23
	v_exp_f32_e32 v26, v26
	v_exp_f32_e32 v24, v24
	v_exp_f32_e32 v27, v27
	v_exp_f32_e32 v25, v25
	v_exp_f32_e32 v28, v28
	v_add_f32_e32 v2, 1.0, v2
	v_add_f32_e32 v29, 1.0, v22
	v_add_f32_e32 v23, 1.0, v23
	v_add_f32_e32 v30, 1.0, v26
	v_add_f32_e32 v24, 1.0, v24
	v_add_f32_e32 v31, 1.0, v27
	v_add_f32_e32 v25, 1.0, v25
	v_add_f32_e32 v32, 1.0, v28
	v_rcp_f32_e32 v22, v2
	v_rcp_f32_e32 v26, v29
	v_rcp_f32_e32 v23, v23
	v_rcp_f32_e32 v27, v30
	v_rcp_f32_e32 v24, v24
	v_rcp_f32_e32 v28, v31
	v_rcp_f32_e32 v25, v25
	v_rcp_f32_e32 v29, v32
.LBB0_239:
	s_andn2_saveexec_b64 s[4:5], s[4:5]
	v_pk_mul_f32 v[24:25], v[20:21], s[18:19] op_sel_hi:[1,0]
	v_pk_mul_f32 v[22:23], v[18:19], s[18:19] op_sel_hi:[1,0]
	v_pk_mul_f32 v[28:29], v[16:17], s[18:19] op_sel_hi:[1,0]
	v_pk_mul_f32 v[26:27], v[14:15], s[18:19] op_sel_hi:[1,0]
	s_or_b64 exec, exec, s[4:5]
	v_readlane_b32 s4, v253, 54
	v_readlane_b32 s5, v253, 55
	v_add_u32_e32 v2, s28, v230
	v_cvt_pk_bf16_f32 v14, v22, v23
	v_mov_b64_e32 v[18:19], s[4:5]
	v_mad_i64_i32 v[18:19], s[4:5], v2, s59, v[18:19]
	v_cvt_pk_bf16_f32 v15, v24, v25
	v_cvt_pk_bf16_f32 v16, v26, v27
	v_cvt_pk_bf16_f32 v17, v28, v29
	v_lshl_add_u64 v[22:23], v[4:5], 1, v[18:19]
	global_store_dwordx4 v[22:23], v[14:17], off
	s_and_saveexec_b64 s[4:5], s[6:7]
	s_xor_b64 s[4:5], exec, s[4:5]
	s_cbranch_execz .LBB0_244
	s_addk_i32 s23, 0xf7e0
	v_mov_b64_e32 v[20:21], v[8:9]
	v_mov_b64_e32 v[16:17], v[12:13]
	s_cmpk_gt_u32 s23, 0x7ff
	v_mov_b64_e32 v[18:19], v[6:7]
	v_mov_b64_e32 v[14:15], v[10:11]
	s_cbranch_scc1 .LBB0_244
	v_readlane_b32 s60, v253, 5
	v_mov_b32_e32 v5, v3
	v_readlane_b32 s64, v253, 9
	v_readlane_b32 s65, v253, 10
	v_readlane_b32 s61, v253, 6
	v_readlane_b32 s62, v253, 7
	v_lshl_add_u64 v[4:5], v[4:5], 2, s[64:65]
	v_lshl_add_u64 v[18:19], v[4:5], 0, s[20:21]
	v_add_co_u32_e32 v4, vcc, 0xffffe000, v4
	v_readlane_b32 s63, v253, 8
	s_nop 0
	v_addc_co_u32_e32 v5, vcc, -1, v5, vcc
	v_mov_b64_e32 v[14:15], v[158:159]
	v_mov_b64_e32 v[16:17], v[160:161]
	s_nop 0
	v_mov_b64_e32 v[18:19], v[162:163]
	v_mov_b64_e32 v[20:21], v[164:165]
	v_readlane_b32 s66, v253, 11
	v_readlane_b32 s67, v253, 12
	v_readlane_b32 s68, v253, 13
	v_readlane_b32 s69, v253, 14
	v_readlane_b32 s70, v253, 15
	v_readlane_b32 s71, v253, 16
	v_readlane_b32 s72, v253, 17
	v_readlane_b32 s73, v253, 18
	v_readlane_b32 s74, v253, 19
	v_readlane_b32 s75, v253, 20
	v_add_f32_e32 v2, v10, v14
	v_add_f32_e32 v4, v6, v18
	v_add_f32_e32 v5, v11, v15
	v_add_f32_e32 v14, v7, v19
	v_add_f32_e32 v15, v12, v16
	v_add_f32_e32 v16, v8, v20
	v_add_f32_e32 v17, v13, v17
	v_add_f32_e32 v18, v9, v21
	v_mul_f32_e32 v2, 0xbfb8aa3b, v2
	v_mul_f32_e32 v4, 0xbfb8aa3b, v4
	v_mul_f32_e32 v5, 0xbfb8aa3b, v5
	v_mul_f32_e32 v14, 0xbfb8aa3b, v14
	v_mul_f32_e32 v15, 0xbfb8aa3b, v15
	v_mul_f32_e32 v16, 0xbfb8aa3b, v16
	v_mul_f32_e32 v17, 0xbfb8aa3b, v17
	v_mul_f32_e32 v18, 0xbfb8aa3b, v18
	v_exp_f32_e32 v2, v2
	v_exp_f32_e32 v4, v4
	v_exp_f32_e32 v5, v5
	v_exp_f32_e32 v14, v14
	v_exp_f32_e32 v15, v15
	v_exp_f32_e32 v16, v16
	v_exp_f32_e32 v17, v17
	v_exp_f32_e32 v18, v18
	v_add_f32_e32 v2, 1.0, v2
	v_add_f32_e32 v4, 1.0, v4
	v_add_f32_e32 v5, 1.0, v5
	v_add_f32_e32 v19, 1.0, v14
	v_add_f32_e32 v20, 1.0, v15
	v_add_f32_e32 v21, 1.0, v16
	v_add_f32_e32 v17, 1.0, v17
	v_add_f32_e32 v24, 1.0, v18
	v_rcp_f32_e32 v14, v2
	v_rcp_f32_e32 v18, v4
	v_rcp_f32_e32 v15, v5
	v_rcp_f32_e32 v19, v19
	v_rcp_f32_e32 v16, v20
	v_rcp_f32_e32 v20, v21
	v_rcp_f32_e32 v17, v17
	v_rcp_f32_e32 v21, v24

; __device__ __forceinline__ float sigmoidf_(float x) { return __builtin_amdgcn_rcpf(1.f + __expf(-x)); }
; __device__ __forceinline__ u32x4 pack8(f32x4 v0, f32x4 v1) { u32x4 w; w.x = cvt_pk_bf16(v0[0], v0[1]); w.y = cvt_pk_bf16(v0[2], v0[3]); w.z = cvt_pk_bf16(v1[0], v1[1]); w.w = cvt_pk_bf16(v1[2], v1[3]); return w; }
;     __device__ __forceinline__ void operator()(const f32x4 (&acc)[2][2][4][2], const pg8::Unit& u, int wr, int wc, int fr, int fq) const {
;     ...
;             const int row = u.pm * 256 + trow, col = u.pn * 256 + tcol;
;             if (col < C_KA) { v0 = v0 * QS_A; v1 = v1 * QS_A; }
;             else if (col >= C_GA && col < INC) { const f32x4 b0 = *(const f32x4*)(bg + col - C_GA), b1 = *(const f32x4*)(bg + col - C_GA + 4);
; #pragma unroll
;                 for (int i = 0; i < 4; ++i) { v0[i] = sigmoidf_(v0[i] + b0[i]); v1[i] = sigmoidf_(v1[i] + b1[i]); } }
;             *(u32x4*)(O + (size_t)row * INCP + col) = pg8::pack8(v0, v1);
.LBB0_2625:
	s_lshl_b32 s2, s2, 8
	s_or_b32 s25, s47, s2
	v_or_b32_e32 v4, s25, v222
	v_cmp_lt_i32_e64 s[4:5], s54, v4
	s_and_saveexec_b64 s[2:3], s[4:5]
	s_xor_b64 s[2:3], exec, s[2:3]
	s_mov_b32 s59, s64
	s_cbranch_execz .LBB0_2628
	s_add_i32 s6, s25, 0xfffff760
	s_cmpk_gt_u32 s6, 0x7ff
	v_mov_b32_e32 v135, v129
	v_mov_b32_e32 v134, v128
	v_mov_b32_e32 v137, v127
	v_mov_b32_e32 v136, v126
	v_mov_b32_e32 v139, v133
	v_mov_b32_e32 v138, v132
	v_mov_b32_e32 v141, v131
	v_mov_b32_e32 v140, v130
	s_cbranch_scc1 .LBB0_2628
	v_mov_b32_e32 v5, v3
	v_lshl_add_u64 v[134:135], v[4:5], 2, s[16:17]
	v_lshl_add_u64 v[138:139], v[134:135], 0, s[20:21]
	v_add_co_u32_e32 v134, vcc, 0xffffe000, v134
	s_nop 1
	v_addc_co_u32_e32 v135, vcc, -1, v135, vcc
	global_load_dwordx4 v[134:137], v[134:135], off offset:-640
	s_nop 0
	global_load_dwordx4 v[138:141], v[138:139], off offset:16
	s_waitcnt vmcnt(0)
	v_mov_b64_e32 v[150:151], v[134:135]
	v_mov_b64_e32 v[152:153], v[136:137]
	v_mov_b64_e32 v[154:155], v[138:139]
	v_mov_b64_e32 v[156:157], v[140:141]
	v_add_f32_e32 v2, v130, v134
	v_add_f32_e32 v5, v126, v138
	v_add_f32_e32 v134, v131, v135
	v_add_f32_e32 v135, v127, v139
	v_add_f32_e32 v136, v132, v136
	v_add_f32_e32 v138, v128, v140
	v_add_f32_e32 v137, v133, v137
	v_add_f32_e32 v139, v129, v141
	v_mul_f32_e32 v2, 0xbfb8aa3b, v2
	v_mul_f32_e32 v5, 0xbfb8aa3b, v5
	v_mul_f32_e32 v134, 0xbfb8aa3b, v134
	v_mul_f32_e32 v135, 0xbfb8aa3b, v135
	v_mul_f32_e32 v136, 0xbfb8aa3b, v136
	v_mul_f32_e32 v138, 0xbfb8aa3b, v138
	v_mul_f32_e32 v137, 0xbfb8aa3b, v137
	v_mul_f32_e32 v139, 0xbfb8aa3b, v139
	v_exp_f32_e32 v2, v2
	v_exp_f32_e32 v5, v5
	v_exp_f32_e32 v134, v134
	v_exp_f32_e32 v135, v135
	v_exp_f32_e32 v136, v136
	v_exp_f32_e32 v138, v138
	v_exp_f32_e32 v137, v137
	v_exp_f32_e32 v139, v139
	v_add_f32_e32 v2, 1.0, v2
	v_add_f32_e32 v5, 1.0, v5
	v_add_f32_e32 v134, 1.0, v134
	v_add_f32_e32 v135, 1.0, v135
	v_add_f32_e32 v142, 1.0, v136
	v_add_f32_e32 v143, 1.0, v138
	v_add_f32_e32 v144, 1.0, v137
	v_add_f32_e32 v145, 1.0, v139
	v_rcp_f32_e32 v140, v2
	v_rcp_f32_e32 v136, v5
	v_rcp_f32_e32 v141, v134
	v_rcp_f32_e32 v137, v135
	v_rcp_f32_e32 v138, v142
	v_rcp_f32_e32 v134, v143
	v_rcp_f32_e32 v139, v144
	v_rcp_f32_e32 v135, v145
.LBB0_2628:
	s_andn2_saveexec_b64 s[2:3], s[2:3]
	v_pk_mul_f32 v[138:139], v[132:133], s[22:23] op_sel_hi:[1,0]
	v_pk_mul_f32 v[140:141], v[130:131], s[22:23] op_sel_hi:[1,0]
	v_pk_mul_f32 v[134:135], v[128:129], s[22:23] op_sel_hi:[1,0]
	v_pk_mul_f32 v[136:137], v[126:127], s[22:23] op_sel_hi:[1,0]
	s_or_b64 exec, exec, s[2:3]
	v_readlane_b32 s2, v253, 54
	s_lshl_b32 s28, s33, 8
	v_readlane_b32 s3, v253, 55
	v_add_u32_e32 v2, s28, v221
	v_ashrrev_i32_e32 v5, 31, v4
	v_mov_b64_e32 v[126:127], s[2:3]
	v_mad_i64_i32 v[126:127], s[2:3], v2, s55, v[126:127]
	v_or_b32_e32 v2, 0x80, v4
	v_cvt_pk_bf16_f32 v128, v140, v141
	v_cvt_pk_bf16_f32 v129, v138, v139
	v_cvt_pk_bf16_f32 v130, v136, v137
	v_cvt_pk_bf16_f32 v131, v134, v135
	v_lshl_add_u64 v[126:127], v[4:5], 1, v[126:127]
	v_cmp_lt_i32_e64 s[6:7], s54, v2
	global_store_dwordx4 v[126:127], v[128:131], off
	s_and_saveexec_b64 s[2:3], s[6:7]
	s_xor_b64 s[2:3], exec, s[2:3]
	s_cbranch_execz .LBB0_2633
	s_add_i32 s29, s25, 0xfffff7e0
	s_cmpk_gt_u32 s29, 0x7ff
	v_mov_b32_e32 v129, v121
	v_mov_b32_e32 v128, v120
	v_mov_b32_e32 v131, v119
	v_mov_b32_e32 v130, v118
	v_mov_b32_e32 v133, v125
	v_mov_b32_e32 v132, v124
	v_mov_b32_e32 v135, v123
	v_mov_b32_e32 v134, v122
	s_cbranch_scc1 .LBB0_2633
	v_lshl_add_u64 v[128:129], v[2:3], 2, s[16:17]
	v_lshl_add_u64 v[132:133], v[128:129], 0, s[20:21]
	v_add_co_u32_e32 v128, vcc, 0xffffe000, v128
	s_nop 1
	v_addc_co_u32_e32 v129, vcc, -1, v129, vcc
	global_load_dwordx4 v[128:131], v[128:129], off offset:-640
	s_nop 0
	global_load_dwordx4 v[132:135], v[132:133], off offset:16
	s_waitcnt vmcnt(0)
	v_mov_b64_e32 v[158:159], v[128:129]
	v_mov_b64_e32 v[160:161], v[130:131]
	v_mov_b64_e32 v[162:163], v[132:133]
	v_mov_b64_e32 v[164:165], v[134:135]
	v_add_f32_e32 v128, v122, v128
	v_add_f32_e32 v132, v118, v132
	v_add_f32_e32 v129, v123, v129
	v_add_f32_e32 v133, v119, v133
	v_add_f32_e32 v130, v124, v130
	v_add_f32_e32 v134, v120, v134
	v_add_f32_e32 v131, v125, v131
	v_add_f32_e32 v135, v121, v135
	v_mul_f32_e32 v128, 0xbfb8aa3b, v128
	v_mul_f32_e32 v132, 0xbfb8aa3b, v132
	v_mul_f32_e32 v129, 0xbfb8aa3b, v129
	v_mul_f32_e32 v133, 0xbfb8aa3b, v133
	v_mul_f32_e32 v130, 0xbfb8aa3b, v130
	v_mul_f32_e32 v134, 0xbfb8aa3b, v134
	v_mul_f32_e32 v131, 0xbfb8aa3b, v131
	v_mul_f32_e32 v135, 0xbfb8aa3b, v135
	v_exp_f32_e32 v128, v128
	v_exp_f32_e32 v132, v132
	v_exp_f32_e32 v129, v129
	v_exp_f32_e32 v133, v133
	v_exp_f32_e32 v130, v130
	v_exp_f32_e32 v134, v134
	v_exp_f32_e32 v131, v131
	v_exp_f32_e32 v135, v135
	v_add_f32_e32 v128, 1.0, v128
	v_add_f32_e32 v132, 1.0, v132
	v_add_f32_e32 v129, 1.0, v129
	v_add_f32_e32 v133, 1.0, v133
	v_add_f32_e32 v136, 1.0, v130
	v_add_f32_e32 v137, 1.0, v134
	v_add_f32_e32 v138, 1.0, v131
	v_add_f32_e32 v139, 1.0, v135
	v_rcp_f32_e32 v134, v128
	v_rcp_f32_e32 v130, v132
	v_rcp_f32_e32 v135, v129
	v_rcp_f32_e32 v131, v133
	v_rcp_f32_e32 v132, v136
	v_rcp_f32_e32 v128, v137
	v_rcp_f32_e32 v133, v138
	v_rcp_f32_e32 v129, v139
; __device__ __forceinline__ float sigmoidf_(float x) { return __builtin_amdgcn_rcpf(1.f + __expf(-x)); }
; __device__ __forceinline__ u32x4 pack8(f32x4 v0, f32x4 v1) { u32x4 w; w.x = cvt_pk_bf16(v0[0], v0[1]); w.y = cvt_pk_bf16(v0[2], v0[3]); w.z = cvt_pk_bf16(v1[0], v1[1]); w.w = cvt_pk_bf16(v1[2], v1[3]); return w; }
;     __device__ __forceinline__ void operator()(const f32x4 (&acc)[2][2][4][2], const pg8::Unit& u, int wr, int wc, int fr, int fq) const {
;     ...
;             const int row = u.pm * 256 + trow, col = u.pn * 256 + tcol;
;             if (col < C_KA) { v0 = v0 * QS_A; v1 = v1 * QS_A; }
;             else if (col >= C_GA && col < INC) { const f32x4 b0 = *(const f32x4*)(bg + col - C_GA), b1 = *(const f32x4*)(bg + col - C_GA + 4);
; #pragma unroll
;                 for (int i = 0; i < 4; ++i) { v0[i] = sigmoidf_(v0[i] + b0[i]); v1[i] = sigmoidf_(v1[i] + b1[i]); } }
;             *(u32x4*)(O + (size_t)row * INCP + col) = pg8::pack8(v0, v1);
.LBB0_2633:
	s_andn2_saveexec_b64 s[2:3], s[2:3]
	v_pk_mul_f32 v[132:133], v[124:125], s[22:23] op_sel_hi:[1,0]
	v_pk_mul_f32 v[134:135], v[122:123], s[22:23] op_sel_hi:[1,0]
	v_pk_mul_f32 v[128:129], v[120:121], s[22:23] op_sel_hi:[1,0]
	v_pk_mul_f32 v[130:131], v[118:119], s[22:23] op_sel_hi:[1,0]
	s_or_b64 exec, exec, s[2:3]
	v_cvt_pk_bf16_f32 v118, v134, v135
	v_cvt_pk_bf16_f32 v119, v132, v133
	v_cvt_pk_bf16_f32 v120, v130, v131
	v_cvt_pk_bf16_f32 v121, v128, v129
	global_store_dwordx4 v[126:127], v[118:121], off offset:256
	s_and_saveexec_b64 s[2:3], s[4:5]
	s_xor_b64 s[2:3], exec, s[2:3]
	s_cbranch_execz .LBB0_2638
	s_add_i32 s29, s25, 0xfffff760
	s_cmpk_gt_u32 s29, 0x7ff
	v_mov_b32_e32 v119, v113
	v_mov_b32_e32 v118, v112
	v_mov_b32_e32 v121, v111
	v_mov_b32_e32 v120, v110
	v_mov_b32_e32 v123, v117
	v_mov_b32_e32 v122, v116
	v_mov_b32_e32 v125, v115
	v_mov_b32_e32 v124, v114
	s_cbranch_scc1 .LBB0_2638
	v_mov_b32_e32 v118, v4
	v_mov_b32_e32 v119, v3
	v_lshl_add_u64 v[118:119], v[118:119], 2, s[16:17]
	v_lshl_add_u64 v[122:123], v[118:119], 0, s[20:21]
	v_add_co_u32_e32 v118, vcc, 0xffffe000, v118
	s_nop 1
	v_addc_co_u32_e32 v119, vcc, -1, v119, vcc
	v_mov_b64_e32 v[118:119], v[150:151]
	v_mov_b64_e32 v[120:121], v[152:153]
	s_nop 0
	v_mov_b64_e32 v[122:123], v[154:155]
	v_mov_b64_e32 v[124:125], v[156:157]
	v_add_f32_e32 v118, v114, v118
	v_add_f32_e32 v122, v110, v122
	v_add_f32_e32 v119, v115, v119
	v_add_f32_e32 v123, v111, v123
	v_add_f32_e32 v120, v116, v120
	v_add_f32_e32 v124, v112, v124
	v_add_f32_e32 v121, v117, v121
	v_add_f32_e32 v125, v113, v125
	v_mul_f32_e32 v118, 0xbfb8aa3b, v118
	v_mul_f32_e32 v122, 0xbfb8aa3b, v122
	v_mul_f32_e32 v119, 0xbfb8aa3b, v119
	v_mul_f32_e32 v123, 0xbfb8aa3b, v123
	v_mul_f32_e32 v120, 0xbfb8aa3b, v120
	v_mul_f32_e32 v124, 0xbfb8aa3b, v124
	v_mul_f32_e32 v121, 0xbfb8aa3b, v121
	v_mul_f32_e32 v125, 0xbfb8aa3b, v125
	v_exp_f32_e32 v118, v118
	v_exp_f32_e32 v122, v122
	v_exp_f32_e32 v119, v119
	v_exp_f32_e32 v123, v123
	v_exp_f32_e32 v120, v120
	v_exp_f32_e32 v124, v124
	v_exp_f32_e32 v121, v121
	v_exp_f32_e32 v125, v125
	v_add_f32_e32 v118, 1.0, v118
	v_add_f32_e32 v122, 1.0, v122
	v_add_f32_e32 v119, 1.0, v119
	v_add_f32_e32 v123, 1.0, v123
	v_add_f32_e32 v126, 1.0, v120
	v_add_f32_e32 v127, 1.0, v124
	v_add_f32_e32 v128, 1.0, v121
	v_add_f32_e32 v129, 1.0, v125
	v_rcp_f32_e32 v124, v118
	v_rcp_f32_e32 v120, v122
	v_rcp_f32_e32 v125, v119
	v_rcp_f32_e32 v121, v123
	v_rcp_f32_e32 v122, v126
	v_rcp_f32_e32 v118, v127
	v_rcp_f32_e32 v123, v128
	v_rcp_f32_e32 v119, v129
.LBB0_2638:
	s_andn2_saveexec_b64 s[2:3], s[2:3]
	v_pk_mul_f32 v[122:123], v[116:117], s[22:23] op_sel_hi:[1,0]
	v_pk_mul_f32 v[124:125], v[114:115], s[22:23] op_sel_hi:[1,0]
	v_pk_mul_f32 v[118:119], v[112:113], s[22:23] op_sel_hi:[1,0]
	v_pk_mul_f32 v[120:121], v[110:111], s[22:23] op_sel_hi:[1,0]
	s_or_b64 exec, exec, s[2:3]
	v_readlane_b32 s2, v253, 54
	v_readlane_b32 s3, v253, 55
	v_add_u32_e32 v116, s28, v224
	v_cvt_pk_bf16_f32 v112, v124, v125
	v_mov_b64_e32 v[110:111], s[2:3]
	v_mad_i64_i32 v[110:111], s[2:3], v116, s55, v[110:111]
	v_cvt_pk_bf16_f32 v113, v122, v123
	v_cvt_pk_bf16_f32 v114, v120, v121
	v_cvt_pk_bf16_f32 v115, v118, v119
	v_lshl_add_u64 v[110:111], v[4:5], 1, v[110:111]
	global_store_dwordx4 v[110:111], v[112:115], off
	s_and_saveexec_b64 s[2:3], s[6:7]
	s_xor_b64 s[2:3], exec, s[2:3]
	s_cbranch_execz .LBB0_2643
	s_add_i32 s29, s25, 0xfffff7e0
	s_cmpk_gt_u32 s29, 0x7ff
	v_mov_b32_e32 v113, v105
	v_mov_b32_e32 v112, v104
	v_mov_b32_e32 v115, v103
	v_mov_b32_e32 v114, v102
	v_mov_b32_e32 v117, v109
	v_mov_b32_e32 v116, v108
	v_mov_b32_e32 v119, v107
	v_mov_b32_e32 v118, v106
	s_cbranch_scc1 .LBB0_2643
	v_lshl_add_u64 v[112:113], v[2:3], 2, s[16:17]
	v_lshl_add_u64 v[116:117], v[112:113], 0, s[20:21]
	v_add_co_u32_e32 v112, vcc, 0xffffe000, v112
	s_nop 1
	v_addc_co_u32_e32 v113, vcc, -1, v113, vcc
	v_mov_b64_e32 v[112:113], v[158:159]
	v_mov_b64_e32 v[114:115], v[160:161]
	s_nop 0
	v_mov_b64_e32 v[116:117], v[162:163]
	v_mov_b64_e32 v[118:119], v[164:165]
	v_add_f32_e32 v112, v106, v112
	v_add_f32_e32 v116, v102, v116
	v_add_f32_e32 v113, v107, v113
	v_add_f32_e32 v117, v103, v117
	v_add_f32_e32 v114, v108, v114
	v_add_f32_e32 v118, v104, v118
	v_add_f32_e32 v115, v109, v115
	v_add_f32_e32 v119, v105, v119
	v_mul_f32_e32 v112, 0xbfb8aa3b, v112
	v_mul_f32_e32 v116, 0xbfb8aa3b, v116
	v_mul_f32_e32 v113, 0xbfb8aa3b, v113
	v_mul_f32_e32 v117, 0xbfb8aa3b, v117
	v_mul_f32_e32 v114, 0xbfb8aa3b, v114
	v_mul_f32_e32 v118, 0xbfb8aa3b, v118
	v_mul_f32_e32 v115, 0xbfb8aa3b, v115
	v_mul_f32_e32 v119, 0xbfb8aa3b, v119
	v_exp_f32_e32 v112, v112
	v_exp_f32_e32 v116, v116
	v_exp_f32_e32 v113, v113
	v_exp_f32_e32 v117, v117
	v_exp_f32_e32 v114, v114
	v_exp_f32_e32 v118, v118
	v_exp_f32_e32 v115, v115
	v_exp_f32_e32 v119, v119
	v_add_f32_e32 v112, 1.0, v112
	v_add_f32_e32 v116, 1.0, v116
	v_add_f32_e32 v113, 1.0, v113
	v_add_f32_e32 v117, 1.0, v117
	v_add_f32_e32 v120, 1.0, v114
	v_add_f32_e32 v121, 1.0, v118
	v_add_f32_e32 v122, 1.0, v115
	v_add_f32_e32 v123, 1.0, v119
	v_rcp_f32_e32 v118, v112
	v_rcp_f32_e32 v114, v116
	v_rcp_f32_e32 v119, v113
	v_rcp_f32_e32 v115, v117
	v_rcp_f32_e32 v116, v120
	v_rcp_f32_e32 v112, v121
	v_rcp_f32_e32 v117, v122
	v_rcp_f32_e32 v113, v123
; __device__ __forceinline__ float sigmoidf_(float x) { return __builtin_amdgcn_rcpf(1.f + __expf(-x)); }
; __device__ __forceinline__ u32x4 pack8(f32x4 v0, f32x4 v1) { u32x4 w; w.x = cvt_pk_bf16(v0[0], v0[1]); w.y = cvt_pk_bf16(v0[2], v0[3]); w.z = cvt_pk_bf16(v1[0], v1[1]); w.w = cvt_pk_bf16(v1[2], v1[3]); return w; }
;     __device__ __forceinline__ void operator()(const f32x4 (&acc)[2][2][4][2], const pg8::Unit& u, int wr, int wc, int fr, int fq) const {
;     ...
;             const int row = u.pm * 256 + trow, col = u.pn * 256 + tcol;
;             if (col < C_KA) { v0 = v0 * QS_A; v1 = v1 * QS_A; }
;             else if (col >= C_GA && col < INC) { const f32x4 b0 = *(const f32x4*)(bg + col - C_GA), b1 = *(const f32x4*)(bg + col - C_GA + 4);
; #pragma unroll
;                 for (int i = 0; i < 4; ++i) { v0[i] = sigmoidf_(v0[i] + b0[i]); v1[i] = sigmoidf_(v1[i] + b1[i]); } }
;             *(u32x4*)(O + (size_t)row * INCP + col) = pg8::pack8(v0, v1);
.LBB0_2643:
	s_andn2_saveexec_b64 s[2:3], s[2:3]
	v_pk_mul_f32 v[116:117], v[108:109], s[22:23] op_sel_hi:[1,0]
	v_pk_mul_f32 v[118:119], v[106:107], s[22:23] op_sel_hi:[1,0]
	v_pk_mul_f32 v[112:113], v[104:105], s[22:23] op_sel_hi:[1,0]
	v_pk_mul_f32 v[114:115], v[102:103], s[22:23] op_sel_hi:[1,0]
	s_or_b64 exec, exec, s[2:3]
	v_cvt_pk_bf16_f32 v102, v118, v119
	v_cvt_pk_bf16_f32 v103, v116, v117
	v_cvt_pk_bf16_f32 v104, v114, v115
	v_cvt_pk_bf16_f32 v105, v112, v113
	global_store_dwordx4 v[110:111], v[102:105], off offset:256
	s_and_saveexec_b64 s[2:3], s[4:5]
	s_xor_b64 s[2:3], exec, s[2:3]
	s_cbranch_execz .LBB0_2648
	s_add_i32 s29, s25, 0xfffff760
	s_cmpk_gt_u32 s29, 0x7ff
	v_mov_b32_e32 v103, v97
	v_mov_b32_e32 v102, v96
	v_mov_b32_e32 v105, v95
	v_mov_b32_e32 v104, v94
	v_mov_b32_e32 v107, v101
	v_mov_b32_e32 v106, v100
	v_mov_b32_e32 v109, v99
	v_mov_b32_e32 v108, v98
	s_cbranch_scc1 .LBB0_2648
	v_mov_b32_e32 v102, v4
	v_mov_b32_e32 v103, v3
	v_lshl_add_u64 v[102:103], v[102:103], 2, s[16:17]
	v_lshl_add_u64 v[106:107], v[102:103], 0, s[20:21]
	v_add_co_u32_e32 v102, vcc, 0xffffe000, v102
	s_nop 1
	v_addc_co_u32_e32 v103, vcc, -1, v103, vcc
	v_mov_b64_e32 v[102:103], v[150:151]
	v_mov_b64_e32 v[104:105], v[152:153]
	s_nop 0
	v_mov_b64_e32 v[106:107], v[154:155]
	v_mov_b64_e32 v[108:109], v[156:157]
	v_add_f32_e32 v102, v98, v102
	v_add_f32_e32 v106, v94, v106
	v_add_f32_e32 v103, v99, v103
	v_add_f32_e32 v107, v95, v107
	v_add_f32_e32 v104, v100, v104
	v_add_f32_e32 v108, v96, v108
	v_add_f32_e32 v105, v101, v105
	v_add_f32_e32 v109, v97, v109
	v_mul_f32_e32 v102, 0xbfb8aa3b, v102
	v_mul_f32_e32 v106, 0xbfb8aa3b, v106
	v_mul_f32_e32 v103, 0xbfb8aa3b, v103
	v_mul_f32_e32 v107, 0xbfb8aa3b, v107
	v_mul_f32_e32 v104, 0xbfb8aa3b, v104
	v_mul_f32_e32 v108, 0xbfb8aa3b, v108
	v_mul_f32_e32 v105, 0xbfb8aa3b, v105
	v_mul_f32_e32 v109, 0xbfb8aa3b, v109
	v_exp_f32_e32 v102, v102
	v_exp_f32_e32 v106, v106
	v_exp_f32_e32 v103, v103
	v_exp_f32_e32 v107, v107
	v_exp_f32_e32 v104, v104
	v_exp_f32_e32 v108, v108
	v_exp_f32_e32 v105, v105
	v_exp_f32_e32 v109, v109
	v_add_f32_e32 v102, 1.0, v102
	v_add_f32_e32 v106, 1.0, v106
	v_add_f32_e32 v103, 1.0, v103
	v_add_f32_e32 v107, 1.0, v107
	v_add_f32_e32 v110, 1.0, v104
	v_add_f32_e32 v111, 1.0, v108
	v_add_f32_e32 v112, 1.0, v105
	v_add_f32_e32 v113, 1.0, v109
	v_rcp_f32_e32 v108, v102
	v_rcp_f32_e32 v104, v106
	v_rcp_f32_e32 v109, v103
	v_rcp_f32_e32 v105, v107
	v_rcp_f32_e32 v106, v110
	v_rcp_f32_e32 v102, v111
	v_rcp_f32_e32 v107, v112
	v_rcp_f32_e32 v103, v113
.LBB0_2648:
	s_andn2_saveexec_b64 s[2:3], s[2:3]
	v_pk_mul_f32 v[106:107], v[100:101], s[22:23] op_sel_hi:[1,0]
	v_pk_mul_f32 v[108:109], v[98:99], s[22:23] op_sel_hi:[1,0]
	v_pk_mul_f32 v[102:103], v[96:97], s[22:23] op_sel_hi:[1,0]
	v_pk_mul_f32 v[104:105], v[94:95], s[22:23] op_sel_hi:[1,0]
	s_or_b64 exec, exec, s[2:3]
	v_readlane_b32 s2, v253, 54
	v_readlane_b32 s3, v253, 55
	v_add_u32_e32 v100, s28, v225
	v_cvt_pk_bf16_f32 v96, v108, v109
	v_mov_b64_e32 v[94:95], s[2:3]
	v_mad_i64_i32 v[94:95], s[2:3], v100, s55, v[94:95]
	v_cvt_pk_bf16_f32 v97, v106, v107
	v_cvt_pk_bf16_f32 v98, v104, v105
	v_cvt_pk_bf16_f32 v99, v102, v103
	v_lshl_add_u64 v[94:95], v[4:5], 1, v[94:95]
	global_store_dwordx4 v[94:95], v[96:99], off
	s_and_saveexec_b64 s[2:3], s[6:7]
	s_xor_b64 s[2:3], exec, s[2:3]
	s_cbranch_execz .LBB0_2653
	s_add_i32 s29, s25, 0xfffff7e0
	s_cmpk_gt_u32 s29, 0x7ff
	v_mov_b32_e32 v97, v89
	v_mov_b32_e32 v96, v88
	v_mov_b32_e32 v99, v87
	v_mov_b32_e32 v98, v86
	v_mov_b32_e32 v101, v93
	v_mov_b32_e32 v100, v92
	v_mov_b32_e32 v103, v91
	v_mov_b32_e32 v102, v90
	s_cbranch_scc1 .LBB0_2653
	v_lshl_add_u64 v[96:97], v[2:3], 2, s[16:17]
	v_lshl_add_u64 v[100:101], v[96:97], 0, s[20:21]
	v_add_co_u32_e32 v96, vcc, 0xffffe000, v96
	s_nop 1
	v_addc_co_u32_e32 v97, vcc, -1, v97, vcc
	v_mov_b64_e32 v[96:97], v[158:159]
	v_mov_b64_e32 v[98:99], v[160:161]
	s_nop 0
	v_mov_b64_e32 v[100:101], v[162:163]
	v_mov_b64_e32 v[102:103], v[164:165]
	v_add_f32_e32 v96, v90, v96
	v_add_f32_e32 v100, v86, v100
	v_add_f32_e32 v97, v91, v97
	v_add_f32_e32 v101, v87, v101
	v_add_f32_e32 v98, v92, v98
	v_add_f32_e32 v102, v88, v102
	v_add_f32_e32 v99, v93, v99
	v_add_f32_e32 v103, v89, v103
	v_mul_f32_e32 v96, 0xbfb8aa3b, v96
	v_mul_f32_e32 v100, 0xbfb8aa3b, v100
	v_mul_f32_e32 v97, 0xbfb8aa3b, v97
	v_mul_f32_e32 v101, 0xbfb8aa3b, v101
	v_mul_f32_e32 v98, 0xbfb8aa3b, v98
	v_mul_f32_e32 v102, 0xbfb8aa3b, v102
	v_mul_f32_e32 v99, 0xbfb8aa3b, v99
	v_mul_f32_e32 v103, 0xbfb8aa3b, v103
	v_exp_f32_e32 v96, v96
	v_exp_f32_e32 v100, v100
	v_exp_f32_e32 v97, v97
	v_exp_f32_e32 v101, v101
	v_exp_f32_e32 v98, v98
	v_exp_f32_e32 v102, v102
	v_exp_f32_e32 v99, v99
	v_exp_f32_e32 v103, v103
	v_add_f32_e32 v96, 1.0, v96
	v_add_f32_e32 v100, 1.0, v100
	v_add_f32_e32 v97, 1.0, v97
	v_add_f32_e32 v101, 1.0, v101
	v_add_f32_e32 v104, 1.0, v98
	v_add_f32_e32 v105, 1.0, v102
	v_add_f32_e32 v106, 1.0, v99
	v_add_f32_e32 v107, 1.0, v103
	v_rcp_f32_e32 v102, v96
	v_rcp_f32_e32 v98, v100
	v_rcp_f32_e32 v103, v97
	v_rcp_f32_e32 v99, v101
	v_rcp_f32_e32 v100, v104
	v_rcp_f32_e32 v96, v105
	v_rcp_f32_e32 v101, v106
	v_rcp_f32_e32 v97, v107
; __device__ __forceinline__ float sigmoidf_(float x) { return __builtin_amdgcn_rcpf(1.f + __expf(-x)); }
; __device__ __forceinline__ u32x4 pack8(f32x4 v0, f32x4 v1) { u32x4 w; w.x = cvt_pk_bf16(v0[0], v0[1]); w.y = cvt_pk_bf16(v0[2], v0[3]); w.z = cvt_pk_bf16(v1[0], v1[1]); w.w = cvt_pk_bf16(v1[2], v1[3]); return w; }
;     __device__ __forceinline__ void operator()(const f32x4 (&acc)[2][2][4][2], const pg8::Unit& u, int wr, int wc, int fr, int fq) const {
;     ...
;             const int row = u.pm * 256 + trow, col = u.pn * 256 + tcol;
;             if (col < C_KA) { v0 = v0 * QS_A; v1 = v1 * QS_A; }
;             else if (col >= C_GA && col < INC) { const f32x4 b0 = *(const f32x4*)(bg + col - C_GA), b1 = *(const f32x4*)(bg + col - C_GA + 4);
; #pragma unroll
;                 for (int i = 0; i < 4; ++i) { v0[i] = sigmoidf_(v0[i] + b0[i]); v1[i] = sigmoidf_(v1[i] + b1[i]); } }
;             *(u32x4*)(O + (size_t)row * INCP + col) = pg8::pack8(v0, v1);
.LBB0_2653:
	s_andn2_saveexec_b64 s[2:3], s[2:3]
	v_pk_mul_f32 v[100:101], v[92:93], s[22:23] op_sel_hi:[1,0]
	v_pk_mul_f32 v[102:103], v[90:91], s[22:23] op_sel_hi:[1,0]
	v_pk_mul_f32 v[96:97], v[88:89], s[22:23] op_sel_hi:[1,0]
	v_pk_mul_f32 v[98:99], v[86:87], s[22:23] op_sel_hi:[1,0]
	s_or_b64 exec, exec, s[2:3]
	v_cvt_pk_bf16_f32 v86, v102, v103
	v_cvt_pk_bf16_f32 v87, v100, v101
	v_cvt_pk_bf16_f32 v88, v98, v99
	v_cvt_pk_bf16_f32 v89, v96, v97
	global_store_dwordx4 v[94:95], v[86:89], off offset:256
	s_and_saveexec_b64 s[2:3], s[4:5]
	s_xor_b64 s[2:3], exec, s[2:3]
	s_cbranch_execz .LBB0_2658
	s_add_i32 s29, s25, 0xfffff760
	s_cmpk_gt_u32 s29, 0x7ff
	v_mov_b32_e32 v87, v81
	v_mov_b32_e32 v86, v80
	v_mov_b32_e32 v89, v79
	v_mov_b32_e32 v88, v78
	v_mov_b32_e32 v91, v85
	v_mov_b32_e32 v90, v84
	v_mov_b32_e32 v93, v83
	v_mov_b32_e32 v92, v82
	s_cbranch_scc1 .LBB0_2658
	v_mov_b32_e32 v86, v4
	v_mov_b32_e32 v87, v3
	v_lshl_add_u64 v[86:87], v[86:87], 2, s[16:17]
	v_lshl_add_u64 v[90:91], v[86:87], 0, s[20:21]
	v_add_co_u32_e32 v86, vcc, 0xffffe000, v86
	s_nop 1
	v_addc_co_u32_e32 v87, vcc, -1, v87, vcc
	v_mov_b64_e32 v[86:87], v[150:151]
	v_mov_b64_e32 v[88:89], v[152:153]
	s_nop 0
	v_mov_b64_e32 v[90:91], v[154:155]
	v_mov_b64_e32 v[92:93], v[156:157]
	v_add_f32_e32 v86, v82, v86
	v_add_f32_e32 v90, v78, v90
	v_add_f32_e32 v87, v83, v87
	v_add_f32_e32 v91, v79, v91
	v_add_f32_e32 v88, v84, v88
	v_add_f32_e32 v92, v80, v92
	v_add_f32_e32 v89, v85, v89
	v_add_f32_e32 v93, v81, v93
	v_mul_f32_e32 v86, 0xbfb8aa3b, v86
	v_mul_f32_e32 v90, 0xbfb8aa3b, v90
	v_mul_f32_e32 v87, 0xbfb8aa3b, v87
	v_mul_f32_e32 v91, 0xbfb8aa3b, v91
	v_mul_f32_e32 v88, 0xbfb8aa3b, v88
	v_mul_f32_e32 v92, 0xbfb8aa3b, v92
	v_mul_f32_e32 v89, 0xbfb8aa3b, v89
	v_mul_f32_e32 v93, 0xbfb8aa3b, v93
	v_exp_f32_e32 v86, v86
	v_exp_f32_e32 v90, v90
	v_exp_f32_e32 v87, v87
	v_exp_f32_e32 v91, v91
	v_exp_f32_e32 v88, v88
	v_exp_f32_e32 v92, v92
	v_exp_f32_e32 v89, v89
	v_exp_f32_e32 v93, v93
	v_add_f32_e32 v86, 1.0, v86
	v_add_f32_e32 v90, 1.0, v90
	v_add_f32_e32 v87, 1.0, v87
	v_add_f32_e32 v91, 1.0, v91
	v_add_f32_e32 v94, 1.0, v88
	v_add_f32_e32 v95, 1.0, v92
	v_add_f32_e32 v96, 1.0, v89
	v_add_f32_e32 v97, 1.0, v93
	v_rcp_f32_e32 v92, v86
	v_rcp_f32_e32 v88, v90
	v_rcp_f32_e32 v93, v87
	v_rcp_f32_e32 v89, v91
	v_rcp_f32_e32 v90, v94
	v_rcp_f32_e32 v86, v95
	v_rcp_f32_e32 v91, v96
	v_rcp_f32_e32 v87, v97
.LBB0_2658:
	s_andn2_saveexec_b64 s[2:3], s[2:3]
	v_pk_mul_f32 v[90:91], v[84:85], s[22:23] op_sel_hi:[1,0]
	v_pk_mul_f32 v[92:93], v[82:83], s[22:23] op_sel_hi:[1,0]
	v_pk_mul_f32 v[86:87], v[80:81], s[22:23] op_sel_hi:[1,0]
	v_pk_mul_f32 v[88:89], v[78:79], s[22:23] op_sel_hi:[1,0]
	s_or_b64 exec, exec, s[2:3]
	v_readlane_b32 s2, v253, 54
	v_readlane_b32 s3, v253, 55
	v_add_u32_e32 v84, s28, v226
	v_cvt_pk_bf16_f32 v80, v92, v93
	v_mov_b64_e32 v[78:79], s[2:3]
	v_mad_i64_i32 v[78:79], s[2:3], v84, s55, v[78:79]
	v_cvt_pk_bf16_f32 v81, v90, v91
	v_cvt_pk_bf16_f32 v82, v88, v89
	v_cvt_pk_bf16_f32 v83, v86, v87
	v_lshl_add_u64 v[78:79], v[4:5], 1, v[78:79]
	global_store_dwordx4 v[78:79], v[80:83], off
	s_and_saveexec_b64 s[2:3], s[6:7]
	s_xor_b64 s[2:3], exec, s[2:3]
	s_cbranch_execz .LBB0_2663
	s_add_i32 s29, s25, 0xfffff7e0
	s_cmpk_gt_u32 s29, 0x7ff
	v_mov_b32_e32 v81, v73
	v_mov_b32_e32 v80, v72
	v_mov_b32_e32 v83, v71
	v_mov_b32_e32 v82, v70
	v_mov_b32_e32 v85, v77
	v_mov_b32_e32 v84, v76
	v_mov_b32_e32 v87, v75
	v_mov_b32_e32 v86, v74
	s_cbranch_scc1 .LBB0_2663
	v_lshl_add_u64 v[80:81], v[2:3], 2, s[16:17]
	v_lshl_add_u64 v[84:85], v[80:81], 0, s[20:21]
	v_add_co_u32_e32 v80, vcc, 0xffffe000, v80
	s_nop 1
	v_addc_co_u32_e32 v81, vcc, -1, v81, vcc
	v_mov_b64_e32 v[80:81], v[158:159]
	v_mov_b64_e32 v[82:83], v[160:161]
	s_nop 0
	v_mov_b64_e32 v[84:85], v[162:163]
	v_mov_b64_e32 v[86:87], v[164:165]
	v_add_f32_e32 v80, v74, v80
	v_add_f32_e32 v84, v70, v84
	v_add_f32_e32 v81, v75, v81
	v_add_f32_e32 v85, v71, v85
	v_add_f32_e32 v82, v76, v82
	v_add_f32_e32 v86, v72, v86
	v_add_f32_e32 v83, v77, v83
	v_add_f32_e32 v87, v73, v87
	v_mul_f32_e32 v80, 0xbfb8aa3b, v80
	v_mul_f32_e32 v84, 0xbfb8aa3b, v84
	v_mul_f32_e32 v81, 0xbfb8aa3b, v81
	v_mul_f32_e32 v85, 0xbfb8aa3b, v85
	v_mul_f32_e32 v82, 0xbfb8aa3b, v82
	v_mul_f32_e32 v86, 0xbfb8aa3b, v86
	v_mul_f32_e32 v83, 0xbfb8aa3b, v83
	v_mul_f32_e32 v87, 0xbfb8aa3b, v87
	v_exp_f32_e32 v80, v80
	v_exp_f32_e32 v84, v84
	v_exp_f32_e32 v81, v81
	v_exp_f32_e32 v85, v85
	v_exp_f32_e32 v82, v82
	v_exp_f32_e32 v86, v86
	v_exp_f32_e32 v83, v83
	v_exp_f32_e32 v87, v87
	v_add_f32_e32 v80, 1.0, v80
	v_add_f32_e32 v84, 1.0, v84
	v_add_f32_e32 v81, 1.0, v81
	v_add_f32_e32 v85, 1.0, v85
	v_add_f32_e32 v88, 1.0, v82
	v_add_f32_e32 v89, 1.0, v86
	v_add_f32_e32 v90, 1.0, v83
	v_add_f32_e32 v91, 1.0, v87
	v_rcp_f32_e32 v86, v80
	v_rcp_f32_e32 v82, v84
	v_rcp_f32_e32 v87, v81
	v_rcp_f32_e32 v83, v85
	v_rcp_f32_e32 v84, v88
	v_rcp_f32_e32 v80, v89
	v_rcp_f32_e32 v85, v90
	v_rcp_f32_e32 v81, v91
; __device__ __forceinline__ float sigmoidf_(float x) { return __builtin_amdgcn_rcpf(1.f + __expf(-x)); }
; __device__ __forceinline__ u32x4 pack8(f32x4 v0, f32x4 v1) { u32x4 w; w.x = cvt_pk_bf16(v0[0], v0[1]); w.y = cvt_pk_bf16(v0[2], v0[3]); w.z = cvt_pk_bf16(v1[0], v1[1]); w.w = cvt_pk_bf16(v1[2], v1[3]); return w; }
;     __device__ __forceinline__ void operator()(const f32x4 (&acc)[2][2][4][2], const pg8::Unit& u, int wr, int wc, int fr, int fq) const {
;     ...
;             const int row = u.pm * 256 + trow, col = u.pn * 256 + tcol;
;             if (col < C_KA) { v0 = v0 * QS_A; v1 = v1 * QS_A; }
;             else if (col >= C_GA && col < INC) { const f32x4 b0 = *(const f32x4*)(bg + col - C_GA), b1 = *(const f32x4*)(bg + col - C_GA + 4);
; #pragma unroll
;                 for (int i = 0; i < 4; ++i) { v0[i] = sigmoidf_(v0[i] + b0[i]); v1[i] = sigmoidf_(v1[i] + b1[i]); } }
;             *(u32x4*)(O + (size_t)row * INCP + col) = pg8::pack8(v0, v1);
.LBB0_2663:
	s_andn2_saveexec_b64 s[2:3], s[2:3]
	v_pk_mul_f32 v[84:85], v[76:77], s[22:23] op_sel_hi:[1,0]
	v_pk_mul_f32 v[86:87], v[74:75], s[22:23] op_sel_hi:[1,0]
	v_pk_mul_f32 v[80:81], v[72:73], s[22:23] op_sel_hi:[1,0]
	v_pk_mul_f32 v[82:83], v[70:71], s[22:23] op_sel_hi:[1,0]
	s_or_b64 exec, exec, s[2:3]
	v_cvt_pk_bf16_f32 v70, v86, v87
	v_cvt_pk_bf16_f32 v71, v84, v85
	v_cvt_pk_bf16_f32 v72, v82, v83
	v_cvt_pk_bf16_f32 v73, v80, v81
	global_store_dwordx4 v[78:79], v[70:73], off offset:256
	s_and_saveexec_b64 s[2:3], s[4:5]
	s_xor_b64 s[2:3], exec, s[2:3]
	s_cbranch_execz .LBB0_2668
	s_add_i32 s29, s25, 0xfffff760
	v_mov_b64_e32 v[76:77], v[64:65]
	v_mov_b64_e32 v[72:73], v[68:69]
	s_cmpk_gt_u32 s29, 0x7ff
	v_mov_b64_e32 v[74:75], v[62:63]
	v_mov_b64_e32 v[70:71], v[66:67]
	s_cbranch_scc1 .LBB0_2668
	v_mov_b32_e32 v70, v4
	v_mov_b32_e32 v71, v3
	v_lshl_add_u64 v[70:71], v[70:71], 2, s[16:17]
	v_lshl_add_u64 v[74:75], v[70:71], 0, s[20:21]
	v_add_co_u32_e32 v70, vcc, 0xffffe000, v70
	s_nop 1
	v_addc_co_u32_e32 v71, vcc, -1, v71, vcc
	v_mov_b64_e32 v[70:71], v[150:151]
	v_mov_b64_e32 v[72:73], v[152:153]
	s_nop 0
	v_mov_b64_e32 v[74:75], v[154:155]
	v_mov_b64_e32 v[76:77], v[156:157]
	v_add_f32_e32 v70, v66, v70
	v_add_f32_e32 v74, v62, v74
	v_add_f32_e32 v71, v67, v71
	v_add_f32_e32 v75, v63, v75
	v_add_f32_e32 v72, v68, v72
	v_add_f32_e32 v76, v64, v76
	v_add_f32_e32 v73, v69, v73
	v_add_f32_e32 v77, v65, v77
	v_mul_f32_e32 v70, 0xbfb8aa3b, v70
	v_mul_f32_e32 v74, 0xbfb8aa3b, v74
	v_mul_f32_e32 v71, 0xbfb8aa3b, v71
	v_mul_f32_e32 v75, 0xbfb8aa3b, v75
	v_mul_f32_e32 v72, 0xbfb8aa3b, v72
	v_mul_f32_e32 v76, 0xbfb8aa3b, v76
	v_mul_f32_e32 v73, 0xbfb8aa3b, v73
	v_mul_f32_e32 v77, 0xbfb8aa3b, v77
	v_exp_f32_e32 v70, v70
	v_exp_f32_e32 v74, v74
	v_exp_f32_e32 v71, v71
	v_exp_f32_e32 v75, v75
	v_exp_f32_e32 v72, v72
	v_exp_f32_e32 v76, v76
	v_exp_f32_e32 v73, v73
	v_exp_f32_e32 v77, v77
	v_add_f32_e32 v70, 1.0, v70
	v_add_f32_e32 v74, 1.0, v74
	v_add_f32_e32 v71, 1.0, v71
	v_add_f32_e32 v75, 1.0, v75
	v_add_f32_e32 v72, 1.0, v72
	v_add_f32_e32 v76, 1.0, v76
	v_add_f32_e32 v73, 1.0, v73
	v_add_f32_e32 v77, 1.0, v77
	v_rcp_f32_e32 v70, v70
	v_rcp_f32_e32 v74, v74
	v_rcp_f32_e32 v71, v71
	v_rcp_f32_e32 v75, v75
	v_rcp_f32_e32 v72, v72
	v_rcp_f32_e32 v76, v76
	v_rcp_f32_e32 v73, v73
	v_rcp_f32_e32 v77, v77
.LBB0_2668:
	s_andn2_saveexec_b64 s[2:3], s[2:3]
	v_pk_mul_f32 v[72:73], v[68:69], s[22:23] op_sel_hi:[1,0]
	v_pk_mul_f32 v[70:71], v[66:67], s[22:23] op_sel_hi:[1,0]
	v_pk_mul_f32 v[76:77], v[64:65], s[22:23] op_sel_hi:[1,0]
	v_pk_mul_f32 v[74:75], v[62:63], s[22:23] op_sel_hi:[1,0]
	s_or_b64 exec, exec, s[2:3]
	v_readlane_b32 s2, v253, 54
	v_readlane_b32 s3, v253, 55
	v_add_u32_e32 v68, s28, v227
	v_cvt_pk_bf16_f32 v62, v70, v71
	v_mov_b64_e32 v[66:67], s[2:3]
	v_mad_i64_i32 v[66:67], s[2:3], v68, s55, v[66:67]
	v_cvt_pk_bf16_f32 v63, v72, v73
	v_cvt_pk_bf16_f32 v64, v74, v75
	v_cvt_pk_bf16_f32 v65, v76, v77
	v_lshl_add_u64 v[70:71], v[4:5], 1, v[66:67]
	global_store_dwordx4 v[70:71], v[62:65], off
	s_and_saveexec_b64 s[2:3], s[6:7]
	s_xor_b64 s[2:3], exec, s[2:3]
	s_cbranch_execz .LBB0_2673
	s_add_i32 s29, s25, 0xfffff7e0
	v_mov_b64_e32 v[68:69], v[56:57]
	v_mov_b64_e32 v[64:65], v[60:61]
	s_cmpk_gt_u32 s29, 0x7ff
	v_mov_b64_e32 v[66:67], v[54:55]
	v_mov_b64_e32 v[62:63], v[58:59]
	s_cbranch_scc1 .LBB0_2673
	v_lshl_add_u64 v[62:63], v[2:3], 2, s[16:17]
	v_lshl_add_u64 v[66:67], v[62:63], 0, s[20:21]
	v_add_co_u32_e32 v62, vcc, 0xffffe000, v62
	s_nop 1
	v_addc_co_u32_e32 v63, vcc, -1, v63, vcc
	v_mov_b64_e32 v[62:63], v[158:159]
	v_mov_b64_e32 v[64:65], v[160:161]
	s_nop 0
	v_mov_b64_e32 v[66:67], v[162:163]
	v_mov_b64_e32 v[68:69], v[164:165]
	v_add_f32_e32 v62, v58, v62
	v_add_f32_e32 v66, v54, v66
	v_add_f32_e32 v63, v59, v63
	v_add_f32_e32 v67, v55, v67
	v_add_f32_e32 v64, v60, v64
	v_add_f32_e32 v68, v56, v68
	v_add_f32_e32 v65, v61, v65
	v_add_f32_e32 v69, v57, v69
	v_mul_f32_e32 v62, 0xbfb8aa3b, v62
	v_mul_f32_e32 v66, 0xbfb8aa3b, v66
	v_mul_f32_e32 v63, 0xbfb8aa3b, v63
	v_mul_f32_e32 v67, 0xbfb8aa3b, v67
	v_mul_f32_e32 v64, 0xbfb8aa3b, v64
	v_mul_f32_e32 v68, 0xbfb8aa3b, v68
	v_mul_f32_e32 v65, 0xbfb8aa3b, v65
	v_mul_f32_e32 v69, 0xbfb8aa3b, v69
	v_exp_f32_e32 v62, v62
	v_exp_f32_e32 v66, v66
	v_exp_f32_e32 v63, v63
	v_exp_f32_e32 v67, v67
	v_exp_f32_e32 v64, v64
	v_exp_f32_e32 v68, v68
	v_exp_f32_e32 v65, v65
	v_exp_f32_e32 v69, v69
	v_add_f32_e32 v62, 1.0, v62
	v_add_f32_e32 v66, 1.0, v66
	v_add_f32_e32 v63, 1.0, v63
	v_add_f32_e32 v67, 1.0, v67
	v_add_f32_e32 v64, 1.0, v64
	v_add_f32_e32 v68, 1.0, v68
	v_add_f32_e32 v65, 1.0, v65
	v_add_f32_e32 v69, 1.0, v69
	v_rcp_f32_e32 v62, v62
	v_rcp_f32_e32 v66, v66
	v_rcp_f32_e32 v63, v63
	v_rcp_f32_e32 v67, v67
	v_rcp_f32_e32 v64, v64
	v_rcp_f32_e32 v68, v68
	v_rcp_f32_e32 v65, v65
	v_rcp_f32_e32 v69, v69
; __device__ __forceinline__ float sigmoidf_(float x) { return __builtin_amdgcn_rcpf(1.f + __expf(-x)); }
; __device__ __forceinline__ u32x4 pack8(f32x4 v0, f32x4 v1) { u32x4 w; w.x = cvt_pk_bf16(v0[0], v0[1]); w.y = cvt_pk_bf16(v0[2], v0[3]); w.z = cvt_pk_bf16(v1[0], v1[1]); w.w = cvt_pk_bf16(v1[2], v1[3]); return w; }
;     __device__ __forceinline__ void operator()(const f32x4 (&acc)[2][2][4][2], const pg8::Unit& u, int wr, int wc, int fr, int fq) const {
;     ...
;             const int row = u.pm * 256 + trow, col = u.pn * 256 + tcol;
;             if (col < C_KA) { v0 = v0 * QS_A; v1 = v1 * QS_A; }
;             else if (col >= C_GA && col < INC) { const f32x4 b0 = *(const f32x4*)(bg + col - C_GA), b1 = *(const f32x4*)(bg + col - C_GA + 4);
; #pragma unroll
;                 for (int i = 0; i < 4; ++i) { v0[i] = sigmoidf_(v0[i] + b0[i]); v1[i] = sigmoidf_(v1[i] + b1[i]); } }
;             *(u32x4*)(O + (size_t)row * INCP + col) = pg8::pack8(v0, v1);
.LBB0_2673:
	s_andn2_saveexec_b64 s[2:3], s[2:3]
	v_pk_mul_f32 v[64:65], v[60:61], s[22:23] op_sel_hi:[1,0]
	v_pk_mul_f32 v[62:63], v[58:59], s[22:23] op_sel_hi:[1,0]
	v_pk_mul_f32 v[68:69], v[56:57], s[22:23] op_sel_hi:[1,0]
	v_pk_mul_f32 v[66:67], v[54:55], s[22:23] op_sel_hi:[1,0]
	s_or_b64 exec, exec, s[2:3]
	v_cvt_pk_bf16_f32 v54, v62, v63
	v_cvt_pk_bf16_f32 v55, v64, v65
	v_cvt_pk_bf16_f32 v56, v66, v67
	v_cvt_pk_bf16_f32 v57, v68, v69
	global_store_dwordx4 v[70:71], v[54:57], off offset:256
	s_and_saveexec_b64 s[2:3], s[4:5]
	s_xor_b64 s[2:3], exec, s[2:3]
	s_cbranch_execz .LBB0_2678
	s_add_i32 s29, s25, 0xfffff760
	v_mov_b64_e32 v[60:61], v[48:49]
	v_mov_b64_e32 v[56:57], v[52:53]
	s_cmpk_gt_u32 s29, 0x7ff
	v_mov_b64_e32 v[58:59], v[46:47]
	v_mov_b64_e32 v[54:55], v[50:51]
	s_cbranch_scc1 .LBB0_2678
	v_mov_b32_e32 v54, v4
	v_mov_b32_e32 v55, v3
	v_lshl_add_u64 v[54:55], v[54:55], 2, s[16:17]
	v_lshl_add_u64 v[58:59], v[54:55], 0, s[20:21]
	v_add_co_u32_e32 v54, vcc, 0xffffe000, v54
	s_nop 1
	v_addc_co_u32_e32 v55, vcc, -1, v55, vcc
	v_mov_b64_e32 v[54:55], v[150:151]
	v_mov_b64_e32 v[56:57], v[152:153]
	s_nop 0
	v_mov_b64_e32 v[58:59], v[154:155]
	v_mov_b64_e32 v[60:61], v[156:157]
	v_add_f32_e32 v54, v50, v54
	v_add_f32_e32 v58, v46, v58
	v_add_f32_e32 v55, v51, v55
	v_add_f32_e32 v59, v47, v59
	v_add_f32_e32 v56, v52, v56
	v_add_f32_e32 v60, v48, v60
	v_add_f32_e32 v57, v53, v57
	v_add_f32_e32 v61, v49, v61
	v_mul_f32_e32 v54, 0xbfb8aa3b, v54
	v_mul_f32_e32 v58, 0xbfb8aa3b, v58
	v_mul_f32_e32 v55, 0xbfb8aa3b, v55
	v_mul_f32_e32 v59, 0xbfb8aa3b, v59
	v_mul_f32_e32 v56, 0xbfb8aa3b, v56
	v_mul_f32_e32 v60, 0xbfb8aa3b, v60
	v_mul_f32_e32 v57, 0xbfb8aa3b, v57
	v_mul_f32_e32 v61, 0xbfb8aa3b, v61
	v_exp_f32_e32 v54, v54
	v_exp_f32_e32 v58, v58
	v_exp_f32_e32 v55, v55
	v_exp_f32_e32 v59, v59
	v_exp_f32_e32 v56, v56
	v_exp_f32_e32 v60, v60
	v_exp_f32_e32 v57, v57
	v_exp_f32_e32 v61, v61
	v_add_f32_e32 v54, 1.0, v54
	v_add_f32_e32 v58, 1.0, v58
	v_add_f32_e32 v55, 1.0, v55
	v_add_f32_e32 v59, 1.0, v59
	v_add_f32_e32 v56, 1.0, v56
	v_add_f32_e32 v60, 1.0, v60
	v_add_f32_e32 v57, 1.0, v57
	v_add_f32_e32 v61, 1.0, v61
	v_rcp_f32_e32 v54, v54
	v_rcp_f32_e32 v58, v58
	v_rcp_f32_e32 v55, v55
	v_rcp_f32_e32 v59, v59
	v_rcp_f32_e32 v56, v56
	v_rcp_f32_e32 v60, v60
	v_rcp_f32_e32 v57, v57
	v_rcp_f32_e32 v61, v61
.LBB0_2678:
	s_andn2_saveexec_b64 s[2:3], s[2:3]
	v_pk_mul_f32 v[56:57], v[52:53], s[22:23] op_sel_hi:[1,0]
	v_pk_mul_f32 v[54:55], v[50:51], s[22:23] op_sel_hi:[1,0]
	v_pk_mul_f32 v[60:61], v[48:49], s[22:23] op_sel_hi:[1,0]
	v_pk_mul_f32 v[58:59], v[46:47], s[22:23] op_sel_hi:[1,0]
	s_or_b64 exec, exec, s[2:3]
	v_readlane_b32 s2, v253, 54
	v_readlane_b32 s3, v253, 55
	v_add_u32_e32 v52, s28, v228
	v_cvt_pk_bf16_f32 v46, v54, v55
	v_mov_b64_e32 v[50:51], s[2:3]
	v_mad_i64_i32 v[50:51], s[2:3], v52, s55, v[50:51]
	v_cvt_pk_bf16_f32 v47, v56, v57
	v_cvt_pk_bf16_f32 v48, v58, v59
	v_cvt_pk_bf16_f32 v49, v60, v61
	v_lshl_add_u64 v[54:55], v[4:5], 1, v[50:51]
	global_store_dwordx4 v[54:55], v[46:49], off
	s_and_saveexec_b64 s[2:3], s[6:7]
	s_xor_b64 s[2:3], exec, s[2:3]
	s_cbranch_execz .LBB0_2683
	s_add_i32 s29, s25, 0xfffff7e0
	v_mov_b64_e32 v[52:53], v[40:41]
	v_mov_b64_e32 v[48:49], v[44:45]
	s_cmpk_gt_u32 s29, 0x7ff
	v_mov_b64_e32 v[50:51], v[38:39]
	v_mov_b64_e32 v[46:47], v[42:43]
	s_cbranch_scc1 .LBB0_2683
	v_lshl_add_u64 v[46:47], v[2:3], 2, s[16:17]
	v_lshl_add_u64 v[50:51], v[46:47], 0, s[20:21]
	v_add_co_u32_e32 v46, vcc, 0xffffe000, v46
	s_nop 1
	v_addc_co_u32_e32 v47, vcc, -1, v47, vcc
	v_mov_b64_e32 v[46:47], v[158:159]
	v_mov_b64_e32 v[48:49], v[160:161]
	s_nop 0
	v_mov_b64_e32 v[50:51], v[162:163]
	v_mov_b64_e32 v[52:53], v[164:165]
	v_add_f32_e32 v46, v42, v46
	v_add_f32_e32 v50, v38, v50
	v_add_f32_e32 v47, v43, v47
	v_add_f32_e32 v51, v39, v51
	v_add_f32_e32 v48, v44, v48
	v_add_f32_e32 v52, v40, v52
	v_add_f32_e32 v49, v45, v49
	v_add_f32_e32 v53, v41, v53
	v_mul_f32_e32 v46, 0xbfb8aa3b, v46
	v_mul_f32_e32 v50, 0xbfb8aa3b, v50
	v_mul_f32_e32 v47, 0xbfb8aa3b, v47
	v_mul_f32_e32 v51, 0xbfb8aa3b, v51
	v_mul_f32_e32 v48, 0xbfb8aa3b, v48
	v_mul_f32_e32 v52, 0xbfb8aa3b, v52
	v_mul_f32_e32 v49, 0xbfb8aa3b, v49
	v_mul_f32_e32 v53, 0xbfb8aa3b, v53
	v_exp_f32_e32 v46, v46
	v_exp_f32_e32 v50, v50
	v_exp_f32_e32 v47, v47
	v_exp_f32_e32 v51, v51
	v_exp_f32_e32 v48, v48
	v_exp_f32_e32 v52, v52
	v_exp_f32_e32 v49, v49
	v_exp_f32_e32 v53, v53
	v_add_f32_e32 v46, 1.0, v46
	v_add_f32_e32 v50, 1.0, v50
	v_add_f32_e32 v47, 1.0, v47
	v_add_f32_e32 v51, 1.0, v51
	v_add_f32_e32 v48, 1.0, v48
	v_add_f32_e32 v52, 1.0, v52
	v_add_f32_e32 v49, 1.0, v49
	v_add_f32_e32 v53, 1.0, v53
	v_rcp_f32_e32 v46, v46
	v_rcp_f32_e32 v50, v50
	v_rcp_f32_e32 v47, v47
	v_rcp_f32_e32 v51, v51
	v_rcp_f32_e32 v48, v48
	v_rcp_f32_e32 v52, v52
	v_rcp_f32_e32 v49, v49
	v_rcp_f32_e32 v53, v53
; __device__ __forceinline__ float sigmoidf_(float x) { return __builtin_amdgcn_rcpf(1.f + __expf(-x)); }
; __device__ __forceinline__ u32x4 pack8(f32x4 v0, f32x4 v1) { u32x4 w; w.x = cvt_pk_bf16(v0[0], v0[1]); w.y = cvt_pk_bf16(v0[2], v0[3]); w.z = cvt_pk_bf16(v1[0], v1[1]); w.w = cvt_pk_bf16(v1[2], v1[3]); return w; }
;     __device__ __forceinline__ void operator()(const f32x4 (&acc)[2][2][4][2], const pg8::Unit& u, int wr, int wc, int fr, int fq) const {
;     ...
;             const int row = u.pm * 256 + trow, col = u.pn * 256 + tcol;
;             if (col < C_KA) { v0 = v0 * QS_A; v1 = v1 * QS_A; }
;             else if (col >= C_GA && col < INC) { const f32x4 b0 = *(const f32x4*)(bg + col - C_GA), b1 = *(const f32x4*)(bg + col - C_GA + 4);
; #pragma unroll
;                 for (int i = 0; i < 4; ++i) { v0[i] = sigmoidf_(v0[i] + b0[i]); v1[i] = sigmoidf_(v1[i] + b1[i]); } }
;             *(u32x4*)(O + (size_t)row * INCP + col) = pg8::pack8(v0, v1);
.LBB0_2683:
	s_andn2_saveexec_b64 s[2:3], s[2:3]
	v_pk_mul_f32 v[48:49], v[44:45], s[22:23] op_sel_hi:[1,0]
	v_pk_mul_f32 v[46:47], v[42:43], s[22:23] op_sel_hi:[1,0]
	v_pk_mul_f32 v[52:53], v[40:41], s[22:23] op_sel_hi:[1,0]
	v_pk_mul_f32 v[50:51], v[38:39], s[22:23] op_sel_hi:[1,0]
	s_or_b64 exec, exec, s[2:3]
	v_cvt_pk_bf16_f32 v38, v46, v47
	v_cvt_pk_bf16_f32 v39, v48, v49
	v_cvt_pk_bf16_f32 v40, v50, v51
	v_cvt_pk_bf16_f32 v41, v52, v53
	global_store_dwordx4 v[54:55], v[38:41], off offset:256
	s_and_saveexec_b64 s[2:3], s[4:5]
	s_xor_b64 s[2:3], exec, s[2:3]
	s_cbranch_execz .LBB0_2688
	s_add_i32 s29, s25, 0xfffff760
	v_mov_b64_e32 v[44:45], v[32:33]
	v_mov_b64_e32 v[40:41], v[36:37]
	s_cmpk_gt_u32 s29, 0x7ff
	v_mov_b64_e32 v[42:43], v[30:31]
	v_mov_b64_e32 v[38:39], v[34:35]
	s_cbranch_scc1 .LBB0_2688
	v_mov_b32_e32 v38, v4
	v_mov_b32_e32 v39, v3
	v_lshl_add_u64 v[38:39], v[38:39], 2, s[16:17]
	v_lshl_add_u64 v[42:43], v[38:39], 0, s[20:21]
	v_add_co_u32_e32 v38, vcc, 0xffffe000, v38
	s_nop 1
	v_addc_co_u32_e32 v39, vcc, -1, v39, vcc
	v_mov_b64_e32 v[38:39], v[150:151]
	v_mov_b64_e32 v[40:41], v[152:153]
	s_nop 0
	v_mov_b64_e32 v[42:43], v[154:155]
	v_mov_b64_e32 v[44:45], v[156:157]
	v_add_f32_e32 v38, v34, v38
	v_add_f32_e32 v42, v30, v42
	v_add_f32_e32 v39, v35, v39
	v_add_f32_e32 v43, v31, v43
	v_add_f32_e32 v40, v36, v40
	v_add_f32_e32 v44, v32, v44
	v_add_f32_e32 v41, v37, v41
	v_add_f32_e32 v45, v33, v45
	v_mul_f32_e32 v38, 0xbfb8aa3b, v38
	v_mul_f32_e32 v42, 0xbfb8aa3b, v42
	v_mul_f32_e32 v39, 0xbfb8aa3b, v39
	v_mul_f32_e32 v43, 0xbfb8aa3b, v43
	v_mul_f32_e32 v40, 0xbfb8aa3b, v40
	v_mul_f32_e32 v44, 0xbfb8aa3b, v44
	v_mul_f32_e32 v41, 0xbfb8aa3b, v41
	v_mul_f32_e32 v45, 0xbfb8aa3b, v45
	v_exp_f32_e32 v38, v38
	v_exp_f32_e32 v42, v42
	v_exp_f32_e32 v39, v39
	v_exp_f32_e32 v43, v43
	v_exp_f32_e32 v40, v40
	v_exp_f32_e32 v44, v44
	v_exp_f32_e32 v41, v41
	v_exp_f32_e32 v45, v45
	v_add_f32_e32 v38, 1.0, v38
	v_add_f32_e32 v42, 1.0, v42
	v_add_f32_e32 v39, 1.0, v39
	v_add_f32_e32 v43, 1.0, v43
	v_add_f32_e32 v40, 1.0, v40
	v_add_f32_e32 v44, 1.0, v44
	v_add_f32_e32 v41, 1.0, v41
	v_add_f32_e32 v45, 1.0, v45
	v_rcp_f32_e32 v38, v38
	v_rcp_f32_e32 v42, v42
	v_rcp_f32_e32 v39, v39
	v_rcp_f32_e32 v43, v43
	v_rcp_f32_e32 v40, v40
	v_rcp_f32_e32 v44, v44
	v_rcp_f32_e32 v41, v41
	v_rcp_f32_e32 v45, v45
.LBB0_2688:
	s_andn2_saveexec_b64 s[2:3], s[2:3]
	v_pk_mul_f32 v[40:41], v[36:37], s[22:23] op_sel_hi:[1,0]
	v_pk_mul_f32 v[38:39], v[34:35], s[22:23] op_sel_hi:[1,0]
	v_pk_mul_f32 v[44:45], v[32:33], s[22:23] op_sel_hi:[1,0]
	v_pk_mul_f32 v[42:43], v[30:31], s[22:23] op_sel_hi:[1,0]
	s_or_b64 exec, exec, s[2:3]
	v_readlane_b32 s2, v253, 54
	v_readlane_b32 s3, v253, 55
	v_add_u32_e32 v36, s28, v229
	v_cvt_pk_bf16_f32 v30, v38, v39
	v_mov_b64_e32 v[34:35], s[2:3]
	v_mad_i64_i32 v[34:35], s[2:3], v36, s55, v[34:35]
	v_cvt_pk_bf16_f32 v31, v40, v41
	v_cvt_pk_bf16_f32 v32, v42, v43
	v_cvt_pk_bf16_f32 v33, v44, v45
	v_lshl_add_u64 v[38:39], v[4:5], 1, v[34:35]
	global_store_dwordx4 v[38:39], v[30:33], off
	s_and_saveexec_b64 s[2:3], s[6:7]
	s_xor_b64 s[2:3], exec, s[2:3]
	s_cbranch_execz .LBB0_2693
	s_add_i32 s29, s25, 0xfffff7e0
	v_mov_b64_e32 v[36:37], v[24:25]
	v_mov_b64_e32 v[32:33], v[28:29]
	s_cmpk_gt_u32 s29, 0x7ff
	v_mov_b64_e32 v[34:35], v[22:23]
	v_mov_b64_e32 v[30:31], v[26:27]
	s_cbranch_scc1 .LBB0_2693
	v_lshl_add_u64 v[30:31], v[2:3], 2, s[16:17]
	v_lshl_add_u64 v[34:35], v[30:31], 0, s[20:21]
	v_add_co_u32_e32 v30, vcc, 0xffffe000, v30
	s_nop 1
	v_addc_co_u32_e32 v31, vcc, -1, v31, vcc
	v_mov_b64_e32 v[30:31], v[158:159]
	v_mov_b64_e32 v[32:33], v[160:161]
	s_nop 0
	v_mov_b64_e32 v[34:35], v[162:163]
	v_mov_b64_e32 v[36:37], v[164:165]
	v_add_f32_e32 v30, v26, v30
	v_add_f32_e32 v34, v22, v34
	v_add_f32_e32 v31, v27, v31
	v_add_f32_e32 v35, v23, v35
	v_add_f32_e32 v32, v28, v32
	v_add_f32_e32 v36, v24, v36
	v_add_f32_e32 v33, v29, v33
	v_add_f32_e32 v37, v25, v37
	v_mul_f32_e32 v30, 0xbfb8aa3b, v30
	v_mul_f32_e32 v34, 0xbfb8aa3b, v34
	v_mul_f32_e32 v31, 0xbfb8aa3b, v31
	v_mul_f32_e32 v35, 0xbfb8aa3b, v35
	v_mul_f32_e32 v32, 0xbfb8aa3b, v32
	v_mul_f32_e32 v36, 0xbfb8aa3b, v36
	v_mul_f32_e32 v33, 0xbfb8aa3b, v33
	v_mul_f32_e32 v37, 0xbfb8aa3b, v37
	v_exp_f32_e32 v30, v30
	v_exp_f32_e32 v34, v34
	v_exp_f32_e32 v31, v31
	v_exp_f32_e32 v35, v35
	v_exp_f32_e32 v32, v32
	v_exp_f32_e32 v36, v36
	v_exp_f32_e32 v33, v33
	v_exp_f32_e32 v37, v37
	v_add_f32_e32 v30, 1.0, v30
	v_add_f32_e32 v34, 1.0, v34
	v_add_f32_e32 v31, 1.0, v31
	v_add_f32_e32 v35, 1.0, v35
	v_add_f32_e32 v32, 1.0, v32
	v_add_f32_e32 v36, 1.0, v36
	v_add_f32_e32 v33, 1.0, v33
	v_add_f32_e32 v37, 1.0, v37
	v_rcp_f32_e32 v30, v30
	v_rcp_f32_e32 v34, v34
	v_rcp_f32_e32 v31, v31
	v_rcp_f32_e32 v35, v35
	v_rcp_f32_e32 v32, v32
	v_rcp_f32_e32 v36, v36
	v_rcp_f32_e32 v33, v33
	v_rcp_f32_e32 v37, v37
; __device__ __forceinline__ float sigmoidf_(float x) { return __builtin_amdgcn_rcpf(1.f + __expf(-x)); }
; __device__ __forceinline__ u32x4 pack8(f32x4 v0, f32x4 v1) { u32x4 w; w.x = cvt_pk_bf16(v0[0], v0[1]); w.y = cvt_pk_bf16(v0[2], v0[3]); w.z = cvt_pk_bf16(v1[0], v1[1]); w.w = cvt_pk_bf16(v1[2], v1[3]); return w; }
;     __device__ __forceinline__ void operator()(const f32x4 (&acc)[2][2][4][2], const pg8::Unit& u, int wr, int wc, int fr, int fq) const {
;     ...
;             const int row = u.pm * 256 + trow, col = u.pn * 256 + tcol;
;             if (col < C_KA) { v0 = v0 * QS_A; v1 = v1 * QS_A; }
;             else if (col >= C_GA && col < INC) { const f32x4 b0 = *(const f32x4*)(bg + col - C_GA), b1 = *(const f32x4*)(bg + col - C_GA + 4);
; #pragma unroll
;                 for (int i = 0; i < 4; ++i) { v0[i] = sigmoidf_(v0[i] + b0[i]); v1[i] = sigmoidf_(v1[i] + b1[i]); } }
;             *(u32x4*)(O + (size_t)row * INCP + col) = pg8::pack8(v0, v1);
.LBB0_2693:
	s_andn2_saveexec_b64 s[2:3], s[2:3]
	v_pk_mul_f32 v[32:33], v[28:29], s[22:23] op_sel_hi:[1,0]
	v_pk_mul_f32 v[30:31], v[26:27], s[22:23] op_sel_hi:[1,0]
	v_pk_mul_f32 v[36:37], v[24:25], s[22:23] op_sel_hi:[1,0]
	v_pk_mul_f32 v[34:35], v[22:23], s[22:23] op_sel_hi:[1,0]
	s_or_b64 exec, exec, s[2:3]
	v_cvt_pk_bf16_f32 v22, v30, v31
	v_cvt_pk_bf16_f32 v23, v32, v33
	v_cvt_pk_bf16_f32 v24, v34, v35
	v_cvt_pk_bf16_f32 v25, v36, v37
	global_store_dwordx4 v[38:39], v[22:25], off offset:256
	s_and_saveexec_b64 s[2:3], s[4:5]
	s_xor_b64 s[2:3], exec, s[2:3]
	s_cbranch_execz .LBB0_2698
	s_add_i32 s4, s25, 0xfffff760
	v_mov_b64_e32 v[28:29], v[16:17]
	v_mov_b64_e32 v[24:25], v[20:21]
	s_cmpk_gt_u32 s4, 0x7ff
	v_mov_b64_e32 v[26:27], v[14:15]
	v_mov_b64_e32 v[22:23], v[18:19]
	s_cbranch_scc1 .LBB0_2698
	v_mov_b32_e32 v22, v4
	v_mov_b32_e32 v23, v3
	v_lshl_add_u64 v[22:23], v[22:23], 2, s[16:17]
	v_lshl_add_u64 v[26:27], v[22:23], 0, s[20:21]
	v_add_co_u32_e32 v22, vcc, 0xffffe000, v22
	s_nop 1
	v_addc_co_u32_e32 v23, vcc, -1, v23, vcc
	v_mov_b64_e32 v[22:23], v[150:151]
	v_mov_b64_e32 v[24:25], v[152:153]
	s_nop 0
	v_mov_b64_e32 v[26:27], v[154:155]
	v_mov_b64_e32 v[28:29], v[156:157]
	v_add_f32_e32 v22, v18, v22
	v_add_f32_e32 v26, v14, v26
	v_add_f32_e32 v23, v19, v23
	v_add_f32_e32 v27, v15, v27
	v_add_f32_e32 v24, v20, v24
	v_add_f32_e32 v28, v16, v28
	v_add_f32_e32 v25, v21, v25
	v_add_f32_e32 v29, v17, v29
	v_mul_f32_e32 v22, 0xbfb8aa3b, v22
	v_mul_f32_e32 v26, 0xbfb8aa3b, v26
	v_mul_f32_e32 v23, 0xbfb8aa3b, v23
	v_mul_f32_e32 v27, 0xbfb8aa3b, v27
	v_mul_f32_e32 v24, 0xbfb8aa3b, v24
	v_mul_f32_e32 v28, 0xbfb8aa3b, v28
	v_mul_f32_e32 v25, 0xbfb8aa3b, v25
	v_mul_f32_e32 v29, 0xbfb8aa3b, v29
	v_exp_f32_e32 v22, v22
	v_exp_f32_e32 v26, v26
	v_exp_f32_e32 v23, v23
	v_exp_f32_e32 v27, v27
	v_exp_f32_e32 v24, v24
	v_exp_f32_e32 v28, v28
	v_exp_f32_e32 v25, v25
	v_exp_f32_e32 v29, v29
	v_add_f32_e32 v22, 1.0, v22
	v_add_f32_e32 v26, 1.0, v26
	v_add_f32_e32 v23, 1.0, v23
	v_add_f32_e32 v27, 1.0, v27
	v_add_f32_e32 v24, 1.0, v24
	v_add_f32_e32 v28, 1.0, v28
	v_add_f32_e32 v25, 1.0, v25
	v_add_f32_e32 v29, 1.0, v29
	v_rcp_f32_e32 v22, v22
	v_rcp_f32_e32 v26, v26
	v_rcp_f32_e32 v23, v23
	v_rcp_f32_e32 v27, v27
	v_rcp_f32_e32 v24, v24
	v_rcp_f32_e32 v28, v28
	v_rcp_f32_e32 v25, v25
	v_rcp_f32_e32 v29, v29
.LBB0_2698:
	s_andn2_saveexec_b64 s[2:3], s[2:3]
	v_pk_mul_f32 v[24:25], v[20:21], s[22:23] op_sel_hi:[1,0]
	v_pk_mul_f32 v[22:23], v[18:19], s[22:23] op_sel_hi:[1,0]
	v_pk_mul_f32 v[28:29], v[16:17], s[22:23] op_sel_hi:[1,0]
	v_pk_mul_f32 v[26:27], v[14:15], s[22:23] op_sel_hi:[1,0]
	s_or_b64 exec, exec, s[2:3]
	v_readlane_b32 s2, v253, 54
	v_readlane_b32 s3, v253, 55
	v_add_u32_e32 v20, s28, v230
	v_cvt_pk_bf16_f32 v14, v22, v23
	v_mov_b64_e32 v[18:19], s[2:3]
	v_mad_i64_i32 v[18:19], s[2:3], v20, s55, v[18:19]
	v_cvt_pk_bf16_f32 v15, v24, v25
	v_cvt_pk_bf16_f32 v16, v26, v27
	v_cvt_pk_bf16_f32 v17, v28, v29
	v_lshl_add_u64 v[4:5], v[4:5], 1, v[18:19]
	global_store_dwordx4 v[4:5], v[14:17], off
	s_and_saveexec_b64 s[2:3], s[6:7]
	s_xor_b64 s[2:3], exec, s[2:3]
	s_cbranch_execz .LBB0_2703
	s_addk_i32 s25, 0xf7e0
	v_mov_b64_e32 v[20:21], v[8:9]
	v_mov_b64_e32 v[16:17], v[12:13]
	s_cmpk_gt_u32 s25, 0x7ff
	v_mov_b64_e32 v[18:19], v[6:7]
	v_mov_b64_e32 v[14:15], v[10:11]
	s_cbranch_scc1 .LBB0_2703
	v_lshl_add_u64 v[14:15], v[2:3], 2, s[16:17]
	v_lshl_add_u64 v[18:19], v[14:15], 0, s[20:21]
	v_add_co_u32_e32 v14, vcc, 0xffffe000, v14
	s_nop 1
	v_addc_co_u32_e32 v15, vcc, -1, v15, vcc
	v_mov_b64_e32 v[14:15], v[158:159]
	v_mov_b64_e32 v[16:17], v[160:161]
	s_nop 0
	v_mov_b64_e32 v[18:19], v[162:163]
	v_mov_b64_e32 v[20:21], v[164:165]
	v_add_f32_e32 v2, v10, v14
	v_add_f32_e32 v14, v6, v18
	v_add_f32_e32 v15, v11, v15
	v_add_f32_e32 v18, v7, v19
	v_add_f32_e32 v16, v12, v16
	v_add_f32_e32 v19, v8, v20
	v_add_f32_e32 v17, v13, v17
	v_add_f32_e32 v20, v9, v21
	v_mul_f32_e32 v2, 0xbfb8aa3b, v2
	v_mul_f32_e32 v14, 0xbfb8aa3b, v14
	v_mul_f32_e32 v15, 0xbfb8aa3b, v15
	v_mul_f32_e32 v18, 0xbfb8aa3b, v18
	v_mul_f32_e32 v16, 0xbfb8aa3b, v16
	v_mul_f32_e32 v19, 0xbfb8aa3b, v19
	v_mul_f32_e32 v17, 0xbfb8aa3b, v17
	v_mul_f32_e32 v20, 0xbfb8aa3b, v20
	v_exp_f32_e32 v2, v2
	v_exp_f32_e32 v14, v14
	v_exp_f32_e32 v15, v15
	v_exp_f32_e32 v18, v18
	v_exp_f32_e32 v16, v16
	v_exp_f32_e32 v19, v19
	v_exp_f32_e32 v17, v17
	v_exp_f32_e32 v20, v20
	v_add_f32_e32 v2, 1.0, v2
	v_add_f32_e32 v21, 1.0, v14
	v_add_f32_e32 v15, 1.0, v15
	v_add_f32_e32 v22, 1.0, v18
	v_add_f32_e32 v16, 1.0, v16
	v_add_f32_e32 v23, 1.0, v19
	v_add_f32_e32 v17, 1.0, v17
	v_add_f32_e32 v24, 1.0, v20
	v_rcp_f32_e32 v14, v2
	v_rcp_f32_e32 v18, v21
	v_rcp_f32_e32 v15, v15
	v_rcp_f32_e32 v19, v22
	v_rcp_f32_e32 v16, v16
	v_rcp_f32_e32 v20, v23
	v_rcp_f32_e32 v17, v17
	v_rcp_f32_e32 v21, v24

; __device__ __forceinline__ float sigmoidf_(float x) { return __builtin_amdgcn_rcpf(1.f + __expf(-x)); }
; __device__ __forceinline__ u32x4 pack8(f32x4 v0, f32x4 v1) { u32x4 w; w.x = cvt_pk_bf16(v0[0], v0[1]); w.y = cvt_pk_bf16(v0[2], v0[3]); w.z = cvt_pk_bf16(v1[0], v1[1]); w.w = cvt_pk_bf16(v1[2], v1[3]); return w; }
;     __device__ __forceinline__ void operator()(const f32x4 (&acc)[2][2][4][2], const pg8::Unit& u, int wr, int wc, int fr, int fq) const {
;     ...
;             const int row = u.pm * 256 + trow, col = u.pn * 256 + tcol;
;             if (col < C_KA) { v0 = v0 * QS_A; v1 = v1 * QS_A; }
;             else if (col >= C_GA && col < INC) { const f32x4 b0 = *(const f32x4*)(bg + col - C_GA), b1 = *(const f32x4*)(bg + col - C_GA + 4);
; #pragma unroll
;                 for (int i = 0; i < 4; ++i) { v0[i] = sigmoidf_(v0[i] + b0[i]); v1[i] = sigmoidf_(v1[i] + b1[i]); } }
;             *(u32x4*)(O + (size_t)row * INCP + col) = pg8::pack8(v0, v1);
.LBB0_3078:
	s_lshl_b32 s4, s58, 8
	s_or_b32 s23, s47, s4
	v_or_b32_e32 v4, s23, v218
	v_cmp_lt_i32_e64 s[4:5], s53, v4
	s_and_saveexec_b64 s[6:7], s[4:5]
	s_xor_b64 s[6:7], exec, s[6:7]
	s_mov_b32 s59, s64
	s_cbranch_execz .LBB0_3081
	s_add_i32 s26, s23, 0xfffff760
	s_cmpk_gt_u32 s26, 0x7ff
	v_mov_b32_e32 v135, v129
	v_mov_b32_e32 v134, v128
	v_mov_b32_e32 v137, v127
	v_mov_b32_e32 v136, v126
	v_mov_b32_e32 v139, v133
	v_mov_b32_e32 v138, v132
	v_mov_b32_e32 v141, v131
	v_mov_b32_e32 v140, v130
	s_cbranch_scc1 .LBB0_3081
	v_mov_b32_e32 v5, v3
	v_lshl_add_u64 v[134:135], v[4:5], 2, s[12:13]
	v_lshl_add_u64 v[138:139], v[134:135], 0, s[18:19]
	v_add_co_u32_e32 v134, vcc, 0xffffe000, v134
	s_nop 1
	v_addc_co_u32_e32 v135, vcc, -1, v135, vcc
	global_load_dwordx4 v[134:137], v[134:135], off offset:-640
	s_nop 0
	global_load_dwordx4 v[138:141], v[138:139], off offset:16
	s_waitcnt vmcnt(0)
	v_mov_b64_e32 v[150:151], v[134:135]
	v_mov_b64_e32 v[152:153], v[136:137]
	v_mov_b64_e32 v[154:155], v[138:139]
	v_mov_b64_e32 v[156:157], v[140:141]
	v_add_f32_e32 v2, v130, v134
	v_add_f32_e32 v5, v126, v138
	v_add_f32_e32 v134, v131, v135
	v_add_f32_e32 v135, v127, v139
	v_add_f32_e32 v136, v132, v136
	v_add_f32_e32 v138, v128, v140
	v_add_f32_e32 v137, v133, v137
	v_add_f32_e32 v139, v129, v141
	v_mul_f32_e32 v2, 0xbfb8aa3b, v2
	v_mul_f32_e32 v5, 0xbfb8aa3b, v5
	v_mul_f32_e32 v134, 0xbfb8aa3b, v134
	v_mul_f32_e32 v135, 0xbfb8aa3b, v135
	v_mul_f32_e32 v136, 0xbfb8aa3b, v136
	v_mul_f32_e32 v138, 0xbfb8aa3b, v138
	v_mul_f32_e32 v137, 0xbfb8aa3b, v137
	v_mul_f32_e32 v139, 0xbfb8aa3b, v139
	v_exp_f32_e32 v2, v2
	v_exp_f32_e32 v5, v5
	v_exp_f32_e32 v134, v134
	v_exp_f32_e32 v135, v135
	v_exp_f32_e32 v136, v136
	v_exp_f32_e32 v138, v138
	v_exp_f32_e32 v137, v137
	v_exp_f32_e32 v139, v139
	v_add_f32_e32 v2, 1.0, v2
	v_add_f32_e32 v5, 1.0, v5
	v_add_f32_e32 v134, 1.0, v134
	v_add_f32_e32 v135, 1.0, v135
	v_add_f32_e32 v142, 1.0, v136
	v_add_f32_e32 v143, 1.0, v138
	v_add_f32_e32 v144, 1.0, v137
	v_add_f32_e32 v145, 1.0, v139
	v_rcp_f32_e32 v140, v2
	v_rcp_f32_e32 v136, v5
	v_rcp_f32_e32 v141, v134
	v_rcp_f32_e32 v137, v135
	v_rcp_f32_e32 v138, v142
	v_rcp_f32_e32 v134, v143
	v_rcp_f32_e32 v139, v144
	v_rcp_f32_e32 v135, v145
.LBB0_3081:
	s_andn2_saveexec_b64 s[6:7], s[6:7]
	v_pk_mul_f32 v[138:139], v[132:133], s[20:21] op_sel_hi:[1,0]
	v_pk_mul_f32 v[140:141], v[130:131], s[20:21] op_sel_hi:[1,0]
	v_pk_mul_f32 v[134:135], v[128:129], s[20:21] op_sel_hi:[1,0]
	v_pk_mul_f32 v[136:137], v[126:127], s[20:21] op_sel_hi:[1,0]
	s_or_b64 exec, exec, s[6:7]
	v_readlane_b32 s6, v253, 54
	s_lshl_b32 s28, s33, 8
	v_readlane_b32 s7, v253, 55
	v_add_u32_e32 v2, s28, v217
	v_ashrrev_i32_e32 v5, 31, v4
	v_mov_b64_e32 v[126:127], s[6:7]
	v_mad_i64_i32 v[126:127], s[6:7], v2, s54, v[126:127]
	v_or_b32_e32 v2, 0x80, v4
	v_cvt_pk_bf16_f32 v128, v140, v141
	v_cvt_pk_bf16_f32 v129, v138, v139
	v_cvt_pk_bf16_f32 v130, v136, v137
	v_cvt_pk_bf16_f32 v131, v134, v135
	v_lshl_add_u64 v[126:127], v[4:5], 1, v[126:127]
	v_cmp_lt_i32_e64 s[6:7], s53, v2
	global_store_dwordx4 v[126:127], v[128:131], off
	s_and_saveexec_b64 s[26:27], s[6:7]
	s_xor_b64 s[26:27], exec, s[26:27]
	s_cbranch_execz .LBB0_3086
	s_add_i32 s29, s23, 0xfffff7e0
	s_cmpk_gt_u32 s29, 0x7ff
	v_mov_b32_e32 v129, v121
	v_mov_b32_e32 v128, v120
	v_mov_b32_e32 v131, v119
	v_mov_b32_e32 v130, v118
	v_mov_b32_e32 v133, v125
	v_mov_b32_e32 v132, v124
	v_mov_b32_e32 v135, v123
	v_mov_b32_e32 v134, v122
	s_cbranch_scc1 .LBB0_3086
	v_lshl_add_u64 v[128:129], v[2:3], 2, s[12:13]
	v_lshl_add_u64 v[132:133], v[128:129], 0, s[18:19]
	v_add_co_u32_e32 v128, vcc, 0xffffe000, v128
	s_nop 1
	v_addc_co_u32_e32 v129, vcc, -1, v129, vcc
	global_load_dwordx4 v[128:131], v[128:129], off offset:-640
	s_nop 0
	global_load_dwordx4 v[132:135], v[132:133], off offset:16
	s_waitcnt vmcnt(0)
	v_mov_b64_e32 v[158:159], v[128:129]
	v_mov_b64_e32 v[160:161], v[130:131]
	v_mov_b64_e32 v[162:163], v[132:133]
	v_mov_b64_e32 v[164:165], v[134:135]
	v_add_f32_e32 v128, v122, v128
	v_add_f32_e32 v132, v118, v132
	v_add_f32_e32 v129, v123, v129
	v_add_f32_e32 v133, v119, v133
	v_add_f32_e32 v130, v124, v130
	v_add_f32_e32 v134, v120, v134
	v_add_f32_e32 v131, v125, v131
	v_add_f32_e32 v135, v121, v135
	v_mul_f32_e32 v128, 0xbfb8aa3b, v128
	v_mul_f32_e32 v132, 0xbfb8aa3b, v132
	v_mul_f32_e32 v129, 0xbfb8aa3b, v129
	v_mul_f32_e32 v133, 0xbfb8aa3b, v133
	v_mul_f32_e32 v130, 0xbfb8aa3b, v130
	v_mul_f32_e32 v134, 0xbfb8aa3b, v134
	v_mul_f32_e32 v131, 0xbfb8aa3b, v131
	v_mul_f32_e32 v135, 0xbfb8aa3b, v135
	v_exp_f32_e32 v128, v128
	v_exp_f32_e32 v132, v132
	v_exp_f32_e32 v129, v129
	v_exp_f32_e32 v133, v133
	v_exp_f32_e32 v130, v130
	v_exp_f32_e32 v134, v134
	v_exp_f32_e32 v131, v131
	v_exp_f32_e32 v135, v135
	v_add_f32_e32 v128, 1.0, v128
	v_add_f32_e32 v132, 1.0, v132
	v_add_f32_e32 v129, 1.0, v129
	v_add_f32_e32 v133, 1.0, v133
	v_add_f32_e32 v136, 1.0, v130
	v_add_f32_e32 v137, 1.0, v134
	v_add_f32_e32 v138, 1.0, v131
	v_add_f32_e32 v139, 1.0, v135
	v_rcp_f32_e32 v134, v128
	v_rcp_f32_e32 v130, v132
	v_rcp_f32_e32 v135, v129
	v_rcp_f32_e32 v131, v133
	v_rcp_f32_e32 v132, v136
	v_rcp_f32_e32 v128, v137
	v_rcp_f32_e32 v133, v138
	v_rcp_f32_e32 v129, v139
; __device__ __forceinline__ float sigmoidf_(float x) { return __builtin_amdgcn_rcpf(1.f + __expf(-x)); }
; __device__ __forceinline__ u32x4 pack8(f32x4 v0, f32x4 v1) { u32x4 w; w.x = cvt_pk_bf16(v0[0], v0[1]); w.y = cvt_pk_bf16(v0[2], v0[3]); w.z = cvt_pk_bf16(v1[0], v1[1]); w.w = cvt_pk_bf16(v1[2], v1[3]); return w; }
;     __device__ __forceinline__ void operator()(const f32x4 (&acc)[2][2][4][2], const pg8::Unit& u, int wr, int wc, int fr, int fq) const {
;     ...
;             const int row = u.pm * 256 + trow, col = u.pn * 256 + tcol;
;             if (col < C_KA) { v0 = v0 * QS_A; v1 = v1 * QS_A; }
;             else if (col >= C_GA && col < INC) { const f32x4 b0 = *(const f32x4*)(bg + col - C_GA), b1 = *(const f32x4*)(bg + col - C_GA + 4);
; #pragma unroll
;                 for (int i = 0; i < 4; ++i) { v0[i] = sigmoidf_(v0[i] + b0[i]); v1[i] = sigmoidf_(v1[i] + b1[i]); } }
;             *(u32x4*)(O + (size_t)row * INCP + col) = pg8::pack8(v0, v1);
.LBB0_3086:
	s_andn2_saveexec_b64 s[26:27], s[26:27]
	v_pk_mul_f32 v[132:133], v[124:125], s[20:21] op_sel_hi:[1,0]
	v_pk_mul_f32 v[134:135], v[122:123], s[20:21] op_sel_hi:[1,0]
	v_pk_mul_f32 v[128:129], v[120:121], s[20:21] op_sel_hi:[1,0]
	v_pk_mul_f32 v[130:131], v[118:119], s[20:21] op_sel_hi:[1,0]
	s_or_b64 exec, exec, s[26:27]
	v_cvt_pk_bf16_f32 v118, v134, v135
	v_cvt_pk_bf16_f32 v119, v132, v133
	v_cvt_pk_bf16_f32 v120, v130, v131
	v_cvt_pk_bf16_f32 v121, v128, v129
	global_store_dwordx4 v[126:127], v[118:121], off offset:256
	s_and_saveexec_b64 s[26:27], s[4:5]
	s_xor_b64 s[26:27], exec, s[26:27]
	s_cbranch_execz .LBB0_3091
	s_add_i32 s29, s23, 0xfffff760
	s_cmpk_gt_u32 s29, 0x7ff
	v_mov_b32_e32 v119, v113
	v_mov_b32_e32 v118, v112
	v_mov_b32_e32 v121, v111
	v_mov_b32_e32 v120, v110
	v_mov_b32_e32 v123, v117
	v_mov_b32_e32 v122, v116
	v_mov_b32_e32 v125, v115
	v_mov_b32_e32 v124, v114
	s_cbranch_scc1 .LBB0_3091
	v_mov_b32_e32 v118, v4
	v_mov_b32_e32 v119, v3
	v_lshl_add_u64 v[118:119], v[118:119], 2, s[12:13]
	v_lshl_add_u64 v[122:123], v[118:119], 0, s[18:19]
	v_add_co_u32_e32 v118, vcc, 0xffffe000, v118
	s_nop 1
	v_addc_co_u32_e32 v119, vcc, -1, v119, vcc
	v_mov_b64_e32 v[118:119], v[150:151]
	v_mov_b64_e32 v[120:121], v[152:153]
	s_nop 0
	v_mov_b64_e32 v[122:123], v[154:155]
	v_mov_b64_e32 v[124:125], v[156:157]
	v_add_f32_e32 v118, v114, v118
	v_add_f32_e32 v122, v110, v122
	v_add_f32_e32 v119, v115, v119
	v_add_f32_e32 v123, v111, v123
	v_add_f32_e32 v120, v116, v120
	v_add_f32_e32 v124, v112, v124
	v_add_f32_e32 v121, v117, v121
	v_add_f32_e32 v125, v113, v125
	v_mul_f32_e32 v118, 0xbfb8aa3b, v118
	v_mul_f32_e32 v122, 0xbfb8aa3b, v122
	v_mul_f32_e32 v119, 0xbfb8aa3b, v119
	v_mul_f32_e32 v123, 0xbfb8aa3b, v123
	v_mul_f32_e32 v120, 0xbfb8aa3b, v120
	v_mul_f32_e32 v124, 0xbfb8aa3b, v124
	v_mul_f32_e32 v121, 0xbfb8aa3b, v121
	v_mul_f32_e32 v125, 0xbfb8aa3b, v125
	v_exp_f32_e32 v118, v118
	v_exp_f32_e32 v122, v122
	v_exp_f32_e32 v119, v119
	v_exp_f32_e32 v123, v123
	v_exp_f32_e32 v120, v120
	v_exp_f32_e32 v124, v124
	v_exp_f32_e32 v121, v121
	v_exp_f32_e32 v125, v125
	v_add_f32_e32 v118, 1.0, v118
	v_add_f32_e32 v122, 1.0, v122
	v_add_f32_e32 v119, 1.0, v119
	v_add_f32_e32 v123, 1.0, v123
	v_add_f32_e32 v126, 1.0, v120
	v_add_f32_e32 v127, 1.0, v124
	v_add_f32_e32 v128, 1.0, v121
	v_add_f32_e32 v129, 1.0, v125
	v_rcp_f32_e32 v124, v118
	v_rcp_f32_e32 v120, v122
	v_rcp_f32_e32 v125, v119
	v_rcp_f32_e32 v121, v123
	v_rcp_f32_e32 v122, v126
	v_rcp_f32_e32 v118, v127
	v_rcp_f32_e32 v123, v128
	v_rcp_f32_e32 v119, v129
.LBB0_3091:
	s_andn2_saveexec_b64 s[26:27], s[26:27]
	v_pk_mul_f32 v[122:123], v[116:117], s[20:21] op_sel_hi:[1,0]
	v_pk_mul_f32 v[124:125], v[114:115], s[20:21] op_sel_hi:[1,0]
	v_pk_mul_f32 v[118:119], v[112:113], s[20:21] op_sel_hi:[1,0]
	v_pk_mul_f32 v[120:121], v[110:111], s[20:21] op_sel_hi:[1,0]
	s_or_b64 exec, exec, s[26:27]
	v_readlane_b32 s26, v253, 54
	v_readlane_b32 s27, v253, 55
	v_add_u32_e32 v116, s28, v220
	v_cvt_pk_bf16_f32 v112, v124, v125
	v_mov_b64_e32 v[110:111], s[26:27]
	v_mad_i64_i32 v[110:111], s[26:27], v116, s54, v[110:111]
	v_cvt_pk_bf16_f32 v113, v122, v123
	v_cvt_pk_bf16_f32 v114, v120, v121
	v_cvt_pk_bf16_f32 v115, v118, v119
	v_lshl_add_u64 v[110:111], v[4:5], 1, v[110:111]
	global_store_dwordx4 v[110:111], v[112:115], off
	s_and_saveexec_b64 s[26:27], s[6:7]
	s_xor_b64 s[26:27], exec, s[26:27]
	s_cbranch_execz .LBB0_3096
	s_add_i32 s29, s23, 0xfffff7e0
	s_cmpk_gt_u32 s29, 0x7ff
	v_mov_b32_e32 v113, v105
	v_mov_b32_e32 v112, v104
	v_mov_b32_e32 v115, v103
	v_mov_b32_e32 v114, v102
	v_mov_b32_e32 v117, v109
	v_mov_b32_e32 v116, v108
	v_mov_b32_e32 v119, v107
	v_mov_b32_e32 v118, v106
	s_cbranch_scc1 .LBB0_3096
	v_lshl_add_u64 v[112:113], v[2:3], 2, s[12:13]
	v_lshl_add_u64 v[116:117], v[112:113], 0, s[18:19]
	v_add_co_u32_e32 v112, vcc, 0xffffe000, v112
	s_nop 1
	v_addc_co_u32_e32 v113, vcc, -1, v113, vcc
	v_mov_b64_e32 v[112:113], v[158:159]
	v_mov_b64_e32 v[114:115], v[160:161]
	s_nop 0
	v_mov_b64_e32 v[116:117], v[162:163]
	v_mov_b64_e32 v[118:119], v[164:165]
	v_add_f32_e32 v112, v106, v112
	v_add_f32_e32 v116, v102, v116
	v_add_f32_e32 v113, v107, v113
	v_add_f32_e32 v117, v103, v117
	v_add_f32_e32 v114, v108, v114
	v_add_f32_e32 v118, v104, v118
	v_add_f32_e32 v115, v109, v115
	v_add_f32_e32 v119, v105, v119
	v_mul_f32_e32 v112, 0xbfb8aa3b, v112
	v_mul_f32_e32 v116, 0xbfb8aa3b, v116
	v_mul_f32_e32 v113, 0xbfb8aa3b, v113
	v_mul_f32_e32 v117, 0xbfb8aa3b, v117
	v_mul_f32_e32 v114, 0xbfb8aa3b, v114
	v_mul_f32_e32 v118, 0xbfb8aa3b, v118
	v_mul_f32_e32 v115, 0xbfb8aa3b, v115
	v_mul_f32_e32 v119, 0xbfb8aa3b, v119
	v_exp_f32_e32 v112, v112
	v_exp_f32_e32 v116, v116
	v_exp_f32_e32 v113, v113
	v_exp_f32_e32 v117, v117
	v_exp_f32_e32 v114, v114
	v_exp_f32_e32 v118, v118
	v_exp_f32_e32 v115, v115
	v_exp_f32_e32 v119, v119
	v_add_f32_e32 v112, 1.0, v112
	v_add_f32_e32 v116, 1.0, v116
	v_add_f32_e32 v113, 1.0, v113
	v_add_f32_e32 v117, 1.0, v117
	v_add_f32_e32 v120, 1.0, v114
	v_add_f32_e32 v121, 1.0, v118
	v_add_f32_e32 v122, 1.0, v115
	v_add_f32_e32 v123, 1.0, v119
	v_rcp_f32_e32 v118, v112
	v_rcp_f32_e32 v114, v116
	v_rcp_f32_e32 v119, v113
	v_rcp_f32_e32 v115, v117
	v_rcp_f32_e32 v116, v120
	v_rcp_f32_e32 v112, v121
	v_rcp_f32_e32 v117, v122
	v_rcp_f32_e32 v113, v123
; __device__ __forceinline__ float sigmoidf_(float x) { return __builtin_amdgcn_rcpf(1.f + __expf(-x)); }
; __device__ __forceinline__ u32x4 pack8(f32x4 v0, f32x4 v1) { u32x4 w; w.x = cvt_pk_bf16(v0[0], v0[1]); w.y = cvt_pk_bf16(v0[2], v0[3]); w.z = cvt_pk_bf16(v1[0], v1[1]); w.w = cvt_pk_bf16(v1[2], v1[3]); return w; }
;     __device__ __forceinline__ void operator()(const f32x4 (&acc)[2][2][4][2], const pg8::Unit& u, int wr, int wc, int fr, int fq) const {
;     ...
;             const int row = u.pm * 256 + trow, col = u.pn * 256 + tcol;
;             if (col < C_KA) { v0 = v0 * QS_A; v1 = v1 * QS_A; }
;             else if (col >= C_GA && col < INC) { const f32x4 b0 = *(const f32x4*)(bg + col - C_GA), b1 = *(const f32x4*)(bg + col - C_GA + 4);
; #pragma unroll
;                 for (int i = 0; i < 4; ++i) { v0[i] = sigmoidf_(v0[i] + b0[i]); v1[i] = sigmoidf_(v1[i] + b1[i]); } }
;             *(u32x4*)(O + (size_t)row * INCP + col) = pg8::pack8(v0, v1);
.LBB0_3096:
	s_andn2_saveexec_b64 s[26:27], s[26:27]
	v_pk_mul_f32 v[116:117], v[108:109], s[20:21] op_sel_hi:[1,0]
	v_pk_mul_f32 v[118:119], v[106:107], s[20:21] op_sel_hi:[1,0]
	v_pk_mul_f32 v[112:113], v[104:105], s[20:21] op_sel_hi:[1,0]
	v_pk_mul_f32 v[114:115], v[102:103], s[20:21] op_sel_hi:[1,0]
	s_or_b64 exec, exec, s[26:27]
	v_cvt_pk_bf16_f32 v102, v118, v119
	v_cvt_pk_bf16_f32 v103, v116, v117
	v_cvt_pk_bf16_f32 v104, v114, v115
	v_cvt_pk_bf16_f32 v105, v112, v113
	global_store_dwordx4 v[110:111], v[102:105], off offset:256
	s_and_saveexec_b64 s[26:27], s[4:5]
	s_xor_b64 s[26:27], exec, s[26:27]
	s_cbranch_execz .LBB0_3101
	s_add_i32 s29, s23, 0xfffff760
	s_cmpk_gt_u32 s29, 0x7ff
	v_mov_b32_e32 v103, v97
	v_mov_b32_e32 v102, v96
	v_mov_b32_e32 v105, v95
	v_mov_b32_e32 v104, v94
	v_mov_b32_e32 v107, v101
	v_mov_b32_e32 v106, v100
	v_mov_b32_e32 v109, v99
	v_mov_b32_e32 v108, v98
	s_cbranch_scc1 .LBB0_3101
	v_mov_b32_e32 v102, v4
	v_mov_b32_e32 v103, v3
	v_lshl_add_u64 v[102:103], v[102:103], 2, s[12:13]
	v_lshl_add_u64 v[106:107], v[102:103], 0, s[18:19]
	v_add_co_u32_e32 v102, vcc, 0xffffe000, v102
	s_nop 1
	v_addc_co_u32_e32 v103, vcc, -1, v103, vcc
	v_mov_b64_e32 v[102:103], v[150:151]
	v_mov_b64_e32 v[104:105], v[152:153]
	s_nop 0
	v_mov_b64_e32 v[106:107], v[154:155]
	v_mov_b64_e32 v[108:109], v[156:157]
	v_add_f32_e32 v102, v98, v102
	v_add_f32_e32 v106, v94, v106
	v_add_f32_e32 v103, v99, v103
	v_add_f32_e32 v107, v95, v107
	v_add_f32_e32 v104, v100, v104
	v_add_f32_e32 v108, v96, v108
	v_add_f32_e32 v105, v101, v105
	v_add_f32_e32 v109, v97, v109
	v_mul_f32_e32 v102, 0xbfb8aa3b, v102
	v_mul_f32_e32 v106, 0xbfb8aa3b, v106
	v_mul_f32_e32 v103, 0xbfb8aa3b, v103
	v_mul_f32_e32 v107, 0xbfb8aa3b, v107
	v_mul_f32_e32 v104, 0xbfb8aa3b, v104
	v_mul_f32_e32 v108, 0xbfb8aa3b, v108
	v_mul_f32_e32 v105, 0xbfb8aa3b, v105
	v_mul_f32_e32 v109, 0xbfb8aa3b, v109
	v_exp_f32_e32 v102, v102
	v_exp_f32_e32 v106, v106
	v_exp_f32_e32 v103, v103
	v_exp_f32_e32 v107, v107
	v_exp_f32_e32 v104, v104
	v_exp_f32_e32 v108, v108
	v_exp_f32_e32 v105, v105
	v_exp_f32_e32 v109, v109
	v_add_f32_e32 v102, 1.0, v102
	v_add_f32_e32 v106, 1.0, v106
	v_add_f32_e32 v103, 1.0, v103
	v_add_f32_e32 v107, 1.0, v107
	v_add_f32_e32 v110, 1.0, v104
	v_add_f32_e32 v111, 1.0, v108
	v_add_f32_e32 v112, 1.0, v105
	v_add_f32_e32 v113, 1.0, v109
	v_rcp_f32_e32 v108, v102
	v_rcp_f32_e32 v104, v106
	v_rcp_f32_e32 v109, v103
	v_rcp_f32_e32 v105, v107
	v_rcp_f32_e32 v106, v110
	v_rcp_f32_e32 v102, v111
	v_rcp_f32_e32 v107, v112
	v_rcp_f32_e32 v103, v113
.LBB0_3101:
	s_andn2_saveexec_b64 s[26:27], s[26:27]
	v_pk_mul_f32 v[106:107], v[100:101], s[20:21] op_sel_hi:[1,0]
	v_pk_mul_f32 v[108:109], v[98:99], s[20:21] op_sel_hi:[1,0]
	v_pk_mul_f32 v[102:103], v[96:97], s[20:21] op_sel_hi:[1,0]
	v_pk_mul_f32 v[104:105], v[94:95], s[20:21] op_sel_hi:[1,0]
	s_or_b64 exec, exec, s[26:27]
	v_readlane_b32 s26, v253, 54
	v_readlane_b32 s27, v253, 55
	v_add_u32_e32 v100, s28, v221
	v_cvt_pk_bf16_f32 v96, v108, v109
	v_mov_b64_e32 v[94:95], s[26:27]
	v_mad_i64_i32 v[94:95], s[26:27], v100, s54, v[94:95]
	v_cvt_pk_bf16_f32 v97, v106, v107
	v_cvt_pk_bf16_f32 v98, v104, v105
	v_cvt_pk_bf16_f32 v99, v102, v103
	v_lshl_add_u64 v[94:95], v[4:5], 1, v[94:95]
	global_store_dwordx4 v[94:95], v[96:99], off
	s_and_saveexec_b64 s[26:27], s[6:7]
	s_xor_b64 s[26:27], exec, s[26:27]
	s_cbranch_execz .LBB0_3106
	s_add_i32 s29, s23, 0xfffff7e0
	s_cmpk_gt_u32 s29, 0x7ff
	v_mov_b32_e32 v97, v89
	v_mov_b32_e32 v96, v88
	v_mov_b32_e32 v99, v87
	v_mov_b32_e32 v98, v86
	v_mov_b32_e32 v101, v93
	v_mov_b32_e32 v100, v92
	v_mov_b32_e32 v103, v91
	v_mov_b32_e32 v102, v90
	s_cbranch_scc1 .LBB0_3106
	v_lshl_add_u64 v[96:97], v[2:3], 2, s[12:13]
	v_lshl_add_u64 v[100:101], v[96:97], 0, s[18:19]
	v_add_co_u32_e32 v96, vcc, 0xffffe000, v96
	s_nop 1
	v_addc_co_u32_e32 v97, vcc, -1, v97, vcc
	v_mov_b64_e32 v[96:97], v[158:159]
	v_mov_b64_e32 v[98:99], v[160:161]
	s_nop 0
	v_mov_b64_e32 v[100:101], v[162:163]
	v_mov_b64_e32 v[102:103], v[164:165]
	v_add_f32_e32 v96, v90, v96
	v_add_f32_e32 v100, v86, v100
	v_add_f32_e32 v97, v91, v97
	v_add_f32_e32 v101, v87, v101
	v_add_f32_e32 v98, v92, v98
	v_add_f32_e32 v102, v88, v102
	v_add_f32_e32 v99, v93, v99
	v_add_f32_e32 v103, v89, v103
	v_mul_f32_e32 v96, 0xbfb8aa3b, v96
	v_mul_f32_e32 v100, 0xbfb8aa3b, v100
	v_mul_f32_e32 v97, 0xbfb8aa3b, v97
	v_mul_f32_e32 v101, 0xbfb8aa3b, v101
	v_mul_f32_e32 v98, 0xbfb8aa3b, v98
	v_mul_f32_e32 v102, 0xbfb8aa3b, v102
	v_mul_f32_e32 v99, 0xbfb8aa3b, v99
	v_mul_f32_e32 v103, 0xbfb8aa3b, v103
	v_exp_f32_e32 v96, v96
	v_exp_f32_e32 v100, v100
	v_exp_f32_e32 v97, v97
	v_exp_f32_e32 v101, v101
	v_exp_f32_e32 v98, v98
	v_exp_f32_e32 v102, v102
	v_exp_f32_e32 v99, v99
	v_exp_f32_e32 v103, v103
	v_add_f32_e32 v96, 1.0, v96
	v_add_f32_e32 v100, 1.0, v100
	v_add_f32_e32 v97, 1.0, v97
	v_add_f32_e32 v101, 1.0, v101
	v_add_f32_e32 v104, 1.0, v98
	v_add_f32_e32 v105, 1.0, v102
	v_add_f32_e32 v106, 1.0, v99
	v_add_f32_e32 v107, 1.0, v103
	v_rcp_f32_e32 v102, v96
	v_rcp_f32_e32 v98, v100
	v_rcp_f32_e32 v103, v97
	v_rcp_f32_e32 v99, v101
	v_rcp_f32_e32 v100, v104
	v_rcp_f32_e32 v96, v105
	v_rcp_f32_e32 v101, v106
	v_rcp_f32_e32 v97, v107
; __device__ __forceinline__ float sigmoidf_(float x) { return __builtin_amdgcn_rcpf(1.f + __expf(-x)); }
; __device__ __forceinline__ u32x4 pack8(f32x4 v0, f32x4 v1) { u32x4 w; w.x = cvt_pk_bf16(v0[0], v0[1]); w.y = cvt_pk_bf16(v0[2], v0[3]); w.z = cvt_pk_bf16(v1[0], v1[1]); w.w = cvt_pk_bf16(v1[2], v1[3]); return w; }
;     __device__ __forceinline__ void operator()(const f32x4 (&acc)[2][2][4][2], const pg8::Unit& u, int wr, int wc, int fr, int fq) const {
;     ...
;             const int row = u.pm * 256 + trow, col = u.pn * 256 + tcol;
;             if (col < C_KA) { v0 = v0 * QS_A; v1 = v1 * QS_A; }
;             else if (col >= C_GA && col < INC) { const f32x4 b0 = *(const f32x4*)(bg + col - C_GA), b1 = *(const f32x4*)(bg + col - C_GA + 4);
; #pragma unroll
;                 for (int i = 0; i < 4; ++i) { v0[i] = sigmoidf_(v0[i] + b0[i]); v1[i] = sigmoidf_(v1[i] + b1[i]); } }
;             *(u32x4*)(O + (size_t)row * INCP + col) = pg8::pack8(v0, v1);
.LBB0_3106:
	s_andn2_saveexec_b64 s[26:27], s[26:27]
	v_pk_mul_f32 v[100:101], v[92:93], s[20:21] op_sel_hi:[1,0]
	v_pk_mul_f32 v[102:103], v[90:91], s[20:21] op_sel_hi:[1,0]
	v_pk_mul_f32 v[96:97], v[88:89], s[20:21] op_sel_hi:[1,0]
	v_pk_mul_f32 v[98:99], v[86:87], s[20:21] op_sel_hi:[1,0]
	s_or_b64 exec, exec, s[26:27]
	v_cvt_pk_bf16_f32 v86, v102, v103
	v_cvt_pk_bf16_f32 v87, v100, v101
	v_cvt_pk_bf16_f32 v88, v98, v99
	v_cvt_pk_bf16_f32 v89, v96, v97
	global_store_dwordx4 v[94:95], v[86:89], off offset:256
	s_and_saveexec_b64 s[26:27], s[4:5]
	s_xor_b64 s[26:27], exec, s[26:27]
	s_cbranch_execz .LBB0_3111
	s_add_i32 s29, s23, 0xfffff760
	s_cmpk_gt_u32 s29, 0x7ff
	v_mov_b32_e32 v87, v81
	v_mov_b32_e32 v86, v80
	v_mov_b32_e32 v89, v79
	v_mov_b32_e32 v88, v78
	v_mov_b32_e32 v91, v85
	v_mov_b32_e32 v90, v84
	v_mov_b32_e32 v93, v83
	v_mov_b32_e32 v92, v82
	s_cbranch_scc1 .LBB0_3111
	v_mov_b32_e32 v86, v4
	v_mov_b32_e32 v87, v3
	v_lshl_add_u64 v[86:87], v[86:87], 2, s[12:13]
	v_lshl_add_u64 v[90:91], v[86:87], 0, s[18:19]
	v_add_co_u32_e32 v86, vcc, 0xffffe000, v86
	s_nop 1
	v_addc_co_u32_e32 v87, vcc, -1, v87, vcc
	v_mov_b64_e32 v[86:87], v[150:151]
	v_mov_b64_e32 v[88:89], v[152:153]
	s_nop 0
	v_mov_b64_e32 v[90:91], v[154:155]
	v_mov_b64_e32 v[92:93], v[156:157]
	v_add_f32_e32 v86, v82, v86
	v_add_f32_e32 v90, v78, v90
	v_add_f32_e32 v87, v83, v87
	v_add_f32_e32 v91, v79, v91
	v_add_f32_e32 v88, v84, v88
	v_add_f32_e32 v92, v80, v92
	v_add_f32_e32 v89, v85, v89
	v_add_f32_e32 v93, v81, v93
	v_mul_f32_e32 v86, 0xbfb8aa3b, v86
	v_mul_f32_e32 v90, 0xbfb8aa3b, v90
	v_mul_f32_e32 v87, 0xbfb8aa3b, v87
	v_mul_f32_e32 v91, 0xbfb8aa3b, v91
	v_mul_f32_e32 v88, 0xbfb8aa3b, v88
	v_mul_f32_e32 v92, 0xbfb8aa3b, v92
	v_mul_f32_e32 v89, 0xbfb8aa3b, v89
	v_mul_f32_e32 v93, 0xbfb8aa3b, v93
	v_exp_f32_e32 v86, v86
	v_exp_f32_e32 v90, v90
	v_exp_f32_e32 v87, v87
	v_exp_f32_e32 v91, v91
	v_exp_f32_e32 v88, v88
	v_exp_f32_e32 v92, v92
	v_exp_f32_e32 v89, v89
	v_exp_f32_e32 v93, v93
	v_add_f32_e32 v86, 1.0, v86
	v_add_f32_e32 v90, 1.0, v90
	v_add_f32_e32 v87, 1.0, v87
	v_add_f32_e32 v91, 1.0, v91
	v_add_f32_e32 v94, 1.0, v88
	v_add_f32_e32 v95, 1.0, v92
	v_add_f32_e32 v96, 1.0, v89
	v_add_f32_e32 v97, 1.0, v93
	v_rcp_f32_e32 v92, v86
	v_rcp_f32_e32 v88, v90
	v_rcp_f32_e32 v93, v87
	v_rcp_f32_e32 v89, v91
	v_rcp_f32_e32 v90, v94
	v_rcp_f32_e32 v86, v95
	v_rcp_f32_e32 v91, v96
	v_rcp_f32_e32 v87, v97
.LBB0_3111:
	s_andn2_saveexec_b64 s[26:27], s[26:27]
	v_pk_mul_f32 v[90:91], v[84:85], s[20:21] op_sel_hi:[1,0]
	v_pk_mul_f32 v[92:93], v[82:83], s[20:21] op_sel_hi:[1,0]
	v_pk_mul_f32 v[86:87], v[80:81], s[20:21] op_sel_hi:[1,0]
	v_pk_mul_f32 v[88:89], v[78:79], s[20:21] op_sel_hi:[1,0]
	s_or_b64 exec, exec, s[26:27]
	v_readlane_b32 s26, v253, 54
	v_readlane_b32 s27, v253, 55
	v_add_u32_e32 v84, s28, v222
	v_cvt_pk_bf16_f32 v80, v92, v93
	v_mov_b64_e32 v[78:79], s[26:27]
	v_mad_i64_i32 v[78:79], s[26:27], v84, s54, v[78:79]
	v_cvt_pk_bf16_f32 v81, v90, v91
	v_cvt_pk_bf16_f32 v82, v88, v89
	v_cvt_pk_bf16_f32 v83, v86, v87
	v_lshl_add_u64 v[78:79], v[4:5], 1, v[78:79]
	global_store_dwordx4 v[78:79], v[80:83], off
	s_and_saveexec_b64 s[26:27], s[6:7]
	s_xor_b64 s[26:27], exec, s[26:27]
	s_cbranch_execz .LBB0_3116
	s_add_i32 s29, s23, 0xfffff7e0
	s_cmpk_gt_u32 s29, 0x7ff
	v_mov_b32_e32 v81, v73
	v_mov_b32_e32 v80, v72
	v_mov_b32_e32 v83, v71
	v_mov_b32_e32 v82, v70
	v_mov_b32_e32 v85, v77
	v_mov_b32_e32 v84, v76
	v_mov_b32_e32 v87, v75
	v_mov_b32_e32 v86, v74
	s_cbranch_scc1 .LBB0_3116
	v_lshl_add_u64 v[80:81], v[2:3], 2, s[12:13]
	v_lshl_add_u64 v[84:85], v[80:81], 0, s[18:19]
	v_add_co_u32_e32 v80, vcc, 0xffffe000, v80
	s_nop 1
	v_addc_co_u32_e32 v81, vcc, -1, v81, vcc
	v_mov_b64_e32 v[80:81], v[158:159]
	v_mov_b64_e32 v[82:83], v[160:161]
	s_nop 0
	v_mov_b64_e32 v[84:85], v[162:163]
	v_mov_b64_e32 v[86:87], v[164:165]
	v_add_f32_e32 v80, v74, v80
	v_add_f32_e32 v84, v70, v84
	v_add_f32_e32 v81, v75, v81
	v_add_f32_e32 v85, v71, v85
	v_add_f32_e32 v82, v76, v82
	v_add_f32_e32 v86, v72, v86
	v_add_f32_e32 v83, v77, v83
	v_add_f32_e32 v87, v73, v87
	v_mul_f32_e32 v80, 0xbfb8aa3b, v80
	v_mul_f32_e32 v84, 0xbfb8aa3b, v84
	v_mul_f32_e32 v81, 0xbfb8aa3b, v81
	v_mul_f32_e32 v85, 0xbfb8aa3b, v85
	v_mul_f32_e32 v82, 0xbfb8aa3b, v82
	v_mul_f32_e32 v86, 0xbfb8aa3b, v86
	v_mul_f32_e32 v83, 0xbfb8aa3b, v83
	v_mul_f32_e32 v87, 0xbfb8aa3b, v87
	v_exp_f32_e32 v80, v80
	v_exp_f32_e32 v84, v84
	v_exp_f32_e32 v81, v81
	v_exp_f32_e32 v85, v85
	v_exp_f32_e32 v82, v82
	v_exp_f32_e32 v86, v86
	v_exp_f32_e32 v83, v83
	v_exp_f32_e32 v87, v87
	v_add_f32_e32 v80, 1.0, v80
	v_add_f32_e32 v84, 1.0, v84
	v_add_f32_e32 v81, 1.0, v81
	v_add_f32_e32 v85, 1.0, v85
	v_add_f32_e32 v88, 1.0, v82
	v_add_f32_e32 v89, 1.0, v86
	v_add_f32_e32 v90, 1.0, v83
	v_add_f32_e32 v91, 1.0, v87
	v_rcp_f32_e32 v86, v80
	v_rcp_f32_e32 v82, v84
	v_rcp_f32_e32 v87, v81
	v_rcp_f32_e32 v83, v85
	v_rcp_f32_e32 v84, v88
	v_rcp_f32_e32 v80, v89
	v_rcp_f32_e32 v85, v90
	v_rcp_f32_e32 v81, v91
; __device__ __forceinline__ float sigmoidf_(float x) { return __builtin_amdgcn_rcpf(1.f + __expf(-x)); }
; __device__ __forceinline__ u32x4 pack8(f32x4 v0, f32x4 v1) { u32x4 w; w.x = cvt_pk_bf16(v0[0], v0[1]); w.y = cvt_pk_bf16(v0[2], v0[3]); w.z = cvt_pk_bf16(v1[0], v1[1]); w.w = cvt_pk_bf16(v1[2], v1[3]); return w; }
;     __device__ __forceinline__ void operator()(const f32x4 (&acc)[2][2][4][2], const pg8::Unit& u, int wr, int wc, int fr, int fq) const {
;     ...
;             const int row = u.pm * 256 + trow, col = u.pn * 256 + tcol;
;             if (col < C_KA) { v0 = v0 * QS_A; v1 = v1 * QS_A; }
;             else if (col >= C_GA && col < INC) { const f32x4 b0 = *(const f32x4*)(bg + col - C_GA), b1 = *(const f32x4*)(bg + col - C_GA + 4);
; #pragma unroll
;                 for (int i = 0; i < 4; ++i) { v0[i] = sigmoidf_(v0[i] + b0[i]); v1[i] = sigmoidf_(v1[i] + b1[i]); } }
;             *(u32x4*)(O + (size_t)row * INCP + col) = pg8::pack8(v0, v1);
.LBB0_3116:
	s_andn2_saveexec_b64 s[26:27], s[26:27]
	v_pk_mul_f32 v[84:85], v[76:77], s[20:21] op_sel_hi:[1,0]
	v_pk_mul_f32 v[86:87], v[74:75], s[20:21] op_sel_hi:[1,0]
	v_pk_mul_f32 v[80:81], v[72:73], s[20:21] op_sel_hi:[1,0]
	v_pk_mul_f32 v[82:83], v[70:71], s[20:21] op_sel_hi:[1,0]
	s_or_b64 exec, exec, s[26:27]
	v_cvt_pk_bf16_f32 v70, v86, v87
	v_cvt_pk_bf16_f32 v71, v84, v85
	v_cvt_pk_bf16_f32 v72, v82, v83
	v_cvt_pk_bf16_f32 v73, v80, v81
	global_store_dwordx4 v[78:79], v[70:73], off offset:256
	s_and_saveexec_b64 s[26:27], s[4:5]
	s_xor_b64 s[26:27], exec, s[26:27]
	s_cbranch_execz .LBB0_3121
	s_add_i32 s29, s23, 0xfffff760
	v_mov_b64_e32 v[76:77], v[64:65]
	v_mov_b64_e32 v[72:73], v[68:69]
	s_cmpk_gt_u32 s29, 0x7ff
	v_mov_b64_e32 v[74:75], v[62:63]
	v_mov_b64_e32 v[70:71], v[66:67]
	s_cbranch_scc1 .LBB0_3121
	v_mov_b32_e32 v70, v4
	v_mov_b32_e32 v71, v3
	v_lshl_add_u64 v[70:71], v[70:71], 2, s[12:13]
	v_lshl_add_u64 v[74:75], v[70:71], 0, s[18:19]
	v_add_co_u32_e32 v70, vcc, 0xffffe000, v70
	s_nop 1
	v_addc_co_u32_e32 v71, vcc, -1, v71, vcc
	v_mov_b64_e32 v[70:71], v[150:151]
	v_mov_b64_e32 v[72:73], v[152:153]
	s_nop 0
	v_mov_b64_e32 v[74:75], v[154:155]
	v_mov_b64_e32 v[76:77], v[156:157]
	v_add_f32_e32 v70, v66, v70
	v_add_f32_e32 v74, v62, v74
	v_add_f32_e32 v71, v67, v71
	v_add_f32_e32 v75, v63, v75
	v_add_f32_e32 v72, v68, v72
	v_add_f32_e32 v76, v64, v76
	v_add_f32_e32 v73, v69, v73
	v_add_f32_e32 v77, v65, v77
	v_mul_f32_e32 v70, 0xbfb8aa3b, v70
	v_mul_f32_e32 v74, 0xbfb8aa3b, v74
	v_mul_f32_e32 v71, 0xbfb8aa3b, v71
	v_mul_f32_e32 v75, 0xbfb8aa3b, v75
	v_mul_f32_e32 v72, 0xbfb8aa3b, v72
	v_mul_f32_e32 v76, 0xbfb8aa3b, v76
	v_mul_f32_e32 v73, 0xbfb8aa3b, v73
	v_mul_f32_e32 v77, 0xbfb8aa3b, v77
	v_exp_f32_e32 v70, v70
	v_exp_f32_e32 v74, v74
	v_exp_f32_e32 v71, v71
	v_exp_f32_e32 v75, v75
	v_exp_f32_e32 v72, v72
	v_exp_f32_e32 v76, v76
	v_exp_f32_e32 v73, v73
	v_exp_f32_e32 v77, v77
	v_add_f32_e32 v70, 1.0, v70
	v_add_f32_e32 v74, 1.0, v74
	v_add_f32_e32 v71, 1.0, v71
	v_add_f32_e32 v75, 1.0, v75
	v_add_f32_e32 v72, 1.0, v72
	v_add_f32_e32 v76, 1.0, v76
	v_add_f32_e32 v73, 1.0, v73
	v_add_f32_e32 v77, 1.0, v77
	v_rcp_f32_e32 v70, v70
	v_rcp_f32_e32 v74, v74
	v_rcp_f32_e32 v71, v71
	v_rcp_f32_e32 v75, v75
	v_rcp_f32_e32 v72, v72
	v_rcp_f32_e32 v76, v76
	v_rcp_f32_e32 v73, v73
	v_rcp_f32_e32 v77, v77
.LBB0_3121:
	s_andn2_saveexec_b64 s[26:27], s[26:27]
	v_pk_mul_f32 v[72:73], v[68:69], s[20:21] op_sel_hi:[1,0]
	v_pk_mul_f32 v[70:71], v[66:67], s[20:21] op_sel_hi:[1,0]
	v_pk_mul_f32 v[76:77], v[64:65], s[20:21] op_sel_hi:[1,0]
	v_pk_mul_f32 v[74:75], v[62:63], s[20:21] op_sel_hi:[1,0]
	s_or_b64 exec, exec, s[26:27]
	v_readlane_b32 s26, v253, 54
	v_readlane_b32 s27, v253, 55
	v_add_u32_e32 v68, s28, v223
	v_cvt_pk_bf16_f32 v62, v70, v71
	v_mov_b64_e32 v[66:67], s[26:27]
	v_mad_i64_i32 v[66:67], s[26:27], v68, s54, v[66:67]
	v_cvt_pk_bf16_f32 v63, v72, v73
	v_cvt_pk_bf16_f32 v64, v74, v75
	v_cvt_pk_bf16_f32 v65, v76, v77
	v_lshl_add_u64 v[70:71], v[4:5], 1, v[66:67]
	global_store_dwordx4 v[70:71], v[62:65], off
	s_and_saveexec_b64 s[26:27], s[6:7]
	s_xor_b64 s[26:27], exec, s[26:27]
	s_cbranch_execz .LBB0_3126
	s_add_i32 s29, s23, 0xfffff7e0
	v_mov_b64_e32 v[68:69], v[56:57]
	v_mov_b64_e32 v[64:65], v[60:61]
	s_cmpk_gt_u32 s29, 0x7ff
	v_mov_b64_e32 v[66:67], v[54:55]
	v_mov_b64_e32 v[62:63], v[58:59]
	s_cbranch_scc1 .LBB0_3126
	v_lshl_add_u64 v[62:63], v[2:3], 2, s[12:13]
	v_lshl_add_u64 v[66:67], v[62:63], 0, s[18:19]
	v_add_co_u32_e32 v62, vcc, 0xffffe000, v62
	s_nop 1
	v_addc_co_u32_e32 v63, vcc, -1, v63, vcc
	v_mov_b64_e32 v[62:63], v[158:159]
	v_mov_b64_e32 v[64:65], v[160:161]
	s_nop 0
	v_mov_b64_e32 v[66:67], v[162:163]
	v_mov_b64_e32 v[68:69], v[164:165]
	v_add_f32_e32 v62, v58, v62
	v_add_f32_e32 v66, v54, v66
	v_add_f32_e32 v63, v59, v63
	v_add_f32_e32 v67, v55, v67
	v_add_f32_e32 v64, v60, v64
	v_add_f32_e32 v68, v56, v68
	v_add_f32_e32 v65, v61, v65
	v_add_f32_e32 v69, v57, v69
	v_mul_f32_e32 v62, 0xbfb8aa3b, v62
	v_mul_f32_e32 v66, 0xbfb8aa3b, v66
	v_mul_f32_e32 v63, 0xbfb8aa3b, v63
	v_mul_f32_e32 v67, 0xbfb8aa3b, v67
	v_mul_f32_e32 v64, 0xbfb8aa3b, v64
	v_mul_f32_e32 v68, 0xbfb8aa3b, v68
	v_mul_f32_e32 v65, 0xbfb8aa3b, v65
	v_mul_f32_e32 v69, 0xbfb8aa3b, v69
	v_exp_f32_e32 v62, v62
	v_exp_f32_e32 v66, v66
	v_exp_f32_e32 v63, v63
	v_exp_f32_e32 v67, v67
	v_exp_f32_e32 v64, v64
	v_exp_f32_e32 v68, v68
	v_exp_f32_e32 v65, v65
	v_exp_f32_e32 v69, v69
	v_add_f32_e32 v62, 1.0, v62
	v_add_f32_e32 v66, 1.0, v66
	v_add_f32_e32 v63, 1.0, v63
	v_add_f32_e32 v67, 1.0, v67
	v_add_f32_e32 v64, 1.0, v64
	v_add_f32_e32 v68, 1.0, v68
	v_add_f32_e32 v65, 1.0, v65
	v_add_f32_e32 v69, 1.0, v69
	v_rcp_f32_e32 v62, v62
	v_rcp_f32_e32 v66, v66
	v_rcp_f32_e32 v63, v63
	v_rcp_f32_e32 v67, v67
	v_rcp_f32_e32 v64, v64
	v_rcp_f32_e32 v68, v68
	v_rcp_f32_e32 v65, v65
	v_rcp_f32_e32 v69, v69
; __device__ __forceinline__ float sigmoidf_(float x) { return __builtin_amdgcn_rcpf(1.f + __expf(-x)); }
; __device__ __forceinline__ u32x4 pack8(f32x4 v0, f32x4 v1) { u32x4 w; w.x = cvt_pk_bf16(v0[0], v0[1]); w.y = cvt_pk_bf16(v0[2], v0[3]); w.z = cvt_pk_bf16(v1[0], v1[1]); w.w = cvt_pk_bf16(v1[2], v1[3]); return w; }
;     __device__ __forceinline__ void operator()(const f32x4 (&acc)[2][2][4][2], const pg8::Unit& u, int wr, int wc, int fr, int fq) const {
;     ...
;             const int row = u.pm * 256 + trow, col = u.pn * 256 + tcol;
;             if (col < C_KA) { v0 = v0 * QS_A; v1 = v1 * QS_A; }
;             else if (col >= C_GA && col < INC) { const f32x4 b0 = *(const f32x4*)(bg + col - C_GA), b1 = *(const f32x4*)(bg + col - C_GA + 4);
; #pragma unroll
;                 for (int i = 0; i < 4; ++i) { v0[i] = sigmoidf_(v0[i] + b0[i]); v1[i] = sigmoidf_(v1[i] + b1[i]); } }
;             *(u32x4*)(O + (size_t)row * INCP + col) = pg8::pack8(v0, v1);
.LBB0_3126:
	s_andn2_saveexec_b64 s[26:27], s[26:27]
	v_pk_mul_f32 v[64:65], v[60:61], s[20:21] op_sel_hi:[1,0]
	v_pk_mul_f32 v[62:63], v[58:59], s[20:21] op_sel_hi:[1,0]
	v_pk_mul_f32 v[68:69], v[56:57], s[20:21] op_sel_hi:[1,0]
	v_pk_mul_f32 v[66:67], v[54:55], s[20:21] op_sel_hi:[1,0]
	s_or_b64 exec, exec, s[26:27]
	v_cvt_pk_bf16_f32 v54, v62, v63
	v_cvt_pk_bf16_f32 v55, v64, v65
	v_cvt_pk_bf16_f32 v56, v66, v67
	v_cvt_pk_bf16_f32 v57, v68, v69
	global_store_dwordx4 v[70:71], v[54:57], off offset:256
	s_and_saveexec_b64 s[26:27], s[4:5]
	s_xor_b64 s[26:27], exec, s[26:27]
	s_cbranch_execz .LBB0_3131
	s_add_i32 s29, s23, 0xfffff760
	v_mov_b64_e32 v[60:61], v[48:49]
	v_mov_b64_e32 v[56:57], v[52:53]
	s_cmpk_gt_u32 s29, 0x7ff
	v_mov_b64_e32 v[58:59], v[46:47]
	v_mov_b64_e32 v[54:55], v[50:51]
	s_cbranch_scc1 .LBB0_3131
	v_mov_b32_e32 v54, v4
	v_mov_b32_e32 v55, v3
	v_lshl_add_u64 v[54:55], v[54:55], 2, s[12:13]
	v_lshl_add_u64 v[58:59], v[54:55], 0, s[18:19]
	v_add_co_u32_e32 v54, vcc, 0xffffe000, v54
	s_nop 1
	v_addc_co_u32_e32 v55, vcc, -1, v55, vcc
	v_mov_b64_e32 v[54:55], v[150:151]
	v_mov_b64_e32 v[56:57], v[152:153]
	s_nop 0
	v_mov_b64_e32 v[58:59], v[154:155]
	v_mov_b64_e32 v[60:61], v[156:157]
	v_add_f32_e32 v54, v50, v54
	v_add_f32_e32 v58, v46, v58
	v_add_f32_e32 v55, v51, v55
	v_add_f32_e32 v59, v47, v59
	v_add_f32_e32 v56, v52, v56
	v_add_f32_e32 v60, v48, v60
	v_add_f32_e32 v57, v53, v57
	v_add_f32_e32 v61, v49, v61
	v_mul_f32_e32 v54, 0xbfb8aa3b, v54
	v_mul_f32_e32 v58, 0xbfb8aa3b, v58
	v_mul_f32_e32 v55, 0xbfb8aa3b, v55
	v_mul_f32_e32 v59, 0xbfb8aa3b, v59
	v_mul_f32_e32 v56, 0xbfb8aa3b, v56
	v_mul_f32_e32 v60, 0xbfb8aa3b, v60
	v_mul_f32_e32 v57, 0xbfb8aa3b, v57
	v_mul_f32_e32 v61, 0xbfb8aa3b, v61
	v_exp_f32_e32 v54, v54
	v_exp_f32_e32 v58, v58
	v_exp_f32_e32 v55, v55
	v_exp_f32_e32 v59, v59
	v_exp_f32_e32 v56, v56
	v_exp_f32_e32 v60, v60
	v_exp_f32_e32 v57, v57
	v_exp_f32_e32 v61, v61
	v_add_f32_e32 v54, 1.0, v54
	v_add_f32_e32 v58, 1.0, v58
	v_add_f32_e32 v55, 1.0, v55
	v_add_f32_e32 v59, 1.0, v59
	v_add_f32_e32 v56, 1.0, v56
	v_add_f32_e32 v60, 1.0, v60
	v_add_f32_e32 v57, 1.0, v57
	v_add_f32_e32 v61, 1.0, v61
	v_rcp_f32_e32 v54, v54
	v_rcp_f32_e32 v58, v58
	v_rcp_f32_e32 v55, v55
	v_rcp_f32_e32 v59, v59
	v_rcp_f32_e32 v56, v56
	v_rcp_f32_e32 v60, v60
	v_rcp_f32_e32 v57, v57
	v_rcp_f32_e32 v61, v61
.LBB0_3131:
	s_andn2_saveexec_b64 s[26:27], s[26:27]
	v_pk_mul_f32 v[56:57], v[52:53], s[20:21] op_sel_hi:[1,0]
	v_pk_mul_f32 v[54:55], v[50:51], s[20:21] op_sel_hi:[1,0]
	v_pk_mul_f32 v[60:61], v[48:49], s[20:21] op_sel_hi:[1,0]
	v_pk_mul_f32 v[58:59], v[46:47], s[20:21] op_sel_hi:[1,0]
	s_or_b64 exec, exec, s[26:27]
	v_readlane_b32 s26, v253, 54
	v_readlane_b32 s27, v253, 55
	v_add_u32_e32 v52, s28, v224
	v_cvt_pk_bf16_f32 v46, v54, v55
	v_mov_b64_e32 v[50:51], s[26:27]
	v_mad_i64_i32 v[50:51], s[26:27], v52, s54, v[50:51]
	v_cvt_pk_bf16_f32 v47, v56, v57
	v_cvt_pk_bf16_f32 v48, v58, v59
	v_cvt_pk_bf16_f32 v49, v60, v61
	v_lshl_add_u64 v[54:55], v[4:5], 1, v[50:51]
	global_store_dwordx4 v[54:55], v[46:49], off
	s_and_saveexec_b64 s[26:27], s[6:7]
	s_xor_b64 s[26:27], exec, s[26:27]
	s_cbranch_execz .LBB0_3136
	s_add_i32 s29, s23, 0xfffff7e0
	v_mov_b64_e32 v[52:53], v[40:41]
	v_mov_b64_e32 v[48:49], v[44:45]
	s_cmpk_gt_u32 s29, 0x7ff
	v_mov_b64_e32 v[50:51], v[38:39]
	v_mov_b64_e32 v[46:47], v[42:43]
	s_cbranch_scc1 .LBB0_3136
	v_lshl_add_u64 v[46:47], v[2:3], 2, s[12:13]
	v_lshl_add_u64 v[50:51], v[46:47], 0, s[18:19]
	v_add_co_u32_e32 v46, vcc, 0xffffe000, v46
	s_nop 1
	v_addc_co_u32_e32 v47, vcc, -1, v47, vcc
	v_mov_b64_e32 v[46:47], v[158:159]
	v_mov_b64_e32 v[48:49], v[160:161]
	s_nop 0
	v_mov_b64_e32 v[50:51], v[162:163]
	v_mov_b64_e32 v[52:53], v[164:165]
	v_add_f32_e32 v46, v42, v46
	v_add_f32_e32 v50, v38, v50
	v_add_f32_e32 v47, v43, v47
	v_add_f32_e32 v51, v39, v51
	v_add_f32_e32 v48, v44, v48
	v_add_f32_e32 v52, v40, v52
	v_add_f32_e32 v49, v45, v49
	v_add_f32_e32 v53, v41, v53
	v_mul_f32_e32 v46, 0xbfb8aa3b, v46
	v_mul_f32_e32 v50, 0xbfb8aa3b, v50
	v_mul_f32_e32 v47, 0xbfb8aa3b, v47
	v_mul_f32_e32 v51, 0xbfb8aa3b, v51
	v_mul_f32_e32 v48, 0xbfb8aa3b, v48
	v_mul_f32_e32 v52, 0xbfb8aa3b, v52
	v_mul_f32_e32 v49, 0xbfb8aa3b, v49
	v_mul_f32_e32 v53, 0xbfb8aa3b, v53
	v_exp_f32_e32 v46, v46
	v_exp_f32_e32 v50, v50
	v_exp_f32_e32 v47, v47
	v_exp_f32_e32 v51, v51
	v_exp_f32_e32 v48, v48
	v_exp_f32_e32 v52, v52
	v_exp_f32_e32 v49, v49
	v_exp_f32_e32 v53, v53
	v_add_f32_e32 v46, 1.0, v46
	v_add_f32_e32 v50, 1.0, v50
	v_add_f32_e32 v47, 1.0, v47
	v_add_f32_e32 v51, 1.0, v51
	v_add_f32_e32 v48, 1.0, v48
	v_add_f32_e32 v52, 1.0, v52
	v_add_f32_e32 v49, 1.0, v49
	v_add_f32_e32 v53, 1.0, v53
	v_rcp_f32_e32 v46, v46
	v_rcp_f32_e32 v50, v50
	v_rcp_f32_e32 v47, v47
	v_rcp_f32_e32 v51, v51
	v_rcp_f32_e32 v48, v48
	v_rcp_f32_e32 v52, v52
	v_rcp_f32_e32 v49, v49
	v_rcp_f32_e32 v53, v53
; __device__ __forceinline__ float sigmoidf_(float x) { return __builtin_amdgcn_rcpf(1.f + __expf(-x)); }
; __device__ __forceinline__ u32x4 pack8(f32x4 v0, f32x4 v1) { u32x4 w; w.x = cvt_pk_bf16(v0[0], v0[1]); w.y = cvt_pk_bf16(v0[2], v0[3]); w.z = cvt_pk_bf16(v1[0], v1[1]); w.w = cvt_pk_bf16(v1[2], v1[3]); return w; }
;     __device__ __forceinline__ void operator()(const f32x4 (&acc)[2][2][4][2], const pg8::Unit& u, int wr, int wc, int fr, int fq) const {
;     ...
;             const int row = u.pm * 256 + trow, col = u.pn * 256 + tcol;
;             if (col < C_KA) { v0 = v0 * QS_A; v1 = v1 * QS_A; }
;             else if (col >= C_GA && col < INC) { const f32x4 b0 = *(const f32x4*)(bg + col - C_GA), b1 = *(const f32x4*)(bg + col - C_GA + 4);
; #pragma unroll
;                 for (int i = 0; i < 4; ++i) { v0[i] = sigmoidf_(v0[i] + b0[i]); v1[i] = sigmoidf_(v1[i] + b1[i]); } }
;             *(u32x4*)(O + (size_t)row * INCP + col) = pg8::pack8(v0, v1);
.LBB0_3136:
	s_andn2_saveexec_b64 s[26:27], s[26:27]
	v_pk_mul_f32 v[48:49], v[44:45], s[20:21] op_sel_hi:[1,0]
	v_pk_mul_f32 v[46:47], v[42:43], s[20:21] op_sel_hi:[1,0]
	v_pk_mul_f32 v[52:53], v[40:41], s[20:21] op_sel_hi:[1,0]
	v_pk_mul_f32 v[50:51], v[38:39], s[20:21] op_sel_hi:[1,0]
	s_or_b64 exec, exec, s[26:27]
	v_cvt_pk_bf16_f32 v38, v46, v47
	v_cvt_pk_bf16_f32 v39, v48, v49
	v_cvt_pk_bf16_f32 v40, v50, v51
	v_cvt_pk_bf16_f32 v41, v52, v53
	global_store_dwordx4 v[54:55], v[38:41], off offset:256
	s_and_saveexec_b64 s[26:27], s[4:5]
	s_xor_b64 s[26:27], exec, s[26:27]
	s_cbranch_execz .LBB0_3141
	s_add_i32 s29, s23, 0xfffff760
	v_mov_b64_e32 v[44:45], v[32:33]
	v_mov_b64_e32 v[40:41], v[36:37]
	s_cmpk_gt_u32 s29, 0x7ff
	v_mov_b64_e32 v[42:43], v[30:31]
	v_mov_b64_e32 v[38:39], v[34:35]
	s_cbranch_scc1 .LBB0_3141
	v_mov_b32_e32 v38, v4
	v_mov_b32_e32 v39, v3
	v_lshl_add_u64 v[38:39], v[38:39], 2, s[12:13]
	v_lshl_add_u64 v[42:43], v[38:39], 0, s[18:19]
	v_add_co_u32_e32 v38, vcc, 0xffffe000, v38
	s_nop 1
	v_addc_co_u32_e32 v39, vcc, -1, v39, vcc
	v_mov_b64_e32 v[38:39], v[150:151]
	v_mov_b64_e32 v[40:41], v[152:153]
	s_nop 0
	v_mov_b64_e32 v[42:43], v[154:155]
	v_mov_b64_e32 v[44:45], v[156:157]
	v_add_f32_e32 v38, v34, v38
	v_add_f32_e32 v42, v30, v42
	v_add_f32_e32 v39, v35, v39
	v_add_f32_e32 v43, v31, v43
	v_add_f32_e32 v40, v36, v40
	v_add_f32_e32 v44, v32, v44
	v_add_f32_e32 v41, v37, v41
	v_add_f32_e32 v45, v33, v45
	v_mul_f32_e32 v38, 0xbfb8aa3b, v38
	v_mul_f32_e32 v42, 0xbfb8aa3b, v42
	v_mul_f32_e32 v39, 0xbfb8aa3b, v39
	v_mul_f32_e32 v43, 0xbfb8aa3b, v43
	v_mul_f32_e32 v40, 0xbfb8aa3b, v40
	v_mul_f32_e32 v44, 0xbfb8aa3b, v44
	v_mul_f32_e32 v41, 0xbfb8aa3b, v41
	v_mul_f32_e32 v45, 0xbfb8aa3b, v45
	v_exp_f32_e32 v38, v38
	v_exp_f32_e32 v42, v42
	v_exp_f32_e32 v39, v39
	v_exp_f32_e32 v43, v43
	v_exp_f32_e32 v40, v40
	v_exp_f32_e32 v44, v44
	v_exp_f32_e32 v41, v41
	v_exp_f32_e32 v45, v45
	v_add_f32_e32 v38, 1.0, v38
	v_add_f32_e32 v42, 1.0, v42
	v_add_f32_e32 v39, 1.0, v39
	v_add_f32_e32 v43, 1.0, v43
	v_add_f32_e32 v40, 1.0, v40
	v_add_f32_e32 v44, 1.0, v44
	v_add_f32_e32 v41, 1.0, v41
	v_add_f32_e32 v45, 1.0, v45
	v_rcp_f32_e32 v38, v38
	v_rcp_f32_e32 v42, v42
	v_rcp_f32_e32 v39, v39
	v_rcp_f32_e32 v43, v43
	v_rcp_f32_e32 v40, v40
	v_rcp_f32_e32 v44, v44
	v_rcp_f32_e32 v41, v41
	v_rcp_f32_e32 v45, v45
.LBB0_3141:
	s_andn2_saveexec_b64 s[26:27], s[26:27]
	v_pk_mul_f32 v[40:41], v[36:37], s[20:21] op_sel_hi:[1,0]
	v_pk_mul_f32 v[38:39], v[34:35], s[20:21] op_sel_hi:[1,0]
	v_pk_mul_f32 v[44:45], v[32:33], s[20:21] op_sel_hi:[1,0]
	v_pk_mul_f32 v[42:43], v[30:31], s[20:21] op_sel_hi:[1,0]
	s_or_b64 exec, exec, s[26:27]
	v_readlane_b32 s26, v253, 54
	v_readlane_b32 s27, v253, 55
	v_add_u32_e32 v36, s28, v225
	v_cvt_pk_bf16_f32 v30, v38, v39
	v_mov_b64_e32 v[34:35], s[26:27]
	v_mad_i64_i32 v[34:35], s[26:27], v36, s54, v[34:35]
	v_cvt_pk_bf16_f32 v31, v40, v41
	v_cvt_pk_bf16_f32 v32, v42, v43
	v_cvt_pk_bf16_f32 v33, v44, v45
	v_lshl_add_u64 v[38:39], v[4:5], 1, v[34:35]
	global_store_dwordx4 v[38:39], v[30:33], off
	s_and_saveexec_b64 s[26:27], s[6:7]
	s_xor_b64 s[26:27], exec, s[26:27]
	s_cbranch_execz .LBB0_3146
	s_add_i32 s29, s23, 0xfffff7e0
	v_mov_b64_e32 v[36:37], v[24:25]
	v_mov_b64_e32 v[32:33], v[28:29]
	s_cmpk_gt_u32 s29, 0x7ff
	v_mov_b64_e32 v[34:35], v[22:23]
	v_mov_b64_e32 v[30:31], v[26:27]
	s_cbranch_scc1 .LBB0_3146
	v_lshl_add_u64 v[30:31], v[2:3], 2, s[12:13]
	v_lshl_add_u64 v[34:35], v[30:31], 0, s[18:19]
	v_add_co_u32_e32 v30, vcc, 0xffffe000, v30
	s_nop 1
	v_addc_co_u32_e32 v31, vcc, -1, v31, vcc
	v_mov_b64_e32 v[30:31], v[158:159]
	v_mov_b64_e32 v[32:33], v[160:161]
	s_nop 0
	v_mov_b64_e32 v[34:35], v[162:163]
	v_mov_b64_e32 v[36:37], v[164:165]
	v_add_f32_e32 v30, v26, v30
	v_add_f32_e32 v34, v22, v34
	v_add_f32_e32 v31, v27, v31
	v_add_f32_e32 v35, v23, v35
	v_add_f32_e32 v32, v28, v32
	v_add_f32_e32 v36, v24, v36
	v_add_f32_e32 v33, v29, v33
	v_add_f32_e32 v37, v25, v37
	v_mul_f32_e32 v30, 0xbfb8aa3b, v30
	v_mul_f32_e32 v34, 0xbfb8aa3b, v34
	v_mul_f32_e32 v31, 0xbfb8aa3b, v31
	v_mul_f32_e32 v35, 0xbfb8aa3b, v35
	v_mul_f32_e32 v32, 0xbfb8aa3b, v32
	v_mul_f32_e32 v36, 0xbfb8aa3b, v36
	v_mul_f32_e32 v33, 0xbfb8aa3b, v33
	v_mul_f32_e32 v37, 0xbfb8aa3b, v37
	v_exp_f32_e32 v30, v30
	v_exp_f32_e32 v34, v34
	v_exp_f32_e32 v31, v31
	v_exp_f32_e32 v35, v35
	v_exp_f32_e32 v32, v32
	v_exp_f32_e32 v36, v36
	v_exp_f32_e32 v33, v33
	v_exp_f32_e32 v37, v37
	v_add_f32_e32 v30, 1.0, v30
	v_add_f32_e32 v34, 1.0, v34
	v_add_f32_e32 v31, 1.0, v31
	v_add_f32_e32 v35, 1.0, v35
	v_add_f32_e32 v32, 1.0, v32
	v_add_f32_e32 v36, 1.0, v36
	v_add_f32_e32 v33, 1.0, v33
	v_add_f32_e32 v37, 1.0, v37
	v_rcp_f32_e32 v30, v30
	v_rcp_f32_e32 v34, v34
	v_rcp_f32_e32 v31, v31
	v_rcp_f32_e32 v35, v35
	v_rcp_f32_e32 v32, v32
	v_rcp_f32_e32 v36, v36
	v_rcp_f32_e32 v33, v33
	v_rcp_f32_e32 v37, v37
; __device__ __forceinline__ float sigmoidf_(float x) { return __builtin_amdgcn_rcpf(1.f + __expf(-x)); }
; __device__ __forceinline__ u32x4 pack8(f32x4 v0, f32x4 v1) { u32x4 w; w.x = cvt_pk_bf16(v0[0], v0[1]); w.y = cvt_pk_bf16(v0[2], v0[3]); w.z = cvt_pk_bf16(v1[0], v1[1]); w.w = cvt_pk_bf16(v1[2], v1[3]); return w; }
;     __device__ __forceinline__ void operator()(const f32x4 (&acc)[2][2][4][2], const pg8::Unit& u, int wr, int wc, int fr, int fq) const {
;     ...
;             const int row = u.pm * 256 + trow, col = u.pn * 256 + tcol;
;             if (col < C_KA) { v0 = v0 * QS_A; v1 = v1 * QS_A; }
;             else if (col >= C_GA && col < INC) { const f32x4 b0 = *(const f32x4*)(bg + col - C_GA), b1 = *(const f32x4*)(bg + col - C_GA + 4);
; #pragma unroll
;                 for (int i = 0; i < 4; ++i) { v0[i] = sigmoidf_(v0[i] + b0[i]); v1[i] = sigmoidf_(v1[i] + b1[i]); } }
;             *(u32x4*)(O + (size_t)row * INCP + col) = pg8::pack8(v0, v1);
.LBB0_3146:
	s_andn2_saveexec_b64 s[26:27], s[26:27]
	v_pk_mul_f32 v[32:33], v[28:29], s[20:21] op_sel_hi:[1,0]
	v_pk_mul_f32 v[30:31], v[26:27], s[20:21] op_sel_hi:[1,0]
	v_pk_mul_f32 v[36:37], v[24:25], s[20:21] op_sel_hi:[1,0]
	v_pk_mul_f32 v[34:35], v[22:23], s[20:21] op_sel_hi:[1,0]
	s_or_b64 exec, exec, s[26:27]
	v_cvt_pk_bf16_f32 v22, v30, v31
	v_cvt_pk_bf16_f32 v23, v32, v33
	v_cvt_pk_bf16_f32 v24, v34, v35
	v_cvt_pk_bf16_f32 v25, v36, v37
	global_store_dwordx4 v[38:39], v[22:25], off offset:256
	s_and_saveexec_b64 s[26:27], s[4:5]
	s_xor_b64 s[4:5], exec, s[26:27]
	s_cbranch_execz .LBB0_3151
	s_add_i32 s26, s23, 0xfffff760
	v_mov_b64_e32 v[28:29], v[16:17]
	v_mov_b64_e32 v[24:25], v[20:21]
	s_cmpk_gt_u32 s26, 0x7ff
	v_mov_b64_e32 v[26:27], v[14:15]
	v_mov_b64_e32 v[22:23], v[18:19]
	s_cbranch_scc1 .LBB0_3151
	v_mov_b32_e32 v22, v4
	v_mov_b32_e32 v23, v3
	v_lshl_add_u64 v[22:23], v[22:23], 2, s[12:13]
	v_lshl_add_u64 v[26:27], v[22:23], 0, s[18:19]
	v_add_co_u32_e32 v22, vcc, 0xffffe000, v22
	s_nop 1
	v_addc_co_u32_e32 v23, vcc, -1, v23, vcc
	v_mov_b64_e32 v[22:23], v[150:151]
	v_mov_b64_e32 v[24:25], v[152:153]
	s_nop 0
	v_mov_b64_e32 v[26:27], v[154:155]
	v_mov_b64_e32 v[28:29], v[156:157]
	v_add_f32_e32 v22, v18, v22
	v_add_f32_e32 v26, v14, v26
	v_add_f32_e32 v23, v19, v23
	v_add_f32_e32 v27, v15, v27
	v_add_f32_e32 v24, v20, v24
	v_add_f32_e32 v28, v16, v28
	v_add_f32_e32 v25, v21, v25
	v_add_f32_e32 v29, v17, v29
	v_mul_f32_e32 v22, 0xbfb8aa3b, v22
	v_mul_f32_e32 v26, 0xbfb8aa3b, v26
	v_mul_f32_e32 v23, 0xbfb8aa3b, v23
	v_mul_f32_e32 v27, 0xbfb8aa3b, v27
	v_mul_f32_e32 v24, 0xbfb8aa3b, v24
	v_mul_f32_e32 v28, 0xbfb8aa3b, v28
	v_mul_f32_e32 v25, 0xbfb8aa3b, v25
	v_mul_f32_e32 v29, 0xbfb8aa3b, v29
	v_exp_f32_e32 v22, v22
	v_exp_f32_e32 v26, v26
	v_exp_f32_e32 v23, v23
	v_exp_f32_e32 v27, v27
	v_exp_f32_e32 v24, v24
	v_exp_f32_e32 v28, v28
	v_exp_f32_e32 v25, v25
	v_exp_f32_e32 v29, v29
	v_add_f32_e32 v22, 1.0, v22
	v_add_f32_e32 v26, 1.0, v26
	v_add_f32_e32 v23, 1.0, v23
	v_add_f32_e32 v27, 1.0, v27
	v_add_f32_e32 v24, 1.0, v24
	v_add_f32_e32 v28, 1.0, v28
	v_add_f32_e32 v25, 1.0, v25
	v_add_f32_e32 v29, 1.0, v29
	v_rcp_f32_e32 v22, v22
	v_rcp_f32_e32 v26, v26
	v_rcp_f32_e32 v23, v23
	v_rcp_f32_e32 v27, v27
	v_rcp_f32_e32 v24, v24
	v_rcp_f32_e32 v28, v28
	v_rcp_f32_e32 v25, v25
	v_rcp_f32_e32 v29, v29
.LBB0_3151:
	s_andn2_saveexec_b64 s[4:5], s[4:5]
	v_pk_mul_f32 v[24:25], v[20:21], s[20:21] op_sel_hi:[1,0]
	v_pk_mul_f32 v[22:23], v[18:19], s[20:21] op_sel_hi:[1,0]
	v_pk_mul_f32 v[28:29], v[16:17], s[20:21] op_sel_hi:[1,0]
	v_pk_mul_f32 v[26:27], v[14:15], s[20:21] op_sel_hi:[1,0]
	s_or_b64 exec, exec, s[4:5]
	v_readlane_b32 s4, v253, 54
	v_readlane_b32 s5, v253, 55
	v_add_u32_e32 v20, s28, v226
	v_cvt_pk_bf16_f32 v14, v22, v23
	v_mov_b64_e32 v[18:19], s[4:5]
	v_mad_i64_i32 v[18:19], s[4:5], v20, s54, v[18:19]
	v_cvt_pk_bf16_f32 v15, v24, v25
	v_cvt_pk_bf16_f32 v16, v26, v27
	v_cvt_pk_bf16_f32 v17, v28, v29
	v_lshl_add_u64 v[4:5], v[4:5], 1, v[18:19]
	global_store_dwordx4 v[4:5], v[14:17], off
	s_and_saveexec_b64 s[4:5], s[6:7]
	s_xor_b64 s[4:5], exec, s[4:5]
	s_cbranch_execz .LBB0_3156
	s_addk_i32 s23, 0xf7e0
	v_mov_b64_e32 v[20:21], v[8:9]
	v_mov_b64_e32 v[16:17], v[12:13]
	s_cmpk_gt_u32 s23, 0x7ff
	v_mov_b64_e32 v[18:19], v[6:7]
	v_mov_b64_e32 v[14:15], v[10:11]
	s_cbranch_scc1 .LBB0_3156
	v_lshl_add_u64 v[14:15], v[2:3], 2, s[12:13]
	v_lshl_add_u64 v[18:19], v[14:15], 0, s[18:19]
	v_add_co_u32_e32 v14, vcc, 0xffffe000, v14
	s_nop 1
	v_addc_co_u32_e32 v15, vcc, -1, v15, vcc
	v_mov_b64_e32 v[14:15], v[158:159]
	v_mov_b64_e32 v[16:17], v[160:161]
	s_nop 0
	v_mov_b64_e32 v[18:19], v[162:163]
	v_mov_b64_e32 v[20:21], v[164:165]
	v_add_f32_e32 v2, v10, v14
	v_add_f32_e32 v14, v6, v18
	v_add_f32_e32 v15, v11, v15
	v_add_f32_e32 v18, v7, v19
	v_add_f32_e32 v16, v12, v16
	v_add_f32_e32 v19, v8, v20
	v_add_f32_e32 v17, v13, v17
	v_add_f32_e32 v20, v9, v21
	v_mul_f32_e32 v2, 0xbfb8aa3b, v2
	v_mul_f32_e32 v14, 0xbfb8aa3b, v14
	v_mul_f32_e32 v15, 0xbfb8aa3b, v15
	v_mul_f32_e32 v18, 0xbfb8aa3b, v18
	v_mul_f32_e32 v16, 0xbfb8aa3b, v16
	v_mul_f32_e32 v19, 0xbfb8aa3b, v19
	v_mul_f32_e32 v17, 0xbfb8aa3b, v17
	v_mul_f32_e32 v20, 0xbfb8aa3b, v20
	v_exp_f32_e32 v2, v2
	v_exp_f32_e32 v14, v14
	v_exp_f32_e32 v15, v15
	v_exp_f32_e32 v18, v18
	v_exp_f32_e32 v16, v16
	v_exp_f32_e32 v19, v19
	v_exp_f32_e32 v17, v17
	v_exp_f32_e32 v20, v20
	v_add_f32_e32 v2, 1.0, v2
	v_add_f32_e32 v21, 1.0, v14
	v_add_f32_e32 v15, 1.0, v15
	v_add_f32_e32 v22, 1.0, v18
	v_add_f32_e32 v16, 1.0, v16
	v_add_f32_e32 v23, 1.0, v19
	v_add_f32_e32 v17, 1.0, v17
	v_add_f32_e32 v24, 1.0, v20
	v_rcp_f32_e32 v14, v2
	v_rcp_f32_e32 v18, v21
	v_rcp_f32_e32 v15, v15
	v_rcp_f32_e32 v19, v22
	v_rcp_f32_e32 v16, v16
	v_rcp_f32_e32 v20, v23
	v_rcp_f32_e32 v17, v17
	v_rcp_f32_e32 v21, v24
